# v30 + K-loops: MFMA segments are bare MFMAs (no setprio flips, no redundant lgkmcnt wait), one static s_setprio 1 for waves 4-7 per unit; same placement modulo 64 behind the loops
# baseline (speedup 1.0000x reference)
.LBB0_118:
	s_ashr_i32 s15, s14, 31
	s_lshl_b64 s[16:17], s[14:15], 20
	s_add_u32 s16, s28, s16
	s_addc_u32 s17, s29, s17
	s_and_b64 s[18:19], s[4:5], exec
	s_cselect_b32 s15, s17, s23
	s_cselect_b32 s75, s16, s22
	s_ashr_i32 s13, s12, 31
	s_lshl_b64 s[18:19], s[12:13], 20
	s_add_u32 s18, s30, s18
	s_addc_u32 s19, s31, s19
	s_and_b64 s[26:27], s[4:5], exec
	s_cselect_b32 s13, s19, s25
	s_cselect_b32 s76, s18, s24
	s_add_u32 s22, s22, 0x80080
	s_addc_u32 s23, s23, 0
	s_add_u32 s77, s24, 0x100
	v_mov_b32_e32 v2, 0
	s_addc_u32 s78, s25, 0
	s_mov_b32 s79, -2
	v_mov_b32_e32 v3, v2
	v_mov_b32_e32 v4, v2
	v_mov_b32_e32 v5, v2
	v_mov_b32_e32 v6, v2
	v_mov_b32_e32 v7, v2
	v_mov_b32_e32 v8, v2
	v_mov_b32_e32 v9, v2
	v_mov_b32_e32 v10, v2
	v_mov_b32_e32 v11, v2
	v_mov_b32_e32 v12, v2
	v_mov_b32_e32 v13, v2
	v_mov_b32_e32 v18, v2
	v_mov_b32_e32 v19, v2
	v_mov_b32_e32 v20, v2
	v_mov_b32_e32 v21, v2
	v_mov_b32_e32 v26, v2
	v_mov_b32_e32 v27, v2
	v_mov_b32_e32 v28, v2
	v_mov_b32_e32 v29, v2
	v_mov_b32_e32 v34, v2
	v_mov_b32_e32 v35, v2
	v_mov_b32_e32 v36, v2
	v_mov_b32_e32 v37, v2
	v_mov_b32_e32 v42, v2
	v_mov_b32_e32 v43, v2
	v_mov_b32_e32 v44, v2
	v_mov_b32_e32 v45, v2
	v_mov_b32_e32 v50, v2
	v_mov_b32_e32 v51, v2
	v_mov_b32_e32 v52, v2
	v_mov_b32_e32 v53, v2
	v_mov_b32_e32 v14, v2
	v_mov_b32_e32 v15, v2
	v_mov_b32_e32 v16, v2
	v_mov_b32_e32 v17, v2
	v_mov_b32_e32 v22, v2
	v_mov_b32_e32 v23, v2
	v_mov_b32_e32 v24, v2
	v_mov_b32_e32 v25, v2
	v_mov_b32_e32 v30, v2
	v_mov_b32_e32 v31, v2
	v_mov_b32_e32 v32, v2
	v_mov_b32_e32 v33, v2
	v_mov_b32_e32 v38, v2
	v_mov_b32_e32 v39, v2
	v_mov_b32_e32 v40, v2
	v_mov_b32_e32 v41, v2
	v_mov_b32_e32 v46, v2
	v_mov_b32_e32 v47, v2
	v_mov_b32_e32 v48, v2
	v_mov_b32_e32 v49, v2
	v_mov_b32_e32 v54, v2
	v_mov_b32_e32 v55, v2
	v_mov_b32_e32 v56, v2
	v_mov_b32_e32 v57, v2
	v_mov_b32_e32 v58, v2
	v_mov_b32_e32 v59, v2
	v_mov_b32_e32 v60, v2
	v_mov_b32_e32 v61, v2
	v_mov_b32_e32 v62, v2
	v_mov_b32_e32 v63, v2
	v_mov_b32_e32 v64, v2
	v_mov_b32_e32 v65, v2
	v_mov_b32_e32 v66, v2
	v_mov_b32_e32 v67, v2
	v_mov_b32_e32 v68, v2
	v_mov_b32_e32 v69, v2
	v_mov_b32_e32 v70, v2
	v_mov_b32_e32 v71, v2
	v_mov_b32_e32 v72, v2
	v_mov_b32_e32 v73, v2
	v_mov_b32_e32 v74, v2
	v_mov_b32_e32 v75, v2
	v_mov_b32_e32 v76, v2
	v_mov_b32_e32 v77, v2
	v_mov_b32_e32 v82, v2
	v_mov_b32_e32 v83, v2
	v_mov_b32_e32 v84, v2
	v_mov_b32_e32 v85, v2
	v_mov_b32_e32 v90, v2
	v_mov_b32_e32 v91, v2
	v_mov_b32_e32 v92, v2
	v_mov_b32_e32 v93, v2
	v_mov_b32_e32 v98, v2
	v_mov_b32_e32 v99, v2
	v_mov_b32_e32 v100, v2
	v_mov_b32_e32 v101, v2
	v_mov_b32_e32 v106, v2
	v_mov_b32_e32 v107, v2
	v_mov_b32_e32 v108, v2
	v_mov_b32_e32 v109, v2
	v_mov_b32_e32 v114, v2
	v_mov_b32_e32 v115, v2
	v_mov_b32_e32 v116, v2
	v_mov_b32_e32 v117, v2
	v_mov_b32_e32 v78, v2
	v_mov_b32_e32 v79, v2
	v_mov_b32_e32 v80, v2
	v_mov_b32_e32 v81, v2
	v_mov_b32_e32 v86, v2
	v_mov_b32_e32 v87, v2
	v_mov_b32_e32 v88, v2
	v_mov_b32_e32 v89, v2
	v_mov_b32_e32 v94, v2
	v_mov_b32_e32 v95, v2
	v_mov_b32_e32 v96, v2
	v_mov_b32_e32 v97, v2
	v_mov_b32_e32 v102, v2
	v_mov_b32_e32 v103, v2
	v_mov_b32_e32 v104, v2
	v_mov_b32_e32 v105, v2
	v_mov_b32_e32 v110, v2
	v_mov_b32_e32 v111, v2
	v_mov_b32_e32 v112, v2
	v_mov_b32_e32 v113, v2
	v_mov_b32_e32 v118, v2
	v_mov_b32_e32 v119, v2
	v_mov_b32_e32 v120, v2
	v_mov_b32_e32 v121, v2
	v_mov_b32_e32 v122, v2
	v_mov_b32_e32 v123, v2
	v_mov_b32_e32 v124, v2
	v_mov_b32_e32 v125, v2
	v_mov_b32_e32 v126, v2
	v_mov_b32_e32 v127, v2
	v_mov_b32_e32 v128, v2
	v_mov_b32_e32 v129, v2
	s_mov_b64 vcc, s[10:11]
	s_cbranch_vccnz .Lsp_119
	s_setprio 1
.Lsp_119:
.LBB0_119:
	ds_read_b128 v[148:151], v153
	ds_read_b128 v[156:159], v153 offset:1024
	ds_read_b128 v[160:163], v153 offset:2048
	ds_read_b128 v[164:167], v153 offset:3072
	ds_read_b128 v[168:171], v154
	ds_read_b128 v[172:175], v154 offset:1024
	ds_read_b128 v[176:179], v154 offset:2048
	ds_read_b128 v[180:183], v154 offset:3072
	s_add_u32 s24, s22, 0xfff80080
	s_addc_u32 s25, s23, -1
	s_cmp_eq_u32 s79, 28
	s_cselect_b32 s27, s15, s25
	s_cselect_b32 s26, s75, s24
	s_cselect_b32 s25, s13, s78
	s_cselect_b32 s24, s76, s77
	s_add_i32 m0, s21, 0xc000
	ds_read_b128 v[184:187], v155
	ds_read_b128 v[188:191], v155 offset:1024
	ds_read_b128 v[192:195], v155 offset:2048
	ds_read_b128 v[196:199], v155 offset:3072
	ds_read_b128 v[200:203], v155 offset:4096
	ds_read_b128 v[204:207], v155 offset:5120
	ds_read_b128 v[208:211], v155 offset:6144
	ds_read_b128 v[212:215], v155 offset:7168
	global_load_lds_dwordx4 v140, s[22:23]
	s_add_i32 m0, s21, 0xe000
	s_nop 0
	global_load_lds_dwordx4 v142, s[22:23]
	s_waitcnt vmcnt(8)
	s_waitcnt lgkmcnt(0)
	s_barrier
	v_mfma_f32_16x16x32_bf16 v[126:129], v[148:151], v[184:187], v[126:129]
	v_mfma_f32_16x16x32_bf16 v[122:125], v[160:163], v[184:187], v[122:125]
	v_mfma_f32_16x16x32_bf16 v[118:121], v[148:151], v[192:195], v[118:121]
	v_mfma_f32_16x16x32_bf16 v[110:113], v[160:163], v[192:195], v[110:113]
	v_mfma_f32_16x16x32_bf16 v[102:105], v[148:151], v[200:203], v[102:105]
	v_mfma_f32_16x16x32_bf16 v[94:97], v[160:163], v[200:203], v[94:97]
	v_mfma_f32_16x16x32_bf16 v[86:89], v[148:151], v[208:211], v[86:89]
	v_mfma_f32_16x16x32_bf16 v[78:81], v[160:163], v[208:211], v[78:81]
	v_mfma_f32_16x16x32_bf16 v[126:129], v[156:159], v[188:191], v[126:129]
	v_mfma_f32_16x16x32_bf16 v[122:125], v[164:167], v[188:191], v[122:125]
	v_mfma_f32_16x16x32_bf16 v[118:121], v[156:159], v[196:199], v[118:121]
	v_mfma_f32_16x16x32_bf16 v[110:113], v[164:167], v[196:199], v[110:113]
	v_mfma_f32_16x16x32_bf16 v[102:105], v[156:159], v[204:207], v[102:105]
	v_mfma_f32_16x16x32_bf16 v[94:97], v[164:167], v[204:207], v[94:97]
	v_mfma_f32_16x16x32_bf16 v[86:89], v[156:159], v[212:215], v[86:89]
	v_mfma_f32_16x16x32_bf16 v[78:81], v[164:167], v[212:215], v[78:81]
	v_mfma_f32_16x16x32_bf16 v[114:117], v[168:171], v[184:187], v[114:117]
	v_mfma_f32_16x16x32_bf16 v[106:109], v[176:179], v[184:187], v[106:109]
	v_mfma_f32_16x16x32_bf16 v[98:101], v[168:171], v[192:195], v[98:101]
	v_mfma_f32_16x16x32_bf16 v[90:93], v[176:179], v[192:195], v[90:93]
	v_mfma_f32_16x16x32_bf16 v[82:85], v[168:171], v[200:203], v[82:85]
	v_mfma_f32_16x16x32_bf16 v[74:77], v[176:179], v[200:203], v[74:77]
	v_mfma_f32_16x16x32_bf16 v[70:73], v[168:171], v[208:211], v[70:73]
	v_mfma_f32_16x16x32_bf16 v[66:69], v[176:179], v[208:211], v[66:69]
	v_mfma_f32_16x16x32_bf16 v[114:117], v[172:175], v[188:191], v[114:117]
	v_mfma_f32_16x16x32_bf16 v[106:109], v[180:183], v[188:191], v[106:109]
	v_mfma_f32_16x16x32_bf16 v[98:101], v[172:175], v[196:199], v[98:101]
	v_mfma_f32_16x16x32_bf16 v[90:93], v[180:183], v[196:199], v[90:93]
	v_mfma_f32_16x16x32_bf16 v[82:85], v[172:175], v[204:207], v[82:85]
	v_mfma_f32_16x16x32_bf16 v[74:77], v[180:183], v[204:207], v[74:77]
	v_mfma_f32_16x16x32_bf16 v[70:73], v[172:175], v[212:215], v[70:73]
	v_mfma_f32_16x16x32_bf16 v[66:69], v[180:183], v[212:215], v[66:69]
	s_barrier
	s_add_i32 s80, s71, s33
	v_lshl_add_u64 v[216:217], s[24:25], 0, v[136:137]
	s_mov_b32 m0, s80
	ds_read_b128 v[184:187], v155 offset:16384
	ds_read_b128 v[188:191], v155 offset:17408
	ds_read_b128 v[192:195], v155 offset:18432
	ds_read_b128 v[196:199], v155 offset:19456
	ds_read_b128 v[200:203], v155 offset:20480
	ds_read_b128 v[204:207], v155 offset:21504
	ds_read_b128 v[208:211], v155 offset:22528
	ds_read_b128 v[212:215], v155 offset:23552
	global_load_lds_dwordx4 v136, s[24:25]
	s_add_i32 m0, s80, 0x2000
	s_add_u32 s80, s24, 0x80000
	v_lshl_add_u64 v[218:219], s[24:25], 0, v[132:133]
	s_addc_u32 s81, s25, 0
	s_add_i32 s82, s72, s33
	global_load_lds_dwordx4 v132, s[24:25]
	s_mov_b32 m0, s82
	v_lshl_add_u64 v[222:223], s[26:27], 0, v[134:135]
	global_load_lds_dwordx4 v136, s[80:81]
	s_add_i32 m0, s82, 0x2000
	s_nop 0
	global_load_lds_dwordx4 v132, s[80:81]
	v_lshl_add_u64 v[220:221], s[26:27], 0, v[138:139]
	s_mov_b32 m0, s21
	s_nop 0
	global_load_lds_dwordx4 v138, s[26:27]
	s_mov_b32 m0, s36
	s_nop 0
	global_load_lds_dwordx4 v134, s[26:27]
	s_waitcnt vmcnt(8)
	s_waitcnt lgkmcnt(0)
	s_barrier
	v_mfma_f32_16x16x32_bf16 v[62:65], v[148:151], v[184:187], v[62:65]
	v_mfma_f32_16x16x32_bf16 v[58:61], v[160:163], v[184:187], v[58:61]
	v_mfma_f32_16x16x32_bf16 v[54:57], v[148:151], v[192:195], v[54:57]
	v_mfma_f32_16x16x32_bf16 v[46:49], v[160:163], v[192:195], v[46:49]
	v_mfma_f32_16x16x32_bf16 v[38:41], v[148:151], v[200:203], v[38:41]
	v_mfma_f32_16x16x32_bf16 v[30:33], v[160:163], v[200:203], v[30:33]
	v_mfma_f32_16x16x32_bf16 v[22:25], v[148:151], v[208:211], v[22:25]
	v_mfma_f32_16x16x32_bf16 v[14:17], v[160:163], v[208:211], v[14:17]
	v_mfma_f32_16x16x32_bf16 v[62:65], v[156:159], v[188:191], v[62:65]
	v_mfma_f32_16x16x32_bf16 v[58:61], v[164:167], v[188:191], v[58:61]
	v_mfma_f32_16x16x32_bf16 v[54:57], v[156:159], v[196:199], v[54:57]
	v_mfma_f32_16x16x32_bf16 v[46:49], v[164:167], v[196:199], v[46:49]
	v_mfma_f32_16x16x32_bf16 v[38:41], v[156:159], v[204:207], v[38:41]
	v_mfma_f32_16x16x32_bf16 v[30:33], v[164:167], v[204:207], v[30:33]
	v_mfma_f32_16x16x32_bf16 v[22:25], v[156:159], v[212:215], v[22:25]
	v_mfma_f32_16x16x32_bf16 v[14:17], v[164:167], v[212:215], v[14:17]
	v_mfma_f32_16x16x32_bf16 v[50:53], v[168:171], v[184:187], v[50:53]
	v_mfma_f32_16x16x32_bf16 v[42:45], v[176:179], v[184:187], v[42:45]
	v_mfma_f32_16x16x32_bf16 v[34:37], v[168:171], v[192:195], v[34:37]
	v_mfma_f32_16x16x32_bf16 v[26:29], v[176:179], v[192:195], v[26:29]
	v_mfma_f32_16x16x32_bf16 v[18:21], v[168:171], v[200:203], v[18:21]
	v_mfma_f32_16x16x32_bf16 v[10:13], v[176:179], v[200:203], v[10:13]
	v_mfma_f32_16x16x32_bf16 v[6:9], v[168:171], v[208:211], v[6:9]
	v_mfma_f32_16x16x32_bf16 v[2:5], v[176:179], v[208:211], v[2:5]
	v_mfma_f32_16x16x32_bf16 v[50:53], v[172:175], v[188:191], v[50:53]
	v_mfma_f32_16x16x32_bf16 v[42:45], v[180:183], v[188:191], v[42:45]
	v_mfma_f32_16x16x32_bf16 v[34:37], v[172:175], v[196:199], v[34:37]
	v_mfma_f32_16x16x32_bf16 v[26:29], v[180:183], v[196:199], v[26:29]
	v_mfma_f32_16x16x32_bf16 v[18:21], v[172:175], v[204:207], v[18:21]
	v_mfma_f32_16x16x32_bf16 v[10:13], v[180:183], v[204:207], v[10:13]
	v_mfma_f32_16x16x32_bf16 v[6:9], v[172:175], v[212:215], v[6:9]
	v_mfma_f32_16x16x32_bf16 v[2:5], v[180:183], v[212:215], v[2:5]
	s_barrier
	s_add_i32 s80, 0, 0x18000
	s_add_i32 s81, 0, 0x1c000
	v_add_u32_e32 v164, s80, v131
	v_add_u32_e32 v180, s81, v131
	ds_read_b128 v[148:151], v164
	ds_read_b128 v[156:159], v164 offset:1024
	ds_read_b128 v[160:163], v164 offset:2048
	ds_read_b128 v[164:167], v164 offset:3072
	ds_read_b128 v[168:171], v180
	ds_read_b128 v[172:175], v180 offset:1024
	ds_read_b128 v[176:179], v180 offset:2048
	ds_read_b128 v[180:183], v180 offset:3072
	s_add_u32 s26, s26, 0x80000
	s_addc_u32 s27, s27, 0
	s_mov_b32 m0, s37
	ds_read_b128 v[184:187], v155 offset:32768
	ds_read_b128 v[188:191], v155 offset:33792
	ds_read_b128 v[192:195], v155 offset:34816
	ds_read_b128 v[196:199], v155 offset:35840
	ds_read_b128 v[200:203], v155 offset:36864
	ds_read_b128 v[204:207], v155 offset:37888
	ds_read_b128 v[208:211], v155 offset:38912
	ds_read_b128 v[212:215], v155 offset:39936
	global_load_lds_dwordx4 v138, s[26:27]
	s_mov_b32 m0, s42
	s_nop 0
	global_load_lds_dwordx4 v134, s[26:27]
	s_waitcnt vmcnt(8)
	s_waitcnt lgkmcnt(0)
	s_barrier
	v_mfma_f32_16x16x32_bf16 v[126:129], v[148:151], v[184:187], v[126:129]
	v_mfma_f32_16x16x32_bf16 v[122:125], v[160:163], v[184:187], v[122:125]
	v_mfma_f32_16x16x32_bf16 v[118:121], v[148:151], v[192:195], v[118:121]
	v_mfma_f32_16x16x32_bf16 v[110:113], v[160:163], v[192:195], v[110:113]
	v_mfma_f32_16x16x32_bf16 v[102:105], v[148:151], v[200:203], v[102:105]
	v_mfma_f32_16x16x32_bf16 v[94:97], v[160:163], v[200:203], v[94:97]
	v_mfma_f32_16x16x32_bf16 v[86:89], v[148:151], v[208:211], v[86:89]
	v_mfma_f32_16x16x32_bf16 v[78:81], v[160:163], v[208:211], v[78:81]
	v_mfma_f32_16x16x32_bf16 v[126:129], v[156:159], v[188:191], v[126:129]
	v_mfma_f32_16x16x32_bf16 v[122:125], v[164:167], v[188:191], v[122:125]
	v_mfma_f32_16x16x32_bf16 v[118:121], v[156:159], v[196:199], v[118:121]
	v_mfma_f32_16x16x32_bf16 v[110:113], v[164:167], v[196:199], v[110:113]
	v_mfma_f32_16x16x32_bf16 v[102:105], v[156:159], v[204:207], v[102:105]
	v_mfma_f32_16x16x32_bf16 v[94:97], v[164:167], v[204:207], v[94:97]
	v_mfma_f32_16x16x32_bf16 v[86:89], v[156:159], v[212:215], v[86:89]
	v_mfma_f32_16x16x32_bf16 v[78:81], v[164:167], v[212:215], v[78:81]
	v_mfma_f32_16x16x32_bf16 v[114:117], v[168:171], v[184:187], v[114:117]
	v_mfma_f32_16x16x32_bf16 v[106:109], v[176:179], v[184:187], v[106:109]
	v_mfma_f32_16x16x32_bf16 v[98:101], v[168:171], v[192:195], v[98:101]
	v_mfma_f32_16x16x32_bf16 v[90:93], v[176:179], v[192:195], v[90:93]
	v_mfma_f32_16x16x32_bf16 v[82:85], v[168:171], v[200:203], v[82:85]
	v_mfma_f32_16x16x32_bf16 v[74:77], v[176:179], v[200:203], v[74:77]
	v_mfma_f32_16x16x32_bf16 v[70:73], v[168:171], v[208:211], v[70:73]
	v_mfma_f32_16x16x32_bf16 v[66:69], v[176:179], v[208:211], v[66:69]
	v_mfma_f32_16x16x32_bf16 v[114:117], v[172:175], v[188:191], v[114:117]
	v_mfma_f32_16x16x32_bf16 v[106:109], v[180:183], v[188:191], v[106:109]
	v_mfma_f32_16x16x32_bf16 v[98:101], v[172:175], v[196:199], v[98:101]
	v_mfma_f32_16x16x32_bf16 v[90:93], v[180:183], v[196:199], v[90:93]
	v_mfma_f32_16x16x32_bf16 v[82:85], v[172:175], v[204:207], v[82:85]
	v_mfma_f32_16x16x32_bf16 v[74:77], v[180:183], v[204:207], v[74:77]
	v_mfma_f32_16x16x32_bf16 v[70:73], v[172:175], v[212:215], v[70:73]
	v_mfma_f32_16x16x32_bf16 v[66:69], v[180:183], v[212:215], v[66:69]
	s_barrier
	s_add_i32 s26, s80, s33
	v_lshl_add_u64 v[216:217], v[216:217], 0, s[8:9]
	s_mov_b32 m0, s26
	ds_read_b128 v[184:187], v155 offset:49152
	ds_read_b128 v[188:191], v155 offset:50176
	ds_read_b128 v[192:195], v155 offset:51200
	ds_read_b128 v[196:199], v155 offset:52224
	ds_read_b128 v[200:203], v155 offset:53248
	ds_read_b128 v[204:207], v155 offset:54272
	ds_read_b128 v[208:211], v155 offset:55296
	ds_read_b128 v[212:215], v155 offset:56320
	global_load_lds_dwordx4 v[216:217], off
	s_add_i32 m0, s26, 0x2000
	s_add_u32 s24, s24, 0x80080
	v_lshl_add_u64 v[216:217], v[218:219], 0, s[8:9]
	s_addc_u32 s25, s25, 0
	s_add_i32 s26, s81, s33
	global_load_lds_dwordx4 v[216:217], off
	s_mov_b32 m0, s26
	s_nop 0
	global_load_lds_dwordx4 v136, s[24:25]
	s_add_i32 m0, s26, 0x2000
	s_nop 0
	global_load_lds_dwordx4 v132, s[24:25]
	v_lshl_add_u64 v[216:217], v[220:221], 0, s[8:9]
	s_mov_b32 m0, s44
	s_nop 0
	global_load_lds_dwordx4 v[216:217], off
	v_lshl_add_u64 v[216:217], v[222:223], 0, s[8:9]
	s_mov_b32 m0, s45
	s_nop 0
	global_load_lds_dwordx4 v[216:217], off
	s_waitcnt vmcnt(8)
	s_waitcnt lgkmcnt(0)
	s_barrier
	v_mfma_f32_16x16x32_bf16 v[62:65], v[148:151], v[184:187], v[62:65]
	v_mfma_f32_16x16x32_bf16 v[58:61], v[160:163], v[184:187], v[58:61]
	v_mfma_f32_16x16x32_bf16 v[54:57], v[148:151], v[192:195], v[54:57]
	v_mfma_f32_16x16x32_bf16 v[46:49], v[160:163], v[192:195], v[46:49]
	v_mfma_f32_16x16x32_bf16 v[38:41], v[148:151], v[200:203], v[38:41]
	v_mfma_f32_16x16x32_bf16 v[30:33], v[160:163], v[200:203], v[30:33]
	v_mfma_f32_16x16x32_bf16 v[22:25], v[148:151], v[208:211], v[22:25]
	v_mfma_f32_16x16x32_bf16 v[14:17], v[160:163], v[208:211], v[14:17]
	v_mfma_f32_16x16x32_bf16 v[62:65], v[156:159], v[188:191], v[62:65]
	v_mfma_f32_16x16x32_bf16 v[58:61], v[164:167], v[188:191], v[58:61]
	v_mfma_f32_16x16x32_bf16 v[54:57], v[156:159], v[196:199], v[54:57]
	v_mfma_f32_16x16x32_bf16 v[46:49], v[164:167], v[196:199], v[46:49]
	v_mfma_f32_16x16x32_bf16 v[38:41], v[156:159], v[204:207], v[38:41]
	v_mfma_f32_16x16x32_bf16 v[30:33], v[164:167], v[204:207], v[30:33]
	v_mfma_f32_16x16x32_bf16 v[22:25], v[156:159], v[212:215], v[22:25]
	v_mfma_f32_16x16x32_bf16 v[14:17], v[164:167], v[212:215], v[14:17]
	v_mfma_f32_16x16x32_bf16 v[50:53], v[168:171], v[184:187], v[50:53]
	v_mfma_f32_16x16x32_bf16 v[42:45], v[176:179], v[184:187], v[42:45]
	v_mfma_f32_16x16x32_bf16 v[34:37], v[168:171], v[192:195], v[34:37]
	v_mfma_f32_16x16x32_bf16 v[26:29], v[176:179], v[192:195], v[26:29]
	v_mfma_f32_16x16x32_bf16 v[18:21], v[168:171], v[200:203], v[18:21]
	v_mfma_f32_16x16x32_bf16 v[10:13], v[176:179], v[200:203], v[10:13]
	v_mfma_f32_16x16x32_bf16 v[6:9], v[168:171], v[208:211], v[6:9]
	v_mfma_f32_16x16x32_bf16 v[2:5], v[176:179], v[208:211], v[2:5]
	v_mfma_f32_16x16x32_bf16 v[50:53], v[172:175], v[188:191], v[50:53]
	v_mfma_f32_16x16x32_bf16 v[42:45], v[180:183], v[188:191], v[42:45]
	v_mfma_f32_16x16x32_bf16 v[34:37], v[172:175], v[196:199], v[34:37]
	v_mfma_f32_16x16x32_bf16 v[26:29], v[180:183], v[196:199], v[26:29]
	v_mfma_f32_16x16x32_bf16 v[18:21], v[172:175], v[204:207], v[18:21]
	v_mfma_f32_16x16x32_bf16 v[10:13], v[180:183], v[204:207], v[10:13]
	v_mfma_f32_16x16x32_bf16 v[6:9], v[172:175], v[212:215], v[6:9]
	v_mfma_f32_16x16x32_bf16 v[2:5], v[180:183], v[212:215], v[2:5]
	s_barrier
	s_add_i32 s79, s79, 2
	s_add_u32 s22, s22, 0x100
	s_addc_u32 s23, s23, 0
	s_add_u32 s77, s77, 0x100
	s_addc_u32 s78, s78, 0
	s_cmp_gt_u32 s79, 29
	s_cbranch_scc0 .LBB0_119
	s_setprio 0
	s_and_b64 vcc, exec, s[10:11]
	s_cbranch_vccz .LBB0_122
	s_barrier

.LBB0_465:
	s_ashr_i32 s27, s26, 31
	s_lshl_b64 s[28:29], s[26:27], 20
	s_add_u32 s28, s23, s28
	s_addc_u32 s29, s33, s29
	s_and_b64 s[30:31], s[12:13], exec
	s_cselect_b32 s1, s29, s37
	s_cselect_b32 s27, s28, s36
	s_ashr_i32 s25, s24, 31
	s_lshl_b64 s[30:31], s[24:25], 20
	s_add_u32 s30, s64, s30
	s_addc_u32 s31, s65, s31
	s_and_b64 s[44:45], s[12:13], exec
	s_cselect_b32 s25, s31, s43
	s_cselect_b32 s35, s30, s42
	s_add_u32 s36, s36, 0x80080
	s_addc_u32 s37, s37, 0
	s_add_u32 s62, s42, 0x100
	v_mov_b32_e32 v2, 0
	s_addc_u32 s63, s43, 0
	s_mov_b32 s83, -2
	v_mov_b32_e32 v3, v2
	v_mov_b32_e32 v4, v2
	v_mov_b32_e32 v5, v2
	v_mov_b32_e32 v6, v2
	v_mov_b32_e32 v7, v2
	v_mov_b32_e32 v8, v2
	v_mov_b32_e32 v9, v2
	v_mov_b32_e32 v18, v2
	v_mov_b32_e32 v19, v2
	v_mov_b32_e32 v20, v2
	v_mov_b32_e32 v21, v2
	v_mov_b32_e32 v22, v2
	v_mov_b32_e32 v23, v2
	v_mov_b32_e32 v24, v2
	v_mov_b32_e32 v25, v2
	v_mov_b32_e32 v34, v2
	v_mov_b32_e32 v35, v2
	v_mov_b32_e32 v36, v2
	v_mov_b32_e32 v37, v2
	v_mov_b32_e32 v38, v2
	v_mov_b32_e32 v39, v2
	v_mov_b32_e32 v40, v2
	v_mov_b32_e32 v41, v2
	v_mov_b32_e32 v50, v2
	v_mov_b32_e32 v51, v2
	v_mov_b32_e32 v52, v2
	v_mov_b32_e32 v53, v2
	v_mov_b32_e32 v54, v2
	v_mov_b32_e32 v55, v2
	v_mov_b32_e32 v56, v2
	v_mov_b32_e32 v57, v2
	v_mov_b32_e32 v10, v2
	v_mov_b32_e32 v11, v2
	v_mov_b32_e32 v12, v2
	v_mov_b32_e32 v13, v2
	s_waitcnt vmcnt(0)
	v_mov_b32_e32 v14, v2
	v_mov_b32_e32 v15, v2
	v_mov_b32_e32 v16, v2
	v_mov_b32_e32 v17, v2
	v_mov_b32_e32 v26, v2
	v_mov_b32_e32 v27, v2
	v_mov_b32_e32 v28, v2
	v_mov_b32_e32 v29, v2
	v_mov_b32_e32 v30, v2
	v_mov_b32_e32 v31, v2
	v_mov_b32_e32 v32, v2
	v_mov_b32_e32 v33, v2
	v_mov_b32_e32 v42, v2
	v_mov_b32_e32 v43, v2
	v_mov_b32_e32 v44, v2
	v_mov_b32_e32 v45, v2
	v_mov_b32_e32 v46, v2
	v_mov_b32_e32 v47, v2
	v_mov_b32_e32 v48, v2
	v_mov_b32_e32 v49, v2
	v_mov_b32_e32 v58, v2
	v_mov_b32_e32 v59, v2
	v_mov_b32_e32 v60, v2
	v_mov_b32_e32 v61, v2
	v_mov_b32_e32 v62, v2
	v_mov_b32_e32 v63, v2
	v_mov_b32_e32 v64, v2
	v_mov_b32_e32 v65, v2
	v_mov_b32_e32 v66, v2
	v_mov_b32_e32 v67, v2
	v_mov_b32_e32 v68, v2
	v_mov_b32_e32 v69, v2
	v_mov_b32_e32 v70, v2
	v_mov_b32_e32 v71, v2
	v_mov_b32_e32 v72, v2
	v_mov_b32_e32 v73, v2
	v_mov_b32_e32 v82, v2
	v_mov_b32_e32 v83, v2
	v_mov_b32_e32 v84, v2
	v_mov_b32_e32 v85, v2
	v_mov_b32_e32 v86, v2
	v_mov_b32_e32 v87, v2
	v_mov_b32_e32 v88, v2
	v_mov_b32_e32 v89, v2
	v_mov_b32_e32 v98, v2
	v_mov_b32_e32 v99, v2
	v_mov_b32_e32 v100, v2
	v_mov_b32_e32 v101, v2
	v_mov_b32_e32 v102, v2
	v_mov_b32_e32 v103, v2
	v_mov_b32_e32 v104, v2
	v_mov_b32_e32 v105, v2
	v_mov_b32_e32 v114, v2
	v_mov_b32_e32 v115, v2
	v_mov_b32_e32 v116, v2
	v_mov_b32_e32 v117, v2
	v_mov_b32_e32 v118, v2
	v_mov_b32_e32 v119, v2
	v_mov_b32_e32 v120, v2
	v_mov_b32_e32 v121, v2
	v_mov_b32_e32 v74, v2
	v_mov_b32_e32 v75, v2
	v_mov_b32_e32 v76, v2
	v_mov_b32_e32 v77, v2
	v_mov_b32_e32 v78, v2
	v_mov_b32_e32 v79, v2
	v_mov_b32_e32 v80, v2
	v_mov_b32_e32 v81, v2
	v_mov_b32_e32 v90, v2
	v_mov_b32_e32 v91, v2
	v_mov_b32_e32 v92, v2
	v_mov_b32_e32 v93, v2
	v_mov_b32_e32 v94, v2
	v_mov_b32_e32 v95, v2
	v_mov_b32_e32 v96, v2
	v_mov_b32_e32 v97, v2
	v_mov_b32_e32 v106, v2
	v_mov_b32_e32 v107, v2
	v_mov_b32_e32 v108, v2
	v_mov_b32_e32 v109, v2
	v_mov_b32_e32 v110, v2
	v_mov_b32_e32 v111, v2
	v_mov_b32_e32 v112, v2
	v_mov_b32_e32 v113, v2
	v_mov_b32_e32 v122, v2
	v_mov_b32_e32 v123, v2
	v_mov_b32_e32 v124, v2
	v_mov_b32_e32 v125, v2
	v_mov_b32_e32 v126, v2
	v_mov_b32_e32 v127, v2
	v_mov_b32_e32 v128, v2
	v_mov_b32_e32 v129, v2
	s_mov_b64 vcc, s[20:21]
	s_cbranch_vccnz .Lsp_466
	s_setprio 1
.Lsp_466:
.LBB0_466:
	ds_read_b128 v[150:153], v211
	ds_read_b128 v[154:157], v211 offset:1024
	ds_read_b128 v[158:161], v211 offset:2048
	ds_read_b128 v[162:165], v211 offset:3072
	ds_read_b128 v[166:169], v212
	ds_read_b128 v[170:173], v212 offset:1024
	ds_read_b128 v[174:177], v212 offset:2048
	ds_read_b128 v[178:181], v212 offset:3072
	s_add_u32 s42, s36, 0xfff80080
	s_addc_u32 s43, s37, -1
	s_cmp_eq_u32 s83, 28
	s_cselect_b32 s45, s1, s43
	s_cselect_b32 s44, s27, s42
	s_cselect_b32 s43, s25, s63
	s_cselect_b32 s42, s35, s62
	s_add_i32 m0, s67, 0xc000
	ds_read_b128 v[182:185], v213
	ds_read_b128 v[186:189], v213 offset:1024
	ds_read_b128 v[190:193], v213 offset:2048
	ds_read_b128 v[194:197], v213 offset:3072
	ds_read_b128 v[198:201], v213 offset:4096
	ds_read_b128 v[202:205], v213 offset:5120
	ds_read_b128 v[218:221], v213 offset:6144
	ds_read_b128 v[222:225], v213 offset:7168
	global_load_lds_dwordx4 v142, s[36:37]
	s_add_i32 m0, s67, 0xe000
	s_nop 0
	global_load_lds_dwordx4 v144, s[36:37]
	s_waitcnt vmcnt(8)
	s_waitcnt lgkmcnt(0)
	s_barrier
	v_mfma_f32_16x16x32_bf16 v[126:129], v[150:153], v[182:185], v[126:129]
	v_mfma_f32_16x16x32_bf16 v[122:125], v[158:161], v[182:185], v[122:125]
	v_mfma_f32_16x16x32_bf16 v[110:113], v[150:153], v[190:193], v[110:113]
	v_mfma_f32_16x16x32_bf16 v[106:109], v[158:161], v[190:193], v[106:109]
	v_mfma_f32_16x16x32_bf16 v[94:97], v[150:153], v[198:201], v[94:97]
	v_mfma_f32_16x16x32_bf16 v[90:93], v[158:161], v[198:201], v[90:93]
	v_mfma_f32_16x16x32_bf16 v[78:81], v[150:153], v[218:221], v[78:81]
	v_mfma_f32_16x16x32_bf16 v[74:77], v[158:161], v[218:221], v[74:77]
	v_mfma_f32_16x16x32_bf16 v[126:129], v[154:157], v[186:189], v[126:129]
	v_mfma_f32_16x16x32_bf16 v[122:125], v[162:165], v[186:189], v[122:125]
	v_mfma_f32_16x16x32_bf16 v[110:113], v[154:157], v[194:197], v[110:113]
	v_mfma_f32_16x16x32_bf16 v[106:109], v[162:165], v[194:197], v[106:109]
	v_mfma_f32_16x16x32_bf16 v[94:97], v[154:157], v[202:205], v[94:97]
	v_mfma_f32_16x16x32_bf16 v[90:93], v[162:165], v[202:205], v[90:93]
	v_mfma_f32_16x16x32_bf16 v[78:81], v[154:157], v[222:225], v[78:81]
	v_mfma_f32_16x16x32_bf16 v[74:77], v[162:165], v[222:225], v[74:77]
	v_mfma_f32_16x16x32_bf16 v[118:121], v[166:169], v[182:185], v[118:121]
	v_mfma_f32_16x16x32_bf16 v[114:117], v[174:177], v[182:185], v[114:117]
	v_mfma_f32_16x16x32_bf16 v[102:105], v[166:169], v[190:193], v[102:105]
	v_mfma_f32_16x16x32_bf16 v[98:101], v[174:177], v[190:193], v[98:101]
	v_mfma_f32_16x16x32_bf16 v[86:89], v[166:169], v[198:201], v[86:89]
	v_mfma_f32_16x16x32_bf16 v[82:85], v[174:177], v[198:201], v[82:85]
	v_mfma_f32_16x16x32_bf16 v[70:73], v[166:169], v[218:221], v[70:73]
	v_mfma_f32_16x16x32_bf16 v[66:69], v[174:177], v[218:221], v[66:69]
	v_mfma_f32_16x16x32_bf16 v[118:121], v[170:173], v[186:189], v[118:121]
	v_mfma_f32_16x16x32_bf16 v[114:117], v[178:181], v[186:189], v[114:117]
	v_mfma_f32_16x16x32_bf16 v[102:105], v[170:173], v[194:197], v[102:105]
	v_mfma_f32_16x16x32_bf16 v[98:101], v[178:181], v[194:197], v[98:101]
	v_mfma_f32_16x16x32_bf16 v[86:89], v[170:173], v[202:205], v[86:89]
	v_mfma_f32_16x16x32_bf16 v[82:85], v[178:181], v[202:205], v[82:85]
	v_mfma_f32_16x16x32_bf16 v[70:73], v[170:173], v[222:225], v[70:73]
	v_mfma_f32_16x16x32_bf16 v[66:69], v[178:181], v[222:225], v[66:69]
	s_barrier
	s_add_i32 s84, s79, s66
	v_lshl_add_u64 v[226:227], s[42:43], 0, v[132:133]
	s_mov_b32 m0, s84
	ds_read_b128 v[182:185], v213 offset:16384
	ds_read_b128 v[186:189], v213 offset:17408
	ds_read_b128 v[190:193], v213 offset:18432
	ds_read_b128 v[194:197], v213 offset:19456
	ds_read_b128 v[198:201], v213 offset:20480
	ds_read_b128 v[202:205], v213 offset:21504
	ds_read_b128 v[218:221], v213 offset:22528
	ds_read_b128 v[222:225], v213 offset:23552
	global_load_lds_dwordx4 v132, s[42:43]
	s_add_i32 m0, s84, 0x2000
	s_add_u32 s84, s42, 0x80000
	v_lshl_add_u64 v[228:229], s[42:43], 0, v[136:137]
	s_addc_u32 s85, s43, 0
	s_add_i32 s86, s80, s66
	global_load_lds_dwordx4 v136, s[42:43]
	s_mov_b32 m0, s86
	v_lshl_add_u64 v[232:233], s[44:45], 0, v[134:135]
	global_load_lds_dwordx4 v132, s[84:85]
	s_add_i32 m0, s86, 0x2000
	s_nop 0
	global_load_lds_dwordx4 v136, s[84:85]
	v_lshl_add_u64 v[230:231], s[44:45], 0, v[130:131]
	s_mov_b32 m0, s67
	s_nop 0
	global_load_lds_dwordx4 v130, s[44:45]
	s_mov_b32 m0, s68
	s_nop 0
	global_load_lds_dwordx4 v134, s[44:45]
	s_waitcnt vmcnt(8)
	s_waitcnt lgkmcnt(0)
	s_barrier
	v_mfma_f32_16x16x32_bf16 v[62:65], v[150:153], v[182:185], v[62:65]
	v_mfma_f32_16x16x32_bf16 v[58:61], v[158:161], v[182:185], v[58:61]
	v_mfma_f32_16x16x32_bf16 v[46:49], v[150:153], v[190:193], v[46:49]
	v_mfma_f32_16x16x32_bf16 v[42:45], v[158:161], v[190:193], v[42:45]
	v_mfma_f32_16x16x32_bf16 v[30:33], v[150:153], v[198:201], v[30:33]
	v_mfma_f32_16x16x32_bf16 v[26:29], v[158:161], v[198:201], v[26:29]
	v_mfma_f32_16x16x32_bf16 v[14:17], v[150:153], v[218:221], v[14:17]
	v_mfma_f32_16x16x32_bf16 v[10:13], v[158:161], v[218:221], v[10:13]
	v_mfma_f32_16x16x32_bf16 v[62:65], v[154:157], v[186:189], v[62:65]
	v_mfma_f32_16x16x32_bf16 v[58:61], v[162:165], v[186:189], v[58:61]
	v_mfma_f32_16x16x32_bf16 v[46:49], v[154:157], v[194:197], v[46:49]
	v_mfma_f32_16x16x32_bf16 v[42:45], v[162:165], v[194:197], v[42:45]
	v_mfma_f32_16x16x32_bf16 v[30:33], v[154:157], v[202:205], v[30:33]
	v_mfma_f32_16x16x32_bf16 v[26:29], v[162:165], v[202:205], v[26:29]
	v_mfma_f32_16x16x32_bf16 v[14:17], v[154:157], v[222:225], v[14:17]
	v_mfma_f32_16x16x32_bf16 v[10:13], v[162:165], v[222:225], v[10:13]
	v_mfma_f32_16x16x32_bf16 v[54:57], v[166:169], v[182:185], v[54:57]
	v_mfma_f32_16x16x32_bf16 v[50:53], v[174:177], v[182:185], v[50:53]
	v_mfma_f32_16x16x32_bf16 v[38:41], v[166:169], v[190:193], v[38:41]
	v_mfma_f32_16x16x32_bf16 v[34:37], v[174:177], v[190:193], v[34:37]
	v_mfma_f32_16x16x32_bf16 v[22:25], v[166:169], v[198:201], v[22:25]
	v_mfma_f32_16x16x32_bf16 v[18:21], v[174:177], v[198:201], v[18:21]
	v_mfma_f32_16x16x32_bf16 v[6:9], v[166:169], v[218:221], v[6:9]
	v_mfma_f32_16x16x32_bf16 v[2:5], v[174:177], v[218:221], v[2:5]
	v_mfma_f32_16x16x32_bf16 v[54:57], v[170:173], v[186:189], v[54:57]
	v_mfma_f32_16x16x32_bf16 v[50:53], v[178:181], v[186:189], v[50:53]
	v_mfma_f32_16x16x32_bf16 v[38:41], v[170:173], v[194:197], v[38:41]
	v_mfma_f32_16x16x32_bf16 v[34:37], v[178:181], v[194:197], v[34:37]
	v_mfma_f32_16x16x32_bf16 v[22:25], v[170:173], v[202:205], v[22:25]
	v_mfma_f32_16x16x32_bf16 v[18:21], v[178:181], v[202:205], v[18:21]
	v_mfma_f32_16x16x32_bf16 v[6:9], v[170:173], v[222:225], v[6:9]
	v_mfma_f32_16x16x32_bf16 v[2:5], v[178:181], v[222:225], v[2:5]
	s_barrier
	s_add_i32 s84, 0, 0x18000
	v_add_u32_e32 v139, s84, v206
	s_add_i32 s85, 0, 0x1c000
	ds_read_b128 v[150:153], v139
	ds_read_b128 v[154:157], v139 offset:1024
	ds_read_b128 v[158:161], v139 offset:2048
	ds_read_b128 v[162:165], v139 offset:3072
	v_add_u32_e32 v139, s85, v206
	ds_read_b128 v[166:169], v139
	ds_read_b128 v[170:173], v139 offset:1024
	ds_read_b128 v[174:177], v139 offset:2048
	ds_read_b128 v[178:181], v139 offset:3072
	s_add_u32 s44, s44, 0x80000
	s_addc_u32 s45, s45, 0
	s_mov_b32 m0, s69
	ds_read_b128 v[182:185], v213 offset:32768
	ds_read_b128 v[186:189], v213 offset:33792
	ds_read_b128 v[190:193], v213 offset:34816
	ds_read_b128 v[194:197], v213 offset:35840
	ds_read_b128 v[198:201], v213 offset:36864
	ds_read_b128 v[202:205], v213 offset:37888
	ds_read_b128 v[218:221], v213 offset:38912
	ds_read_b128 v[222:225], v213 offset:39936
	global_load_lds_dwordx4 v130, s[44:45]
	s_mov_b32 m0, s70
	s_nop 0
	global_load_lds_dwordx4 v134, s[44:45]
	s_waitcnt vmcnt(8)
	s_waitcnt lgkmcnt(0)
	s_barrier
	v_mfma_f32_16x16x32_bf16 v[126:129], v[150:153], v[182:185], v[126:129]
	v_mfma_f32_16x16x32_bf16 v[122:125], v[158:161], v[182:185], v[122:125]
	v_mfma_f32_16x16x32_bf16 v[110:113], v[150:153], v[190:193], v[110:113]
	v_mfma_f32_16x16x32_bf16 v[106:109], v[158:161], v[190:193], v[106:109]
	v_mfma_f32_16x16x32_bf16 v[94:97], v[150:153], v[198:201], v[94:97]
	v_mfma_f32_16x16x32_bf16 v[90:93], v[158:161], v[198:201], v[90:93]
	v_mfma_f32_16x16x32_bf16 v[78:81], v[150:153], v[218:221], v[78:81]
	v_mfma_f32_16x16x32_bf16 v[74:77], v[158:161], v[218:221], v[74:77]
	v_mfma_f32_16x16x32_bf16 v[126:129], v[154:157], v[186:189], v[126:129]
	v_mfma_f32_16x16x32_bf16 v[122:125], v[162:165], v[186:189], v[122:125]
	v_mfma_f32_16x16x32_bf16 v[110:113], v[154:157], v[194:197], v[110:113]
	v_mfma_f32_16x16x32_bf16 v[106:109], v[162:165], v[194:197], v[106:109]
	v_mfma_f32_16x16x32_bf16 v[94:97], v[154:157], v[202:205], v[94:97]
	v_mfma_f32_16x16x32_bf16 v[90:93], v[162:165], v[202:205], v[90:93]
	v_mfma_f32_16x16x32_bf16 v[78:81], v[154:157], v[222:225], v[78:81]
	v_mfma_f32_16x16x32_bf16 v[74:77], v[162:165], v[222:225], v[74:77]
	v_mfma_f32_16x16x32_bf16 v[118:121], v[166:169], v[182:185], v[118:121]
	v_mfma_f32_16x16x32_bf16 v[114:117], v[174:177], v[182:185], v[114:117]
	v_mfma_f32_16x16x32_bf16 v[102:105], v[166:169], v[190:193], v[102:105]
	v_mfma_f32_16x16x32_bf16 v[98:101], v[174:177], v[190:193], v[98:101]
	v_mfma_f32_16x16x32_bf16 v[86:89], v[166:169], v[198:201], v[86:89]
	v_mfma_f32_16x16x32_bf16 v[82:85], v[174:177], v[198:201], v[82:85]
	v_mfma_f32_16x16x32_bf16 v[70:73], v[166:169], v[218:221], v[70:73]
	v_mfma_f32_16x16x32_bf16 v[66:69], v[174:177], v[218:221], v[66:69]
	v_mfma_f32_16x16x32_bf16 v[118:121], v[170:173], v[186:189], v[118:121]
	v_mfma_f32_16x16x32_bf16 v[114:117], v[178:181], v[186:189], v[114:117]
	v_mfma_f32_16x16x32_bf16 v[102:105], v[170:173], v[194:197], v[102:105]
	v_mfma_f32_16x16x32_bf16 v[98:101], v[178:181], v[194:197], v[98:101]
	v_mfma_f32_16x16x32_bf16 v[86:89], v[170:173], v[202:205], v[86:89]
	v_mfma_f32_16x16x32_bf16 v[82:85], v[178:181], v[202:205], v[82:85]
	v_mfma_f32_16x16x32_bf16 v[70:73], v[170:173], v[222:225], v[70:73]
	v_mfma_f32_16x16x32_bf16 v[66:69], v[178:181], v[222:225], v[66:69]
	s_barrier
	s_add_i32 s44, s84, s66
	v_lshl_add_u64 v[226:227], v[226:227], 0, s[18:19]
	s_mov_b32 m0, s44
	ds_read_b128 v[182:185], v213 offset:49152
	ds_read_b128 v[186:189], v213 offset:50176
	ds_read_b128 v[190:193], v213 offset:51200
	ds_read_b128 v[194:197], v213 offset:52224
	ds_read_b128 v[198:201], v213 offset:53248
	ds_read_b128 v[202:205], v213 offset:54272
	ds_read_b128 v[218:221], v213 offset:55296
	ds_read_b128 v[222:225], v213 offset:56320
	global_load_lds_dwordx4 v[226:227], off
	s_add_i32 m0, s44, 0x2000
	s_add_u32 s42, s42, 0x80080
	v_lshl_add_u64 v[226:227], v[228:229], 0, s[18:19]
	s_addc_u32 s43, s43, 0
	s_add_i32 s44, s85, s66
	global_load_lds_dwordx4 v[226:227], off
	s_mov_b32 m0, s44
	s_nop 0
	global_load_lds_dwordx4 v132, s[42:43]
	s_add_i32 m0, s44, 0x2000
	s_nop 0
	global_load_lds_dwordx4 v136, s[42:43]
	v_lshl_add_u64 v[226:227], v[230:231], 0, s[18:19]
	s_mov_b32 m0, s74
	s_nop 0
	global_load_lds_dwordx4 v[226:227], off
	v_lshl_add_u64 v[226:227], v[232:233], 0, s[18:19]
	s_mov_b32 m0, s75
	s_nop 0
	global_load_lds_dwordx4 v[226:227], off
	s_waitcnt vmcnt(8)
	s_waitcnt lgkmcnt(0)
	s_barrier
	v_mfma_f32_16x16x32_bf16 v[62:65], v[150:153], v[182:185], v[62:65]
	v_mfma_f32_16x16x32_bf16 v[58:61], v[158:161], v[182:185], v[58:61]
	v_mfma_f32_16x16x32_bf16 v[46:49], v[150:153], v[190:193], v[46:49]
	v_mfma_f32_16x16x32_bf16 v[42:45], v[158:161], v[190:193], v[42:45]
	v_mfma_f32_16x16x32_bf16 v[30:33], v[150:153], v[198:201], v[30:33]
	v_mfma_f32_16x16x32_bf16 v[26:29], v[158:161], v[198:201], v[26:29]
	v_mfma_f32_16x16x32_bf16 v[14:17], v[150:153], v[218:221], v[14:17]
	v_mfma_f32_16x16x32_bf16 v[10:13], v[158:161], v[218:221], v[10:13]
	v_mfma_f32_16x16x32_bf16 v[62:65], v[154:157], v[186:189], v[62:65]
	v_mfma_f32_16x16x32_bf16 v[58:61], v[162:165], v[186:189], v[58:61]
	v_mfma_f32_16x16x32_bf16 v[46:49], v[154:157], v[194:197], v[46:49]
	v_mfma_f32_16x16x32_bf16 v[42:45], v[162:165], v[194:197], v[42:45]
	v_mfma_f32_16x16x32_bf16 v[30:33], v[154:157], v[202:205], v[30:33]
	v_mfma_f32_16x16x32_bf16 v[26:29], v[162:165], v[202:205], v[26:29]
	v_mfma_f32_16x16x32_bf16 v[14:17], v[154:157], v[222:225], v[14:17]
	v_mfma_f32_16x16x32_bf16 v[10:13], v[162:165], v[222:225], v[10:13]
	v_mfma_f32_16x16x32_bf16 v[54:57], v[166:169], v[182:185], v[54:57]
	v_mfma_f32_16x16x32_bf16 v[50:53], v[174:177], v[182:185], v[50:53]
	v_mfma_f32_16x16x32_bf16 v[38:41], v[166:169], v[190:193], v[38:41]
	v_mfma_f32_16x16x32_bf16 v[34:37], v[174:177], v[190:193], v[34:37]
	v_mfma_f32_16x16x32_bf16 v[22:25], v[166:169], v[198:201], v[22:25]
	v_mfma_f32_16x16x32_bf16 v[18:21], v[174:177], v[198:201], v[18:21]
	v_mfma_f32_16x16x32_bf16 v[6:9], v[166:169], v[218:221], v[6:9]
	v_mfma_f32_16x16x32_bf16 v[2:5], v[174:177], v[218:221], v[2:5]
	v_mfma_f32_16x16x32_bf16 v[54:57], v[170:173], v[186:189], v[54:57]
	v_mfma_f32_16x16x32_bf16 v[50:53], v[178:181], v[186:189], v[50:53]
	v_mfma_f32_16x16x32_bf16 v[38:41], v[170:173], v[194:197], v[38:41]
	v_mfma_f32_16x16x32_bf16 v[34:37], v[178:181], v[194:197], v[34:37]
	v_mfma_f32_16x16x32_bf16 v[22:25], v[170:173], v[202:205], v[22:25]
	v_mfma_f32_16x16x32_bf16 v[18:21], v[178:181], v[202:205], v[18:21]
	v_mfma_f32_16x16x32_bf16 v[6:9], v[170:173], v[222:225], v[6:9]
	v_mfma_f32_16x16x32_bf16 v[2:5], v[178:181], v[222:225], v[2:5]
	s_barrier
	s_add_i32 s83, s83, 2
	s_add_u32 s36, s36, 0x100
	s_addc_u32 s37, s37, 0
	s_add_u32 s62, s62, 0x100
	s_addc_u32 s63, s63, 0
	s_cmp_gt_u32 s83, 29
	s_cbranch_scc0 .LBB0_466
	s_setprio 0
	s_and_b64 vcc, exec, s[20:21]
	s_cbranch_vccz .LBB0_469
	s_barrier

.LBB0_573:
	s_ashr_i32 s15, s14, 31
	s_lshl_b64 s[16:17], s[14:15], 20
	s_add_u32 s16, s28, s16
	s_addc_u32 s17, s29, s17
	s_and_b64 s[18:19], s[4:5], exec
	s_cselect_b32 s15, s17, s23
	s_cselect_b32 s65, s16, s22
	s_ashr_i32 s13, s12, 31
	s_lshl_b64 s[18:19], s[12:13], 20
	s_add_u32 s18, s30, s18
	s_addc_u32 s19, s31, s19
	s_and_b64 s[26:27], s[4:5], exec
	s_cselect_b32 s13, s19, s25
	s_cselect_b32 s66, s18, s24
	s_add_u32 s22, s22, 0x80080
	s_addc_u32 s23, s23, 0
	s_add_u32 s67, s24, 0x100
	v_mov_b32_e32 v2, 0
	s_addc_u32 s68, s25, 0
	s_mov_b32 s69, -2
	v_mov_b32_e32 v3, v2
	v_mov_b32_e32 v4, v2
	v_mov_b32_e32 v5, v2
	v_mov_b32_e32 v6, v2
	v_mov_b32_e32 v7, v2
	v_mov_b32_e32 v8, v2
	v_mov_b32_e32 v9, v2
	v_mov_b32_e32 v18, v2
	v_mov_b32_e32 v19, v2
	v_mov_b32_e32 v20, v2
	v_mov_b32_e32 v21, v2
	v_mov_b32_e32 v22, v2
	v_mov_b32_e32 v23, v2
	v_mov_b32_e32 v24, v2
	v_mov_b32_e32 v25, v2
	v_mov_b32_e32 v34, v2
	v_mov_b32_e32 v35, v2
	v_mov_b32_e32 v36, v2
	v_mov_b32_e32 v37, v2
	v_mov_b32_e32 v38, v2
	v_mov_b32_e32 v39, v2
	v_mov_b32_e32 v40, v2
	v_mov_b32_e32 v41, v2
	v_mov_b32_e32 v50, v2
	v_mov_b32_e32 v51, v2
	v_mov_b32_e32 v52, v2
	v_mov_b32_e32 v53, v2
	v_mov_b32_e32 v54, v2
	v_mov_b32_e32 v55, v2
	v_mov_b32_e32 v56, v2
	v_mov_b32_e32 v57, v2
	v_mov_b32_e32 v10, v2
	v_mov_b32_e32 v11, v2
	v_mov_b32_e32 v12, v2
	v_mov_b32_e32 v13, v2
	v_mov_b32_e32 v14, v2
	v_mov_b32_e32 v15, v2
	v_mov_b32_e32 v16, v2
	v_mov_b32_e32 v17, v2
	v_mov_b32_e32 v26, v2
	v_mov_b32_e32 v27, v2
	v_mov_b32_e32 v28, v2
	v_mov_b32_e32 v29, v2
	v_mov_b32_e32 v30, v2
	v_mov_b32_e32 v31, v2
	v_mov_b32_e32 v32, v2
	v_mov_b32_e32 v33, v2
	v_mov_b32_e32 v42, v2
	v_mov_b32_e32 v43, v2
	v_mov_b32_e32 v44, v2
	v_mov_b32_e32 v45, v2
	v_mov_b32_e32 v46, v2
	v_mov_b32_e32 v47, v2
	v_mov_b32_e32 v48, v2
	v_mov_b32_e32 v49, v2
	v_mov_b32_e32 v58, v2
	v_mov_b32_e32 v59, v2
	v_mov_b32_e32 v60, v2
	v_mov_b32_e32 v61, v2
	v_mov_b32_e32 v62, v2
	v_mov_b32_e32 v63, v2
	v_mov_b32_e32 v64, v2
	v_mov_b32_e32 v65, v2
	v_mov_b32_e32 v66, v2
	v_mov_b32_e32 v67, v2
	v_mov_b32_e32 v68, v2
	v_mov_b32_e32 v69, v2
	v_mov_b32_e32 v70, v2
	v_mov_b32_e32 v71, v2
	v_mov_b32_e32 v72, v2
	v_mov_b32_e32 v73, v2
	v_mov_b32_e32 v82, v2
	v_mov_b32_e32 v83, v2
	v_mov_b32_e32 v84, v2
	v_mov_b32_e32 v85, v2
	v_mov_b32_e32 v86, v2
	v_mov_b32_e32 v87, v2
	v_mov_b32_e32 v88, v2
	v_mov_b32_e32 v89, v2
	v_mov_b32_e32 v98, v2
	v_mov_b32_e32 v99, v2
	v_mov_b32_e32 v100, v2
	v_mov_b32_e32 v101, v2
	v_mov_b32_e32 v102, v2
	v_mov_b32_e32 v103, v2
	v_mov_b32_e32 v104, v2
	v_mov_b32_e32 v105, v2
	v_mov_b32_e32 v114, v2
	v_mov_b32_e32 v115, v2
	v_mov_b32_e32 v116, v2
	v_mov_b32_e32 v117, v2
	v_mov_b32_e32 v118, v2
	v_mov_b32_e32 v119, v2
	v_mov_b32_e32 v120, v2
	v_mov_b32_e32 v121, v2
	v_mov_b32_e32 v74, v2
	v_mov_b32_e32 v75, v2
	v_mov_b32_e32 v76, v2
	v_mov_b32_e32 v77, v2
	v_mov_b32_e32 v78, v2
	v_mov_b32_e32 v79, v2
	v_mov_b32_e32 v80, v2
	v_mov_b32_e32 v81, v2
	v_mov_b32_e32 v90, v2
	v_mov_b32_e32 v91, v2
	v_mov_b32_e32 v92, v2
	v_mov_b32_e32 v93, v2
	v_mov_b32_e32 v94, v2
	v_mov_b32_e32 v95, v2
	v_mov_b32_e32 v96, v2
	v_mov_b32_e32 v97, v2
	v_mov_b32_e32 v106, v2
	v_mov_b32_e32 v107, v2
	v_mov_b32_e32 v108, v2
	v_mov_b32_e32 v109, v2
	v_mov_b32_e32 v110, v2
	v_mov_b32_e32 v111, v2
	v_mov_b32_e32 v112, v2
	v_mov_b32_e32 v113, v2
	v_mov_b32_e32 v122, v2
	v_mov_b32_e32 v123, v2
	v_mov_b32_e32 v124, v2
	v_mov_b32_e32 v125, v2
	v_mov_b32_e32 v126, v2
	v_mov_b32_e32 v127, v2
	v_mov_b32_e32 v128, v2
	v_mov_b32_e32 v129, v2
	s_mov_b64 vcc, s[10:11]
	s_cbranch_vccnz .Lsp_574
	s_setprio 1
.Lsp_574:
.LBB0_574:
	ds_read_b128 v[146:149], v152
	ds_read_b128 v[156:159], v152 offset:1024
	ds_read_b128 v[160:163], v152 offset:2048
	ds_read_b128 v[164:167], v152 offset:3072
	ds_read_b128 v[168:171], v153
	ds_read_b128 v[172:175], v153 offset:1024
	ds_read_b128 v[176:179], v153 offset:2048
	ds_read_b128 v[180:183], v153 offset:3072
	s_add_u32 s24, s22, 0xfff80080
	s_addc_u32 s25, s23, -1
	s_cmp_eq_u32 s69, 28
	s_cselect_b32 s27, s15, s25
	s_cselect_b32 s26, s65, s24
	s_cselect_b32 s25, s13, s68
	s_cselect_b32 s24, s66, s67
	s_add_i32 m0, s21, 0xc000
	ds_read_b128 v[184:187], v154
	ds_read_b128 v[188:191], v154 offset:1024
	ds_read_b128 v[192:195], v154 offset:2048
	ds_read_b128 v[196:199], v154 offset:3072
	ds_read_b128 v[200:203], v154 offset:4096
	ds_read_b128 v[204:207], v154 offset:5120
	ds_read_b128 v[208:211], v154 offset:6144
	ds_read_b128 v[212:215], v154 offset:7168
	global_load_lds_dwordx4 v138, s[22:23]
	s_add_i32 m0, s21, 0xe000
	s_nop 0
	global_load_lds_dwordx4 v140, s[22:23]
	s_waitcnt vmcnt(8)
	s_waitcnt lgkmcnt(0)
	s_barrier
	v_mfma_f32_16x16x32_bf16 v[126:129], v[146:149], v[184:187], v[126:129]
	v_mfma_f32_16x16x32_bf16 v[122:125], v[160:163], v[184:187], v[122:125]
	v_mfma_f32_16x16x32_bf16 v[110:113], v[146:149], v[192:195], v[110:113]
	v_mfma_f32_16x16x32_bf16 v[106:109], v[160:163], v[192:195], v[106:109]
	v_mfma_f32_16x16x32_bf16 v[94:97], v[146:149], v[200:203], v[94:97]
	v_mfma_f32_16x16x32_bf16 v[90:93], v[160:163], v[200:203], v[90:93]
	v_mfma_f32_16x16x32_bf16 v[78:81], v[146:149], v[208:211], v[78:81]
	v_mfma_f32_16x16x32_bf16 v[74:77], v[160:163], v[208:211], v[74:77]
	v_mfma_f32_16x16x32_bf16 v[126:129], v[156:159], v[188:191], v[126:129]
	v_mfma_f32_16x16x32_bf16 v[122:125], v[164:167], v[188:191], v[122:125]
	v_mfma_f32_16x16x32_bf16 v[110:113], v[156:159], v[196:199], v[110:113]
	v_mfma_f32_16x16x32_bf16 v[106:109], v[164:167], v[196:199], v[106:109]
	v_mfma_f32_16x16x32_bf16 v[94:97], v[156:159], v[204:207], v[94:97]
	v_mfma_f32_16x16x32_bf16 v[90:93], v[164:167], v[204:207], v[90:93]
	v_mfma_f32_16x16x32_bf16 v[78:81], v[156:159], v[212:215], v[78:81]
	v_mfma_f32_16x16x32_bf16 v[74:77], v[164:167], v[212:215], v[74:77]
	v_mfma_f32_16x16x32_bf16 v[118:121], v[168:171], v[184:187], v[118:121]
	v_mfma_f32_16x16x32_bf16 v[114:117], v[176:179], v[184:187], v[114:117]
	v_mfma_f32_16x16x32_bf16 v[102:105], v[168:171], v[192:195], v[102:105]
	v_mfma_f32_16x16x32_bf16 v[98:101], v[176:179], v[192:195], v[98:101]
	v_mfma_f32_16x16x32_bf16 v[86:89], v[168:171], v[200:203], v[86:89]
	v_mfma_f32_16x16x32_bf16 v[82:85], v[176:179], v[200:203], v[82:85]
	v_mfma_f32_16x16x32_bf16 v[70:73], v[168:171], v[208:211], v[70:73]
	v_mfma_f32_16x16x32_bf16 v[66:69], v[176:179], v[208:211], v[66:69]
	v_mfma_f32_16x16x32_bf16 v[118:121], v[172:175], v[188:191], v[118:121]
	v_mfma_f32_16x16x32_bf16 v[114:117], v[180:183], v[188:191], v[114:117]
	v_mfma_f32_16x16x32_bf16 v[102:105], v[172:175], v[196:199], v[102:105]
	v_mfma_f32_16x16x32_bf16 v[98:101], v[180:183], v[196:199], v[98:101]
	v_mfma_f32_16x16x32_bf16 v[86:89], v[172:175], v[204:207], v[86:89]
	v_mfma_f32_16x16x32_bf16 v[82:85], v[180:183], v[204:207], v[82:85]
	v_mfma_f32_16x16x32_bf16 v[70:73], v[172:175], v[212:215], v[70:73]
	v_mfma_f32_16x16x32_bf16 v[66:69], v[180:183], v[212:215], v[66:69]
	s_barrier
	s_add_i32 s70, s61, s33
	v_lshl_add_u64 v[216:217], s[24:25], 0, v[134:135]
	s_mov_b32 m0, s70
	ds_read_b128 v[184:187], v154 offset:16384
	ds_read_b128 v[188:191], v154 offset:17408
	ds_read_b128 v[192:195], v154 offset:18432
	ds_read_b128 v[196:199], v154 offset:19456
	ds_read_b128 v[200:203], v154 offset:20480
	ds_read_b128 v[204:207], v154 offset:21504
	ds_read_b128 v[208:211], v154 offset:22528
	ds_read_b128 v[212:215], v154 offset:23552
	global_load_lds_dwordx4 v134, s[24:25]
	s_add_i32 m0, s70, 0x2000
	s_add_u32 s70, s24, 0x80000
	v_lshl_add_u64 v[218:219], s[24:25], 0, v[130:131]
	s_addc_u32 s71, s25, 0
	s_add_i32 s72, s62, s33
	global_load_lds_dwordx4 v130, s[24:25]
	s_mov_b32 m0, s72
	v_lshl_add_u64 v[222:223], s[26:27], 0, v[132:133]
	global_load_lds_dwordx4 v134, s[70:71]
	s_add_i32 m0, s72, 0x2000
	s_nop 0
	global_load_lds_dwordx4 v130, s[70:71]
	v_lshl_add_u64 v[220:221], s[26:27], 0, v[136:137]
	s_mov_b32 m0, s21
	s_nop 0
	global_load_lds_dwordx4 v136, s[26:27]
	s_mov_b32 m0, s36
	s_nop 0
	global_load_lds_dwordx4 v132, s[26:27]
	s_waitcnt vmcnt(8)
	s_waitcnt lgkmcnt(0)
	s_barrier
	v_mfma_f32_16x16x32_bf16 v[62:65], v[146:149], v[184:187], v[62:65]
	v_mfma_f32_16x16x32_bf16 v[58:61], v[160:163], v[184:187], v[58:61]
	v_mfma_f32_16x16x32_bf16 v[46:49], v[146:149], v[192:195], v[46:49]
	v_mfma_f32_16x16x32_bf16 v[42:45], v[160:163], v[192:195], v[42:45]
	v_mfma_f32_16x16x32_bf16 v[30:33], v[146:149], v[200:203], v[30:33]
	v_mfma_f32_16x16x32_bf16 v[26:29], v[160:163], v[200:203], v[26:29]
	v_mfma_f32_16x16x32_bf16 v[14:17], v[146:149], v[208:211], v[14:17]
	v_mfma_f32_16x16x32_bf16 v[10:13], v[160:163], v[208:211], v[10:13]
	v_mfma_f32_16x16x32_bf16 v[62:65], v[156:159], v[188:191], v[62:65]
	v_mfma_f32_16x16x32_bf16 v[58:61], v[164:167], v[188:191], v[58:61]
	v_mfma_f32_16x16x32_bf16 v[46:49], v[156:159], v[196:199], v[46:49]
	v_mfma_f32_16x16x32_bf16 v[42:45], v[164:167], v[196:199], v[42:45]
	v_mfma_f32_16x16x32_bf16 v[30:33], v[156:159], v[204:207], v[30:33]
	v_mfma_f32_16x16x32_bf16 v[26:29], v[164:167], v[204:207], v[26:29]
	v_mfma_f32_16x16x32_bf16 v[14:17], v[156:159], v[212:215], v[14:17]
	v_mfma_f32_16x16x32_bf16 v[10:13], v[164:167], v[212:215], v[10:13]
	v_mfma_f32_16x16x32_bf16 v[54:57], v[168:171], v[184:187], v[54:57]
	v_mfma_f32_16x16x32_bf16 v[50:53], v[176:179], v[184:187], v[50:53]
	v_mfma_f32_16x16x32_bf16 v[38:41], v[168:171], v[192:195], v[38:41]
	v_mfma_f32_16x16x32_bf16 v[34:37], v[176:179], v[192:195], v[34:37]
	v_mfma_f32_16x16x32_bf16 v[22:25], v[168:171], v[200:203], v[22:25]
	v_mfma_f32_16x16x32_bf16 v[18:21], v[176:179], v[200:203], v[18:21]
	v_mfma_f32_16x16x32_bf16 v[6:9], v[168:171], v[208:211], v[6:9]
	v_mfma_f32_16x16x32_bf16 v[2:5], v[176:179], v[208:211], v[2:5]
	v_mfma_f32_16x16x32_bf16 v[54:57], v[172:175], v[188:191], v[54:57]
	v_mfma_f32_16x16x32_bf16 v[50:53], v[180:183], v[188:191], v[50:53]
	v_mfma_f32_16x16x32_bf16 v[38:41], v[172:175], v[196:199], v[38:41]
	v_mfma_f32_16x16x32_bf16 v[34:37], v[180:183], v[196:199], v[34:37]
	v_mfma_f32_16x16x32_bf16 v[22:25], v[172:175], v[204:207], v[22:25]
	v_mfma_f32_16x16x32_bf16 v[18:21], v[180:183], v[204:207], v[18:21]
	v_mfma_f32_16x16x32_bf16 v[6:9], v[172:175], v[212:215], v[6:9]
	v_mfma_f32_16x16x32_bf16 v[2:5], v[180:183], v[212:215], v[2:5]
	s_barrier
	s_add_i32 s70, 0, 0x18000
	v_add_u32_e32 v155, s70, v150
	s_add_i32 s71, 0, 0x1c000
	ds_read_b128 v[146:149], v155
	ds_read_b128 v[156:159], v155 offset:1024
	ds_read_b128 v[160:163], v155 offset:2048
	ds_read_b128 v[164:167], v155 offset:3072
	v_add_u32_e32 v155, s71, v150
	ds_read_b128 v[168:171], v155
	ds_read_b128 v[172:175], v155 offset:1024
	ds_read_b128 v[176:179], v155 offset:2048
	ds_read_b128 v[180:183], v155 offset:3072
	s_add_u32 s26, s26, 0x80000
	s_addc_u32 s27, s27, 0
	s_mov_b32 m0, s37
	ds_read_b128 v[184:187], v154 offset:32768
	ds_read_b128 v[188:191], v154 offset:33792
	ds_read_b128 v[192:195], v154 offset:34816
	ds_read_b128 v[196:199], v154 offset:35840
	ds_read_b128 v[200:203], v154 offset:36864
	ds_read_b128 v[204:207], v154 offset:37888
	ds_read_b128 v[208:211], v154 offset:38912
	ds_read_b128 v[212:215], v154 offset:39936
	global_load_lds_dwordx4 v136, s[26:27]
	s_mov_b32 m0, s42
	s_nop 0
	global_load_lds_dwordx4 v132, s[26:27]
	s_waitcnt vmcnt(8)
	s_waitcnt lgkmcnt(0)
	s_barrier
	v_mfma_f32_16x16x32_bf16 v[126:129], v[146:149], v[184:187], v[126:129]
	v_mfma_f32_16x16x32_bf16 v[122:125], v[160:163], v[184:187], v[122:125]
	v_mfma_f32_16x16x32_bf16 v[110:113], v[146:149], v[192:195], v[110:113]
	v_mfma_f32_16x16x32_bf16 v[106:109], v[160:163], v[192:195], v[106:109]
	v_mfma_f32_16x16x32_bf16 v[94:97], v[146:149], v[200:203], v[94:97]
	v_mfma_f32_16x16x32_bf16 v[90:93], v[160:163], v[200:203], v[90:93]
	v_mfma_f32_16x16x32_bf16 v[78:81], v[146:149], v[208:211], v[78:81]
	v_mfma_f32_16x16x32_bf16 v[74:77], v[160:163], v[208:211], v[74:77]
	v_mfma_f32_16x16x32_bf16 v[126:129], v[156:159], v[188:191], v[126:129]
	v_mfma_f32_16x16x32_bf16 v[122:125], v[164:167], v[188:191], v[122:125]
	v_mfma_f32_16x16x32_bf16 v[110:113], v[156:159], v[196:199], v[110:113]
	v_mfma_f32_16x16x32_bf16 v[106:109], v[164:167], v[196:199], v[106:109]
	v_mfma_f32_16x16x32_bf16 v[94:97], v[156:159], v[204:207], v[94:97]
	v_mfma_f32_16x16x32_bf16 v[90:93], v[164:167], v[204:207], v[90:93]
	v_mfma_f32_16x16x32_bf16 v[78:81], v[156:159], v[212:215], v[78:81]
	v_mfma_f32_16x16x32_bf16 v[74:77], v[164:167], v[212:215], v[74:77]
	v_mfma_f32_16x16x32_bf16 v[118:121], v[168:171], v[184:187], v[118:121]
	v_mfma_f32_16x16x32_bf16 v[114:117], v[176:179], v[184:187], v[114:117]
	v_mfma_f32_16x16x32_bf16 v[102:105], v[168:171], v[192:195], v[102:105]
	v_mfma_f32_16x16x32_bf16 v[98:101], v[176:179], v[192:195], v[98:101]
	v_mfma_f32_16x16x32_bf16 v[86:89], v[168:171], v[200:203], v[86:89]
	v_mfma_f32_16x16x32_bf16 v[82:85], v[176:179], v[200:203], v[82:85]
	v_mfma_f32_16x16x32_bf16 v[70:73], v[168:171], v[208:211], v[70:73]
	v_mfma_f32_16x16x32_bf16 v[66:69], v[176:179], v[208:211], v[66:69]
	v_mfma_f32_16x16x32_bf16 v[118:121], v[172:175], v[188:191], v[118:121]
	v_mfma_f32_16x16x32_bf16 v[114:117], v[180:183], v[188:191], v[114:117]
	v_mfma_f32_16x16x32_bf16 v[102:105], v[172:175], v[196:199], v[102:105]
	v_mfma_f32_16x16x32_bf16 v[98:101], v[180:183], v[196:199], v[98:101]
	v_mfma_f32_16x16x32_bf16 v[86:89], v[172:175], v[204:207], v[86:89]
	v_mfma_f32_16x16x32_bf16 v[82:85], v[180:183], v[204:207], v[82:85]
	v_mfma_f32_16x16x32_bf16 v[70:73], v[172:175], v[212:215], v[70:73]
	v_mfma_f32_16x16x32_bf16 v[66:69], v[180:183], v[212:215], v[66:69]
	s_barrier
	s_add_i32 s26, s70, s33
	v_lshl_add_u64 v[216:217], v[216:217], 0, s[8:9]
	s_mov_b32 m0, s26
	ds_read_b128 v[184:187], v154 offset:49152
	ds_read_b128 v[188:191], v154 offset:50176
	ds_read_b128 v[192:195], v154 offset:51200
	ds_read_b128 v[196:199], v154 offset:52224
	ds_read_b128 v[200:203], v154 offset:53248
	ds_read_b128 v[204:207], v154 offset:54272
	ds_read_b128 v[208:211], v154 offset:55296
	ds_read_b128 v[212:215], v154 offset:56320
	global_load_lds_dwordx4 v[216:217], off
	s_add_i32 m0, s26, 0x2000
	s_add_u32 s24, s24, 0x80080
	v_lshl_add_u64 v[216:217], v[218:219], 0, s[8:9]
	s_addc_u32 s25, s25, 0
	s_add_i32 s26, s71, s33
	global_load_lds_dwordx4 v[216:217], off
	s_mov_b32 m0, s26
	s_nop 0
	global_load_lds_dwordx4 v134, s[24:25]
	s_add_i32 m0, s26, 0x2000
	s_nop 0
	global_load_lds_dwordx4 v130, s[24:25]
	v_lshl_add_u64 v[216:217], v[220:221], 0, s[8:9]
	s_mov_b32 m0, s44
	s_nop 0
	global_load_lds_dwordx4 v[216:217], off
	v_lshl_add_u64 v[216:217], v[222:223], 0, s[8:9]
	s_mov_b32 m0, s45
	s_nop 0
	global_load_lds_dwordx4 v[216:217], off
	s_waitcnt vmcnt(8)
	s_waitcnt lgkmcnt(0)
	s_barrier
	v_mfma_f32_16x16x32_bf16 v[62:65], v[146:149], v[184:187], v[62:65]
	v_mfma_f32_16x16x32_bf16 v[58:61], v[160:163], v[184:187], v[58:61]
	v_mfma_f32_16x16x32_bf16 v[46:49], v[146:149], v[192:195], v[46:49]
	v_mfma_f32_16x16x32_bf16 v[42:45], v[160:163], v[192:195], v[42:45]
	v_mfma_f32_16x16x32_bf16 v[30:33], v[146:149], v[200:203], v[30:33]
	v_mfma_f32_16x16x32_bf16 v[26:29], v[160:163], v[200:203], v[26:29]
	v_mfma_f32_16x16x32_bf16 v[14:17], v[146:149], v[208:211], v[14:17]
	v_mfma_f32_16x16x32_bf16 v[10:13], v[160:163], v[208:211], v[10:13]
	v_mfma_f32_16x16x32_bf16 v[62:65], v[156:159], v[188:191], v[62:65]
	v_mfma_f32_16x16x32_bf16 v[58:61], v[164:167], v[188:191], v[58:61]
	v_mfma_f32_16x16x32_bf16 v[46:49], v[156:159], v[196:199], v[46:49]
	v_mfma_f32_16x16x32_bf16 v[42:45], v[164:167], v[196:199], v[42:45]
	v_mfma_f32_16x16x32_bf16 v[30:33], v[156:159], v[204:207], v[30:33]
	v_mfma_f32_16x16x32_bf16 v[26:29], v[164:167], v[204:207], v[26:29]
	v_mfma_f32_16x16x32_bf16 v[14:17], v[156:159], v[212:215], v[14:17]
	v_mfma_f32_16x16x32_bf16 v[10:13], v[164:167], v[212:215], v[10:13]
	v_mfma_f32_16x16x32_bf16 v[54:57], v[168:171], v[184:187], v[54:57]
	v_mfma_f32_16x16x32_bf16 v[50:53], v[176:179], v[184:187], v[50:53]
	v_mfma_f32_16x16x32_bf16 v[38:41], v[168:171], v[192:195], v[38:41]
	v_mfma_f32_16x16x32_bf16 v[34:37], v[176:179], v[192:195], v[34:37]
	v_mfma_f32_16x16x32_bf16 v[22:25], v[168:171], v[200:203], v[22:25]
	v_mfma_f32_16x16x32_bf16 v[18:21], v[176:179], v[200:203], v[18:21]
	v_mfma_f32_16x16x32_bf16 v[6:9], v[168:171], v[208:211], v[6:9]
	v_mfma_f32_16x16x32_bf16 v[2:5], v[176:179], v[208:211], v[2:5]
	v_mfma_f32_16x16x32_bf16 v[54:57], v[172:175], v[188:191], v[54:57]
	v_mfma_f32_16x16x32_bf16 v[50:53], v[180:183], v[188:191], v[50:53]
	v_mfma_f32_16x16x32_bf16 v[38:41], v[172:175], v[196:199], v[38:41]
	v_mfma_f32_16x16x32_bf16 v[34:37], v[180:183], v[196:199], v[34:37]
	v_mfma_f32_16x16x32_bf16 v[22:25], v[172:175], v[204:207], v[22:25]
	v_mfma_f32_16x16x32_bf16 v[18:21], v[180:183], v[204:207], v[18:21]
	v_mfma_f32_16x16x32_bf16 v[6:9], v[172:175], v[212:215], v[6:9]
	v_mfma_f32_16x16x32_bf16 v[2:5], v[180:183], v[212:215], v[2:5]
	s_barrier
	s_add_i32 s69, s69, 2
	s_add_u32 s22, s22, 0x100
	s_addc_u32 s23, s23, 0
	s_add_u32 s67, s67, 0x100
	s_addc_u32 s68, s68, 0
	s_cmp_gt_u32 s69, 29
	s_cbranch_scc0 .LBB0_574
	s_setprio 0
	s_and_b64 vcc, exec, s[10:11]
	s_cbranch_vccz .LBB0_577
	s_barrier

.LBB0_658:
	s_add_u32 s0, s42, 0x158080
	s_addc_u32 s1, s43, 0
	s_add_u32 s31, s36, 0x100
	v_mov_b32_e32 v2, 0
	s_addc_u32 s35, s37, 0
	s_mov_b32 s44, -2
	v_mov_b32_e32 v3, v2
	v_mov_b32_e32 v4, v2
	v_mov_b32_e32 v5, v2
	v_mov_b32_e32 v6, v2
	v_mov_b32_e32 v7, v2
	v_mov_b32_e32 v8, v2
	v_mov_b32_e32 v9, v2
	v_mov_b32_e32 v18, v2
	v_mov_b32_e32 v19, v2
	v_mov_b32_e32 v20, v2
	v_mov_b32_e32 v21, v2
	v_mov_b32_e32 v22, v2
	v_mov_b32_e32 v23, v2
	v_mov_b32_e32 v24, v2
	v_mov_b32_e32 v25, v2
	v_mov_b32_e32 v34, v2
	v_mov_b32_e32 v35, v2
	v_mov_b32_e32 v36, v2
	v_mov_b32_e32 v37, v2
	v_mov_b32_e32 v38, v2
	v_mov_b32_e32 v39, v2
	v_mov_b32_e32 v40, v2
	v_mov_b32_e32 v41, v2
	v_mov_b32_e32 v50, v2
	v_mov_b32_e32 v51, v2
	v_mov_b32_e32 v52, v2
	v_mov_b32_e32 v53, v2
	v_mov_b32_e32 v54, v2
	v_mov_b32_e32 v55, v2
	v_mov_b32_e32 v56, v2
	v_mov_b32_e32 v57, v2
	v_mov_b32_e32 v10, v2
	v_mov_b32_e32 v11, v2
	v_mov_b32_e32 v12, v2
	v_mov_b32_e32 v13, v2
	v_mov_b32_e32 v14, v2
	v_mov_b32_e32 v15, v2
	v_mov_b32_e32 v16, v2
	v_mov_b32_e32 v17, v2
	v_mov_b32_e32 v26, v2
	v_mov_b32_e32 v27, v2
	v_mov_b32_e32 v28, v2
	v_mov_b32_e32 v29, v2
	v_mov_b32_e32 v30, v2
	v_mov_b32_e32 v31, v2
	v_mov_b32_e32 v32, v2
	v_mov_b32_e32 v33, v2
	v_mov_b32_e32 v42, v2
	v_mov_b32_e32 v43, v2
	v_mov_b32_e32 v44, v2
	v_mov_b32_e32 v45, v2
	v_mov_b32_e32 v46, v2
	v_mov_b32_e32 v47, v2
	v_mov_b32_e32 v48, v2
	v_mov_b32_e32 v49, v2
	v_mov_b32_e32 v58, v2
	v_mov_b32_e32 v59, v2
	v_mov_b32_e32 v60, v2
	v_mov_b32_e32 v61, v2
	v_mov_b32_e32 v62, v2
	v_mov_b32_e32 v63, v2
	v_mov_b32_e32 v64, v2
	v_mov_b32_e32 v65, v2
	v_mov_b32_e32 v66, v2
	v_mov_b32_e32 v67, v2
	v_mov_b32_e32 v68, v2
	v_mov_b32_e32 v69, v2
	v_mov_b32_e32 v70, v2
	v_mov_b32_e32 v71, v2
	v_mov_b32_e32 v72, v2
	v_mov_b32_e32 v73, v2
	v_mov_b32_e32 v82, v2
	v_mov_b32_e32 v83, v2
	v_mov_b32_e32 v84, v2
	v_mov_b32_e32 v85, v2
	v_mov_b32_e32 v86, v2
	v_mov_b32_e32 v87, v2
	v_mov_b32_e32 v88, v2
	v_mov_b32_e32 v89, v2
	v_mov_b32_e32 v98, v2
	v_mov_b32_e32 v99, v2
	v_mov_b32_e32 v100, v2
	v_mov_b32_e32 v101, v2
	v_mov_b32_e32 v102, v2
	v_mov_b32_e32 v103, v2
	v_mov_b32_e32 v104, v2
	v_mov_b32_e32 v105, v2
	v_mov_b32_e32 v114, v2
	v_mov_b32_e32 v115, v2
	v_mov_b32_e32 v116, v2
	v_mov_b32_e32 v117, v2
	v_mov_b32_e32 v118, v2
	v_mov_b32_e32 v119, v2
	v_mov_b32_e32 v120, v2
	v_mov_b32_e32 v121, v2
	v_mov_b32_e32 v74, v2
	v_mov_b32_e32 v75, v2
	v_mov_b32_e32 v76, v2
	v_mov_b32_e32 v77, v2
	v_mov_b32_e32 v78, v2
	v_mov_b32_e32 v79, v2
	v_mov_b32_e32 v80, v2
	v_mov_b32_e32 v81, v2
	v_mov_b32_e32 v90, v2
	v_mov_b32_e32 v91, v2
	v_mov_b32_e32 v92, v2
	v_mov_b32_e32 v93, v2
	v_mov_b32_e32 v94, v2
	v_mov_b32_e32 v95, v2
	v_mov_b32_e32 v96, v2
	v_mov_b32_e32 v97, v2
	v_mov_b32_e32 v106, v2
	v_mov_b32_e32 v107, v2
	v_mov_b32_e32 v108, v2
	v_mov_b32_e32 v109, v2
	v_mov_b32_e32 v110, v2
	v_mov_b32_e32 v111, v2
	v_mov_b32_e32 v112, v2
	v_mov_b32_e32 v113, v2
	v_mov_b32_e32 v122, v2
	v_mov_b32_e32 v123, v2
	v_mov_b32_e32 v124, v2
	v_mov_b32_e32 v125, v2
	v_mov_b32_e32 v126, v2
	v_mov_b32_e32 v127, v2
	v_mov_b32_e32 v128, v2
	v_mov_b32_e32 v129, v2
	s_mov_b64 vcc, s[22:23]
	s_cbranch_vccnz .Lsp_659
	s_setprio 1
.Lsp_659:
.LBB0_659:
	ds_read_b128 v[150:153], v211
	ds_read_b128 v[154:157], v211 offset:1024
	ds_read_b128 v[158:161], v211 offset:2048
	ds_read_b128 v[162:165], v211 offset:3072
	ds_read_b128 v[166:169], v212
	ds_read_b128 v[170:173], v212 offset:1024
	ds_read_b128 v[174:177], v212 offset:2048
	ds_read_b128 v[178:181], v212 offset:3072
	s_add_u32 s36, s0, 0xffea8080
	s_addc_u32 s37, s1, -1
	s_cmpk_eq_i32 s44, 0x52
	s_cselect_b32 s43, s27, s37
	s_cselect_b32 s42, s26, s36
	s_cselect_b32 s37, s29, s35
	s_cselect_b32 s36, s28, s31
	s_add_i32 m0, s63, 0xc000
	ds_read_b128 v[182:185], v213
	ds_read_b128 v[186:189], v213 offset:1024
	ds_read_b128 v[190:193], v213 offset:2048
	ds_read_b128 v[194:197], v213 offset:3072
	ds_read_b128 v[198:201], v213 offset:4096
	ds_read_b128 v[202:205], v213 offset:5120
	ds_read_b128 v[218:221], v213 offset:6144
	ds_read_b128 v[222:225], v213 offset:7168
	global_load_lds_dwordx4 v142, s[0:1]
	s_add_i32 m0, s63, 0xe000
	s_nop 0
	global_load_lds_dwordx4 v144, s[0:1]
	s_waitcnt vmcnt(8)
	s_waitcnt lgkmcnt(0)
	s_barrier
	v_mfma_f32_16x16x32_bf16 v[126:129], v[150:153], v[182:185], v[126:129]
	v_mfma_f32_16x16x32_bf16 v[122:125], v[158:161], v[182:185], v[122:125]
	v_mfma_f32_16x16x32_bf16 v[110:113], v[150:153], v[190:193], v[110:113]
	v_mfma_f32_16x16x32_bf16 v[106:109], v[158:161], v[190:193], v[106:109]
	v_mfma_f32_16x16x32_bf16 v[94:97], v[150:153], v[198:201], v[94:97]
	v_mfma_f32_16x16x32_bf16 v[90:93], v[158:161], v[198:201], v[90:93]
	v_mfma_f32_16x16x32_bf16 v[78:81], v[150:153], v[218:221], v[78:81]
	v_mfma_f32_16x16x32_bf16 v[74:77], v[158:161], v[218:221], v[74:77]
	v_mfma_f32_16x16x32_bf16 v[126:129], v[154:157], v[186:189], v[126:129]
	v_mfma_f32_16x16x32_bf16 v[122:125], v[162:165], v[186:189], v[122:125]
	v_mfma_f32_16x16x32_bf16 v[110:113], v[154:157], v[194:197], v[110:113]
	v_mfma_f32_16x16x32_bf16 v[106:109], v[162:165], v[194:197], v[106:109]
	v_mfma_f32_16x16x32_bf16 v[94:97], v[154:157], v[202:205], v[94:97]
	v_mfma_f32_16x16x32_bf16 v[90:93], v[162:165], v[202:205], v[90:93]
	v_mfma_f32_16x16x32_bf16 v[78:81], v[154:157], v[222:225], v[78:81]
	v_mfma_f32_16x16x32_bf16 v[74:77], v[162:165], v[222:225], v[74:77]
	v_mfma_f32_16x16x32_bf16 v[118:121], v[166:169], v[182:185], v[118:121]
	v_mfma_f32_16x16x32_bf16 v[114:117], v[174:177], v[182:185], v[114:117]
	v_mfma_f32_16x16x32_bf16 v[102:105], v[166:169], v[190:193], v[102:105]
	v_mfma_f32_16x16x32_bf16 v[98:101], v[174:177], v[190:193], v[98:101]
	v_mfma_f32_16x16x32_bf16 v[86:89], v[166:169], v[198:201], v[86:89]
	v_mfma_f32_16x16x32_bf16 v[82:85], v[174:177], v[198:201], v[82:85]
	v_mfma_f32_16x16x32_bf16 v[70:73], v[166:169], v[218:221], v[70:73]
	v_mfma_f32_16x16x32_bf16 v[66:69], v[174:177], v[218:221], v[66:69]
	v_mfma_f32_16x16x32_bf16 v[118:121], v[170:173], v[186:189], v[118:121]
	v_mfma_f32_16x16x32_bf16 v[114:117], v[178:181], v[186:189], v[114:117]
	v_mfma_f32_16x16x32_bf16 v[102:105], v[170:173], v[194:197], v[102:105]
	v_mfma_f32_16x16x32_bf16 v[98:101], v[178:181], v[194:197], v[98:101]
	v_mfma_f32_16x16x32_bf16 v[86:89], v[170:173], v[202:205], v[86:89]
	v_mfma_f32_16x16x32_bf16 v[82:85], v[178:181], v[202:205], v[82:85]
	v_mfma_f32_16x16x32_bf16 v[70:73], v[170:173], v[222:225], v[70:73]
	v_mfma_f32_16x16x32_bf16 v[66:69], v[178:181], v[222:225], v[66:69]
	s_barrier
	s_add_i32 s45, s75, s62
	v_lshl_add_u64 v[226:227], s[36:37], 0, v[132:133]
	s_mov_b32 m0, s45
	ds_read_b128 v[182:185], v213 offset:16384
	ds_read_b128 v[186:189], v213 offset:17408
	ds_read_b128 v[190:193], v213 offset:18432
	ds_read_b128 v[194:197], v213 offset:19456
	ds_read_b128 v[198:201], v213 offset:20480
	ds_read_b128 v[202:205], v213 offset:21504
	ds_read_b128 v[218:221], v213 offset:22528
	ds_read_b128 v[222:225], v213 offset:23552
	global_load_lds_dwordx4 v132, s[36:37]
	s_add_i32 m0, s45, 0x2000
	s_add_u32 s82, s36, 0x158000
	v_lshl_add_u64 v[228:229], s[36:37], 0, v[136:137]
	s_addc_u32 s83, s37, 0
	s_add_i32 s45, s76, s62
	global_load_lds_dwordx4 v136, s[36:37]
	s_mov_b32 m0, s45
	v_lshl_add_u64 v[232:233], s[42:43], 0, v[134:135]
	global_load_lds_dwordx4 v132, s[82:83]
	s_add_i32 m0, s45, 0x2000
	s_nop 0
	global_load_lds_dwordx4 v136, s[82:83]
	v_lshl_add_u64 v[230:231], s[42:43], 0, v[130:131]
	s_mov_b32 m0, s63
	s_nop 0
	global_load_lds_dwordx4 v130, s[42:43]
	s_mov_b32 m0, s64
	s_nop 0
	global_load_lds_dwordx4 v134, s[42:43]
	s_waitcnt vmcnt(8)
	s_waitcnt lgkmcnt(0)
	s_barrier
	v_mfma_f32_16x16x32_bf16 v[62:65], v[150:153], v[182:185], v[62:65]
	v_mfma_f32_16x16x32_bf16 v[58:61], v[158:161], v[182:185], v[58:61]
	v_mfma_f32_16x16x32_bf16 v[46:49], v[150:153], v[190:193], v[46:49]
	v_mfma_f32_16x16x32_bf16 v[42:45], v[158:161], v[190:193], v[42:45]
	v_mfma_f32_16x16x32_bf16 v[30:33], v[150:153], v[198:201], v[30:33]
	v_mfma_f32_16x16x32_bf16 v[26:29], v[158:161], v[198:201], v[26:29]
	v_mfma_f32_16x16x32_bf16 v[14:17], v[150:153], v[218:221], v[14:17]
	v_mfma_f32_16x16x32_bf16 v[10:13], v[158:161], v[218:221], v[10:13]
	v_mfma_f32_16x16x32_bf16 v[62:65], v[154:157], v[186:189], v[62:65]
	v_mfma_f32_16x16x32_bf16 v[58:61], v[162:165], v[186:189], v[58:61]
	v_mfma_f32_16x16x32_bf16 v[46:49], v[154:157], v[194:197], v[46:49]
	v_mfma_f32_16x16x32_bf16 v[42:45], v[162:165], v[194:197], v[42:45]
	v_mfma_f32_16x16x32_bf16 v[30:33], v[154:157], v[202:205], v[30:33]
	v_mfma_f32_16x16x32_bf16 v[26:29], v[162:165], v[202:205], v[26:29]
	v_mfma_f32_16x16x32_bf16 v[14:17], v[154:157], v[222:225], v[14:17]
	v_mfma_f32_16x16x32_bf16 v[10:13], v[162:165], v[222:225], v[10:13]
	v_mfma_f32_16x16x32_bf16 v[54:57], v[166:169], v[182:185], v[54:57]
	v_mfma_f32_16x16x32_bf16 v[50:53], v[174:177], v[182:185], v[50:53]
	v_mfma_f32_16x16x32_bf16 v[38:41], v[166:169], v[190:193], v[38:41]
	v_mfma_f32_16x16x32_bf16 v[34:37], v[174:177], v[190:193], v[34:37]
	v_mfma_f32_16x16x32_bf16 v[22:25], v[166:169], v[198:201], v[22:25]
	v_mfma_f32_16x16x32_bf16 v[18:21], v[174:177], v[198:201], v[18:21]
	v_mfma_f32_16x16x32_bf16 v[6:9], v[166:169], v[218:221], v[6:9]
	v_mfma_f32_16x16x32_bf16 v[2:5], v[174:177], v[218:221], v[2:5]
	v_mfma_f32_16x16x32_bf16 v[54:57], v[170:173], v[186:189], v[54:57]
	v_mfma_f32_16x16x32_bf16 v[50:53], v[178:181], v[186:189], v[50:53]
	v_mfma_f32_16x16x32_bf16 v[38:41], v[170:173], v[194:197], v[38:41]
	v_mfma_f32_16x16x32_bf16 v[34:37], v[178:181], v[194:197], v[34:37]
	v_mfma_f32_16x16x32_bf16 v[22:25], v[170:173], v[202:205], v[22:25]
	v_mfma_f32_16x16x32_bf16 v[18:21], v[178:181], v[202:205], v[18:21]
	v_mfma_f32_16x16x32_bf16 v[6:9], v[170:173], v[222:225], v[6:9]
	v_mfma_f32_16x16x32_bf16 v[2:5], v[178:181], v[222:225], v[2:5]
	s_barrier
	s_add_i32 s45, 0, 0x18000
	v_add_u32_e32 v139, s45, v206
	s_add_i32 s81, 0, 0x1c000
	ds_read_b128 v[150:153], v139
	ds_read_b128 v[154:157], v139 offset:1024
	ds_read_b128 v[158:161], v139 offset:2048
	ds_read_b128 v[162:165], v139 offset:3072
	v_add_u32_e32 v139, s81, v206
	ds_read_b128 v[166:169], v139
	ds_read_b128 v[170:173], v139 offset:1024
	ds_read_b128 v[174:177], v139 offset:2048
	ds_read_b128 v[178:181], v139 offset:3072
	s_add_u32 s42, s42, 0x158000
	s_addc_u32 s43, s43, 0
	s_mov_b32 m0, s65
	ds_read_b128 v[182:185], v213 offset:32768
	ds_read_b128 v[186:189], v213 offset:33792
	ds_read_b128 v[190:193], v213 offset:34816
	ds_read_b128 v[194:197], v213 offset:35840
	ds_read_b128 v[198:201], v213 offset:36864
	ds_read_b128 v[202:205], v213 offset:37888
	ds_read_b128 v[218:221], v213 offset:38912
	ds_read_b128 v[222:225], v213 offset:39936
	global_load_lds_dwordx4 v130, s[42:43]
	s_mov_b32 m0, s66
	s_nop 0
	global_load_lds_dwordx4 v134, s[42:43]
	s_waitcnt vmcnt(8)
	s_waitcnt lgkmcnt(0)
	s_barrier
	v_mfma_f32_16x16x32_bf16 v[126:129], v[150:153], v[182:185], v[126:129]
	v_mfma_f32_16x16x32_bf16 v[122:125], v[158:161], v[182:185], v[122:125]
	v_mfma_f32_16x16x32_bf16 v[110:113], v[150:153], v[190:193], v[110:113]
	v_mfma_f32_16x16x32_bf16 v[106:109], v[158:161], v[190:193], v[106:109]
	v_mfma_f32_16x16x32_bf16 v[94:97], v[150:153], v[198:201], v[94:97]
	v_mfma_f32_16x16x32_bf16 v[90:93], v[158:161], v[198:201], v[90:93]
	v_mfma_f32_16x16x32_bf16 v[78:81], v[150:153], v[218:221], v[78:81]
	v_mfma_f32_16x16x32_bf16 v[74:77], v[158:161], v[218:221], v[74:77]
	v_mfma_f32_16x16x32_bf16 v[126:129], v[154:157], v[186:189], v[126:129]
	v_mfma_f32_16x16x32_bf16 v[122:125], v[162:165], v[186:189], v[122:125]
	v_mfma_f32_16x16x32_bf16 v[110:113], v[154:157], v[194:197], v[110:113]
	v_mfma_f32_16x16x32_bf16 v[106:109], v[162:165], v[194:197], v[106:109]
	v_mfma_f32_16x16x32_bf16 v[94:97], v[154:157], v[202:205], v[94:97]
	v_mfma_f32_16x16x32_bf16 v[90:93], v[162:165], v[202:205], v[90:93]
	v_mfma_f32_16x16x32_bf16 v[78:81], v[154:157], v[222:225], v[78:81]
	v_mfma_f32_16x16x32_bf16 v[74:77], v[162:165], v[222:225], v[74:77]
	v_mfma_f32_16x16x32_bf16 v[118:121], v[166:169], v[182:185], v[118:121]
	v_mfma_f32_16x16x32_bf16 v[114:117], v[174:177], v[182:185], v[114:117]
	v_mfma_f32_16x16x32_bf16 v[102:105], v[166:169], v[190:193], v[102:105]
	v_mfma_f32_16x16x32_bf16 v[98:101], v[174:177], v[190:193], v[98:101]
	v_mfma_f32_16x16x32_bf16 v[86:89], v[166:169], v[198:201], v[86:89]
	v_mfma_f32_16x16x32_bf16 v[82:85], v[174:177], v[198:201], v[82:85]
	v_mfma_f32_16x16x32_bf16 v[70:73], v[166:169], v[218:221], v[70:73]
	v_mfma_f32_16x16x32_bf16 v[66:69], v[174:177], v[218:221], v[66:69]
	v_mfma_f32_16x16x32_bf16 v[118:121], v[170:173], v[186:189], v[118:121]
	v_mfma_f32_16x16x32_bf16 v[114:117], v[178:181], v[186:189], v[114:117]
	v_mfma_f32_16x16x32_bf16 v[102:105], v[170:173], v[194:197], v[102:105]
	v_mfma_f32_16x16x32_bf16 v[98:101], v[178:181], v[194:197], v[98:101]
	v_mfma_f32_16x16x32_bf16 v[86:89], v[170:173], v[202:205], v[86:89]
	v_mfma_f32_16x16x32_bf16 v[82:85], v[178:181], v[202:205], v[82:85]
	v_mfma_f32_16x16x32_bf16 v[70:73], v[170:173], v[222:225], v[70:73]
	v_mfma_f32_16x16x32_bf16 v[66:69], v[178:181], v[222:225], v[66:69]
	s_barrier
	s_add_i32 s42, s45, s62
	v_lshl_add_u64 v[226:227], v[226:227], 0, s[20:21]
	s_mov_b32 m0, s42
	ds_read_b128 v[182:185], v213 offset:49152
	ds_read_b128 v[186:189], v213 offset:50176
	ds_read_b128 v[190:193], v213 offset:51200
	ds_read_b128 v[194:197], v213 offset:52224
	ds_read_b128 v[198:201], v213 offset:53248
	ds_read_b128 v[202:205], v213 offset:54272
	ds_read_b128 v[218:221], v213 offset:55296
	ds_read_b128 v[222:225], v213 offset:56320
	global_load_lds_dwordx4 v[226:227], off
	s_add_i32 m0, s42, 0x2000
	s_add_u32 s36, s36, 0x158080
	v_lshl_add_u64 v[226:227], v[228:229], 0, s[20:21]
	s_addc_u32 s37, s37, 0
	s_add_i32 s42, s81, s62
	global_load_lds_dwordx4 v[226:227], off
	s_mov_b32 m0, s42
	s_nop 0
	global_load_lds_dwordx4 v132, s[36:37]
	s_add_i32 m0, s42, 0x2000
	s_nop 0
	global_load_lds_dwordx4 v136, s[36:37]
	v_lshl_add_u64 v[226:227], v[230:231], 0, s[20:21]
	s_mov_b32 m0, s70
	s_nop 0
	global_load_lds_dwordx4 v[226:227], off
	v_lshl_add_u64 v[226:227], v[232:233], 0, s[20:21]
	s_mov_b32 m0, s71
	s_nop 0
	global_load_lds_dwordx4 v[226:227], off
	s_waitcnt vmcnt(8)
	s_waitcnt lgkmcnt(0)
	s_barrier
	v_mfma_f32_16x16x32_bf16 v[62:65], v[150:153], v[182:185], v[62:65]
	v_mfma_f32_16x16x32_bf16 v[58:61], v[158:161], v[182:185], v[58:61]
	v_mfma_f32_16x16x32_bf16 v[46:49], v[150:153], v[190:193], v[46:49]
	v_mfma_f32_16x16x32_bf16 v[42:45], v[158:161], v[190:193], v[42:45]
	v_mfma_f32_16x16x32_bf16 v[30:33], v[150:153], v[198:201], v[30:33]
	v_mfma_f32_16x16x32_bf16 v[26:29], v[158:161], v[198:201], v[26:29]
	v_mfma_f32_16x16x32_bf16 v[14:17], v[150:153], v[218:221], v[14:17]
	v_mfma_f32_16x16x32_bf16 v[10:13], v[158:161], v[218:221], v[10:13]
	v_mfma_f32_16x16x32_bf16 v[62:65], v[154:157], v[186:189], v[62:65]
	v_mfma_f32_16x16x32_bf16 v[58:61], v[162:165], v[186:189], v[58:61]
	v_mfma_f32_16x16x32_bf16 v[46:49], v[154:157], v[194:197], v[46:49]
	v_mfma_f32_16x16x32_bf16 v[42:45], v[162:165], v[194:197], v[42:45]
	v_mfma_f32_16x16x32_bf16 v[30:33], v[154:157], v[202:205], v[30:33]
	v_mfma_f32_16x16x32_bf16 v[26:29], v[162:165], v[202:205], v[26:29]
	v_mfma_f32_16x16x32_bf16 v[14:17], v[154:157], v[222:225], v[14:17]
	v_mfma_f32_16x16x32_bf16 v[10:13], v[162:165], v[222:225], v[10:13]
	v_mfma_f32_16x16x32_bf16 v[54:57], v[166:169], v[182:185], v[54:57]
	v_mfma_f32_16x16x32_bf16 v[50:53], v[174:177], v[182:185], v[50:53]
	v_mfma_f32_16x16x32_bf16 v[38:41], v[166:169], v[190:193], v[38:41]
	v_mfma_f32_16x16x32_bf16 v[34:37], v[174:177], v[190:193], v[34:37]
	v_mfma_f32_16x16x32_bf16 v[22:25], v[166:169], v[198:201], v[22:25]
	v_mfma_f32_16x16x32_bf16 v[18:21], v[174:177], v[198:201], v[18:21]
	v_mfma_f32_16x16x32_bf16 v[6:9], v[166:169], v[218:221], v[6:9]
	v_mfma_f32_16x16x32_bf16 v[2:5], v[174:177], v[218:221], v[2:5]
	v_mfma_f32_16x16x32_bf16 v[54:57], v[170:173], v[186:189], v[54:57]
	v_mfma_f32_16x16x32_bf16 v[50:53], v[178:181], v[186:189], v[50:53]
	v_mfma_f32_16x16x32_bf16 v[38:41], v[170:173], v[194:197], v[38:41]
	v_mfma_f32_16x16x32_bf16 v[34:37], v[178:181], v[194:197], v[34:37]
	v_mfma_f32_16x16x32_bf16 v[22:25], v[170:173], v[202:205], v[22:25]
	v_mfma_f32_16x16x32_bf16 v[18:21], v[178:181], v[202:205], v[18:21]
	v_mfma_f32_16x16x32_bf16 v[6:9], v[170:173], v[222:225], v[6:9]
	v_mfma_f32_16x16x32_bf16 v[2:5], v[178:181], v[222:225], v[2:5]
	s_barrier
	s_add_i32 s44, s44, 2
	s_add_u32 s0, s0, 0x100
	s_addc_u32 s1, s1, 0
	s_add_u32 s31, s31, 0x100
	s_addc_u32 s35, s35, 0
	s_cmpk_gt_u32 s44, 0x53
	s_cbranch_scc0 .LBB0_659
	s_setprio 0
	s_and_b64 vcc, exec, s[22:23]
	s_cbranch_vccz .LBB0_662
	s_barrier

.LBB0_766:
	s_ashr_i32 s15, s14, 31
	s_lshl_b64 s[16:17], s[14:15], 20
	s_add_u32 s16, s28, s16
	s_addc_u32 s17, s29, s17
	s_and_b64 s[18:19], s[4:5], exec
	s_cselect_b32 s15, s17, s23
	s_cselect_b32 s65, s16, s22
	s_ashr_i32 s13, s12, 31
	s_lshl_b64 s[18:19], s[12:13], 20
	s_add_u32 s18, s30, s18
	s_addc_u32 s19, s31, s19
	s_and_b64 s[26:27], s[4:5], exec
	s_cselect_b32 s13, s19, s25
	s_cselect_b32 s66, s18, s24
	s_add_u32 s22, s22, 0x80080
	s_addc_u32 s23, s23, 0
	s_add_u32 s67, s24, 0x100
	v_mov_b32_e32 v2, 0
	s_addc_u32 s68, s25, 0
	s_mov_b32 s69, -2
	v_mov_b32_e32 v3, v2
	v_mov_b32_e32 v4, v2
	v_mov_b32_e32 v5, v2
	v_mov_b32_e32 v6, v2
	v_mov_b32_e32 v7, v2
	v_mov_b32_e32 v8, v2
	v_mov_b32_e32 v9, v2
	v_mov_b32_e32 v10, v2
	v_mov_b32_e32 v11, v2
	v_mov_b32_e32 v12, v2
	v_mov_b32_e32 v13, v2
	v_mov_b32_e32 v18, v2
	v_mov_b32_e32 v19, v2
	v_mov_b32_e32 v20, v2
	v_mov_b32_e32 v21, v2
	v_mov_b32_e32 v26, v2
	v_mov_b32_e32 v27, v2
	v_mov_b32_e32 v28, v2
	v_mov_b32_e32 v29, v2
	v_mov_b32_e32 v34, v2
	v_mov_b32_e32 v35, v2
	v_mov_b32_e32 v36, v2
	v_mov_b32_e32 v37, v2
	v_mov_b32_e32 v42, v2
	v_mov_b32_e32 v43, v2
	v_mov_b32_e32 v44, v2
	v_mov_b32_e32 v45, v2
	v_mov_b32_e32 v50, v2
	v_mov_b32_e32 v51, v2
	v_mov_b32_e32 v52, v2
	v_mov_b32_e32 v53, v2
	v_mov_b32_e32 v14, v2
	v_mov_b32_e32 v15, v2
	v_mov_b32_e32 v16, v2
	v_mov_b32_e32 v17, v2
	v_mov_b32_e32 v22, v2
	v_mov_b32_e32 v23, v2
	v_mov_b32_e32 v24, v2
	v_mov_b32_e32 v25, v2
	v_mov_b32_e32 v30, v2
	v_mov_b32_e32 v31, v2
	v_mov_b32_e32 v32, v2
	v_mov_b32_e32 v33, v2
	v_mov_b32_e32 v38, v2
	v_mov_b32_e32 v39, v2
	v_mov_b32_e32 v40, v2
	v_mov_b32_e32 v41, v2
	v_mov_b32_e32 v46, v2
	v_mov_b32_e32 v47, v2
	v_mov_b32_e32 v48, v2
	v_mov_b32_e32 v49, v2
	v_mov_b32_e32 v54, v2
	v_mov_b32_e32 v55, v2
	v_mov_b32_e32 v56, v2
	v_mov_b32_e32 v57, v2
	v_mov_b32_e32 v58, v2
	v_mov_b32_e32 v59, v2
	v_mov_b32_e32 v60, v2
	v_mov_b32_e32 v61, v2
	v_mov_b32_e32 v62, v2
	v_mov_b32_e32 v63, v2
	v_mov_b32_e32 v64, v2
	v_mov_b32_e32 v65, v2
	v_mov_b32_e32 v66, v2
	v_mov_b32_e32 v67, v2
	v_mov_b32_e32 v68, v2
	v_mov_b32_e32 v69, v2
	v_mov_b32_e32 v70, v2
	v_mov_b32_e32 v71, v2
	v_mov_b32_e32 v72, v2
	v_mov_b32_e32 v73, v2
	v_mov_b32_e32 v74, v2
	v_mov_b32_e32 v75, v2
	v_mov_b32_e32 v76, v2
	v_mov_b32_e32 v77, v2
	v_mov_b32_e32 v82, v2
	v_mov_b32_e32 v83, v2
	v_mov_b32_e32 v84, v2
	v_mov_b32_e32 v85, v2
	v_mov_b32_e32 v90, v2
	v_mov_b32_e32 v91, v2
	v_mov_b32_e32 v92, v2
	v_mov_b32_e32 v93, v2
	v_mov_b32_e32 v98, v2
	v_mov_b32_e32 v99, v2
	v_mov_b32_e32 v100, v2
	v_mov_b32_e32 v101, v2
	v_mov_b32_e32 v106, v2
	v_mov_b32_e32 v107, v2
	v_mov_b32_e32 v108, v2
	v_mov_b32_e32 v109, v2
	v_mov_b32_e32 v114, v2
	v_mov_b32_e32 v115, v2
	v_mov_b32_e32 v116, v2
	v_mov_b32_e32 v117, v2
	v_mov_b32_e32 v78, v2
	v_mov_b32_e32 v79, v2
	v_mov_b32_e32 v80, v2
	v_mov_b32_e32 v81, v2
	v_mov_b32_e32 v86, v2
	v_mov_b32_e32 v87, v2
	v_mov_b32_e32 v88, v2
	v_mov_b32_e32 v89, v2
	v_mov_b32_e32 v94, v2
	v_mov_b32_e32 v95, v2
	v_mov_b32_e32 v96, v2
	v_mov_b32_e32 v97, v2
	v_mov_b32_e32 v102, v2
	v_mov_b32_e32 v103, v2
	v_mov_b32_e32 v104, v2
	v_mov_b32_e32 v105, v2
	v_mov_b32_e32 v110, v2
	v_mov_b32_e32 v111, v2
	v_mov_b32_e32 v112, v2
	v_mov_b32_e32 v113, v2
	v_mov_b32_e32 v118, v2
	v_mov_b32_e32 v119, v2
	v_mov_b32_e32 v120, v2
	v_mov_b32_e32 v121, v2
	v_mov_b32_e32 v122, v2
	v_mov_b32_e32 v123, v2
	v_mov_b32_e32 v124, v2
	v_mov_b32_e32 v125, v2
	v_mov_b32_e32 v126, v2
	v_mov_b32_e32 v127, v2
	v_mov_b32_e32 v128, v2
	v_mov_b32_e32 v129, v2
	s_mov_b64 vcc, s[10:11]
	s_cbranch_vccnz .Lsp_767
	s_setprio 1
.Lsp_767:
.LBB0_767:
	ds_read_b128 v[146:149], v152
	ds_read_b128 v[156:159], v152 offset:1024
	ds_read_b128 v[160:163], v152 offset:2048
	ds_read_b128 v[164:167], v152 offset:3072
	ds_read_b128 v[168:171], v153
	ds_read_b128 v[172:175], v153 offset:1024
	ds_read_b128 v[176:179], v153 offset:2048
	ds_read_b128 v[180:183], v153 offset:3072
	s_add_u32 s24, s22, 0xfff80080
	s_addc_u32 s25, s23, -1
	s_cmp_eq_u32 s69, 28
	s_cselect_b32 s27, s15, s25
	s_cselect_b32 s26, s65, s24
	s_cselect_b32 s25, s13, s68
	s_cselect_b32 s24, s66, s67
	s_add_i32 m0, s21, 0xc000
	ds_read_b128 v[184:187], v154
	ds_read_b128 v[188:191], v154 offset:1024
	ds_read_b128 v[192:195], v154 offset:2048
	ds_read_b128 v[196:199], v154 offset:3072
	ds_read_b128 v[200:203], v154 offset:4096
	ds_read_b128 v[204:207], v154 offset:5120
	ds_read_b128 v[208:211], v154 offset:6144
	ds_read_b128 v[212:215], v154 offset:7168
	global_load_lds_dwordx4 v138, s[22:23]
	s_add_i32 m0, s21, 0xe000
	s_nop 0
	global_load_lds_dwordx4 v140, s[22:23]
	s_waitcnt vmcnt(8)
	s_waitcnt lgkmcnt(0)
	s_barrier
	v_mfma_f32_16x16x32_bf16 v[126:129], v[146:149], v[184:187], v[126:129]
	v_mfma_f32_16x16x32_bf16 v[122:125], v[160:163], v[184:187], v[122:125]
	v_mfma_f32_16x16x32_bf16 v[118:121], v[146:149], v[192:195], v[118:121]
	v_mfma_f32_16x16x32_bf16 v[110:113], v[160:163], v[192:195], v[110:113]
	v_mfma_f32_16x16x32_bf16 v[102:105], v[146:149], v[200:203], v[102:105]
	v_mfma_f32_16x16x32_bf16 v[94:97], v[160:163], v[200:203], v[94:97]
	v_mfma_f32_16x16x32_bf16 v[86:89], v[146:149], v[208:211], v[86:89]
	v_mfma_f32_16x16x32_bf16 v[78:81], v[160:163], v[208:211], v[78:81]
	v_mfma_f32_16x16x32_bf16 v[126:129], v[156:159], v[188:191], v[126:129]
	v_mfma_f32_16x16x32_bf16 v[122:125], v[164:167], v[188:191], v[122:125]
	v_mfma_f32_16x16x32_bf16 v[118:121], v[156:159], v[196:199], v[118:121]
	v_mfma_f32_16x16x32_bf16 v[110:113], v[164:167], v[196:199], v[110:113]
	v_mfma_f32_16x16x32_bf16 v[102:105], v[156:159], v[204:207], v[102:105]
	v_mfma_f32_16x16x32_bf16 v[94:97], v[164:167], v[204:207], v[94:97]
	v_mfma_f32_16x16x32_bf16 v[86:89], v[156:159], v[212:215], v[86:89]
	v_mfma_f32_16x16x32_bf16 v[78:81], v[164:167], v[212:215], v[78:81]
	v_mfma_f32_16x16x32_bf16 v[114:117], v[168:171], v[184:187], v[114:117]
	v_mfma_f32_16x16x32_bf16 v[106:109], v[176:179], v[184:187], v[106:109]
	v_mfma_f32_16x16x32_bf16 v[98:101], v[168:171], v[192:195], v[98:101]
	v_mfma_f32_16x16x32_bf16 v[90:93], v[176:179], v[192:195], v[90:93]
	v_mfma_f32_16x16x32_bf16 v[82:85], v[168:171], v[200:203], v[82:85]
	v_mfma_f32_16x16x32_bf16 v[74:77], v[176:179], v[200:203], v[74:77]
	v_mfma_f32_16x16x32_bf16 v[70:73], v[168:171], v[208:211], v[70:73]
	v_mfma_f32_16x16x32_bf16 v[66:69], v[176:179], v[208:211], v[66:69]
	v_mfma_f32_16x16x32_bf16 v[114:117], v[172:175], v[188:191], v[114:117]
	v_mfma_f32_16x16x32_bf16 v[106:109], v[180:183], v[188:191], v[106:109]
	v_mfma_f32_16x16x32_bf16 v[98:101], v[172:175], v[196:199], v[98:101]
	v_mfma_f32_16x16x32_bf16 v[90:93], v[180:183], v[196:199], v[90:93]
	v_mfma_f32_16x16x32_bf16 v[82:85], v[172:175], v[204:207], v[82:85]
	v_mfma_f32_16x16x32_bf16 v[74:77], v[180:183], v[204:207], v[74:77]
	v_mfma_f32_16x16x32_bf16 v[70:73], v[172:175], v[212:215], v[70:73]
	v_mfma_f32_16x16x32_bf16 v[66:69], v[180:183], v[212:215], v[66:69]
	s_barrier
	s_add_i32 s70, s61, s33
	v_lshl_add_u64 v[216:217], s[24:25], 0, v[134:135]
	s_mov_b32 m0, s70
	ds_read_b128 v[184:187], v154 offset:16384
	ds_read_b128 v[188:191], v154 offset:17408
	ds_read_b128 v[192:195], v154 offset:18432
	ds_read_b128 v[196:199], v154 offset:19456
	ds_read_b128 v[200:203], v154 offset:20480
	ds_read_b128 v[204:207], v154 offset:21504
	ds_read_b128 v[208:211], v154 offset:22528
	ds_read_b128 v[212:215], v154 offset:23552
	global_load_lds_dwordx4 v134, s[24:25]
	s_add_i32 m0, s70, 0x2000
	s_add_u32 s70, s24, 0x80000
	v_lshl_add_u64 v[218:219], s[24:25], 0, v[130:131]
	s_addc_u32 s71, s25, 0
	s_add_i32 s72, s62, s33
	global_load_lds_dwordx4 v130, s[24:25]
	s_mov_b32 m0, s72
	v_lshl_add_u64 v[222:223], s[26:27], 0, v[132:133]
	global_load_lds_dwordx4 v134, s[70:71]
	s_add_i32 m0, s72, 0x2000
	s_nop 0
	global_load_lds_dwordx4 v130, s[70:71]
	v_lshl_add_u64 v[220:221], s[26:27], 0, v[136:137]
	s_mov_b32 m0, s21
	s_nop 0
	global_load_lds_dwordx4 v136, s[26:27]
	s_mov_b32 m0, s36
	s_nop 0
	global_load_lds_dwordx4 v132, s[26:27]
	s_waitcnt vmcnt(8)
	s_waitcnt lgkmcnt(0)
	s_barrier
	v_mfma_f32_16x16x32_bf16 v[62:65], v[146:149], v[184:187], v[62:65]
	v_mfma_f32_16x16x32_bf16 v[58:61], v[160:163], v[184:187], v[58:61]
	v_mfma_f32_16x16x32_bf16 v[54:57], v[146:149], v[192:195], v[54:57]
	v_mfma_f32_16x16x32_bf16 v[46:49], v[160:163], v[192:195], v[46:49]
	v_mfma_f32_16x16x32_bf16 v[38:41], v[146:149], v[200:203], v[38:41]
	v_mfma_f32_16x16x32_bf16 v[30:33], v[160:163], v[200:203], v[30:33]
	v_mfma_f32_16x16x32_bf16 v[22:25], v[146:149], v[208:211], v[22:25]
	v_mfma_f32_16x16x32_bf16 v[14:17], v[160:163], v[208:211], v[14:17]
	v_mfma_f32_16x16x32_bf16 v[62:65], v[156:159], v[188:191], v[62:65]
	v_mfma_f32_16x16x32_bf16 v[58:61], v[164:167], v[188:191], v[58:61]
	v_mfma_f32_16x16x32_bf16 v[54:57], v[156:159], v[196:199], v[54:57]
	v_mfma_f32_16x16x32_bf16 v[46:49], v[164:167], v[196:199], v[46:49]
	v_mfma_f32_16x16x32_bf16 v[38:41], v[156:159], v[204:207], v[38:41]
	v_mfma_f32_16x16x32_bf16 v[30:33], v[164:167], v[204:207], v[30:33]
	v_mfma_f32_16x16x32_bf16 v[22:25], v[156:159], v[212:215], v[22:25]
	v_mfma_f32_16x16x32_bf16 v[14:17], v[164:167], v[212:215], v[14:17]
	v_mfma_f32_16x16x32_bf16 v[50:53], v[168:171], v[184:187], v[50:53]
	v_mfma_f32_16x16x32_bf16 v[42:45], v[176:179], v[184:187], v[42:45]
	v_mfma_f32_16x16x32_bf16 v[34:37], v[168:171], v[192:195], v[34:37]
	v_mfma_f32_16x16x32_bf16 v[26:29], v[176:179], v[192:195], v[26:29]
	v_mfma_f32_16x16x32_bf16 v[18:21], v[168:171], v[200:203], v[18:21]
	v_mfma_f32_16x16x32_bf16 v[10:13], v[176:179], v[200:203], v[10:13]
	v_mfma_f32_16x16x32_bf16 v[6:9], v[168:171], v[208:211], v[6:9]
	v_mfma_f32_16x16x32_bf16 v[2:5], v[176:179], v[208:211], v[2:5]
	v_mfma_f32_16x16x32_bf16 v[50:53], v[172:175], v[188:191], v[50:53]
	v_mfma_f32_16x16x32_bf16 v[42:45], v[180:183], v[188:191], v[42:45]
	v_mfma_f32_16x16x32_bf16 v[34:37], v[172:175], v[196:199], v[34:37]
	v_mfma_f32_16x16x32_bf16 v[26:29], v[180:183], v[196:199], v[26:29]
	v_mfma_f32_16x16x32_bf16 v[18:21], v[172:175], v[204:207], v[18:21]
	v_mfma_f32_16x16x32_bf16 v[10:13], v[180:183], v[204:207], v[10:13]
	v_mfma_f32_16x16x32_bf16 v[6:9], v[172:175], v[212:215], v[6:9]
	v_mfma_f32_16x16x32_bf16 v[2:5], v[180:183], v[212:215], v[2:5]
	s_barrier
	s_add_i32 s70, 0, 0x18000
	v_add_u32_e32 v155, s70, v150
	s_add_i32 s71, 0, 0x1c000
	ds_read_b128 v[146:149], v155
	ds_read_b128 v[156:159], v155 offset:1024
	ds_read_b128 v[160:163], v155 offset:2048
	ds_read_b128 v[164:167], v155 offset:3072
	v_add_u32_e32 v155, s71, v150
	ds_read_b128 v[168:171], v155
	ds_read_b128 v[172:175], v155 offset:1024
	ds_read_b128 v[176:179], v155 offset:2048
	ds_read_b128 v[180:183], v155 offset:3072
	s_add_u32 s26, s26, 0x80000
	s_addc_u32 s27, s27, 0
	s_mov_b32 m0, s37
	ds_read_b128 v[184:187], v154 offset:32768
	ds_read_b128 v[188:191], v154 offset:33792
	ds_read_b128 v[192:195], v154 offset:34816
	ds_read_b128 v[196:199], v154 offset:35840
	ds_read_b128 v[200:203], v154 offset:36864
	ds_read_b128 v[204:207], v154 offset:37888
	ds_read_b128 v[208:211], v154 offset:38912
	ds_read_b128 v[212:215], v154 offset:39936
	global_load_lds_dwordx4 v136, s[26:27]
	s_mov_b32 m0, s42
	s_nop 0
	global_load_lds_dwordx4 v132, s[26:27]
	s_waitcnt vmcnt(8)
	s_waitcnt lgkmcnt(0)
	s_barrier
	v_mfma_f32_16x16x32_bf16 v[126:129], v[146:149], v[184:187], v[126:129]
	v_mfma_f32_16x16x32_bf16 v[122:125], v[160:163], v[184:187], v[122:125]
	v_mfma_f32_16x16x32_bf16 v[118:121], v[146:149], v[192:195], v[118:121]
	v_mfma_f32_16x16x32_bf16 v[110:113], v[160:163], v[192:195], v[110:113]
	v_mfma_f32_16x16x32_bf16 v[102:105], v[146:149], v[200:203], v[102:105]
	v_mfma_f32_16x16x32_bf16 v[94:97], v[160:163], v[200:203], v[94:97]
	v_mfma_f32_16x16x32_bf16 v[86:89], v[146:149], v[208:211], v[86:89]
	v_mfma_f32_16x16x32_bf16 v[78:81], v[160:163], v[208:211], v[78:81]
	v_mfma_f32_16x16x32_bf16 v[126:129], v[156:159], v[188:191], v[126:129]
	v_mfma_f32_16x16x32_bf16 v[122:125], v[164:167], v[188:191], v[122:125]
	v_mfma_f32_16x16x32_bf16 v[118:121], v[156:159], v[196:199], v[118:121]
	v_mfma_f32_16x16x32_bf16 v[110:113], v[164:167], v[196:199], v[110:113]
	v_mfma_f32_16x16x32_bf16 v[102:105], v[156:159], v[204:207], v[102:105]
	v_mfma_f32_16x16x32_bf16 v[94:97], v[164:167], v[204:207], v[94:97]
	v_mfma_f32_16x16x32_bf16 v[86:89], v[156:159], v[212:215], v[86:89]
	v_mfma_f32_16x16x32_bf16 v[78:81], v[164:167], v[212:215], v[78:81]
	v_mfma_f32_16x16x32_bf16 v[114:117], v[168:171], v[184:187], v[114:117]
	v_mfma_f32_16x16x32_bf16 v[106:109], v[176:179], v[184:187], v[106:109]
	v_mfma_f32_16x16x32_bf16 v[98:101], v[168:171], v[192:195], v[98:101]
	v_mfma_f32_16x16x32_bf16 v[90:93], v[176:179], v[192:195], v[90:93]
	v_mfma_f32_16x16x32_bf16 v[82:85], v[168:171], v[200:203], v[82:85]
	v_mfma_f32_16x16x32_bf16 v[74:77], v[176:179], v[200:203], v[74:77]
	v_mfma_f32_16x16x32_bf16 v[70:73], v[168:171], v[208:211], v[70:73]
	v_mfma_f32_16x16x32_bf16 v[66:69], v[176:179], v[208:211], v[66:69]
	v_mfma_f32_16x16x32_bf16 v[114:117], v[172:175], v[188:191], v[114:117]
	v_mfma_f32_16x16x32_bf16 v[106:109], v[180:183], v[188:191], v[106:109]
	v_mfma_f32_16x16x32_bf16 v[98:101], v[172:175], v[196:199], v[98:101]
	v_mfma_f32_16x16x32_bf16 v[90:93], v[180:183], v[196:199], v[90:93]
	v_mfma_f32_16x16x32_bf16 v[82:85], v[172:175], v[204:207], v[82:85]
	v_mfma_f32_16x16x32_bf16 v[74:77], v[180:183], v[204:207], v[74:77]
	v_mfma_f32_16x16x32_bf16 v[70:73], v[172:175], v[212:215], v[70:73]
	v_mfma_f32_16x16x32_bf16 v[66:69], v[180:183], v[212:215], v[66:69]
	s_barrier
	s_add_i32 s26, s70, s33
	v_lshl_add_u64 v[216:217], v[216:217], 0, s[8:9]
	s_mov_b32 m0, s26
	ds_read_b128 v[184:187], v154 offset:49152
	ds_read_b128 v[188:191], v154 offset:50176
	ds_read_b128 v[192:195], v154 offset:51200
	ds_read_b128 v[196:199], v154 offset:52224
	ds_read_b128 v[200:203], v154 offset:53248
	ds_read_b128 v[204:207], v154 offset:54272
	ds_read_b128 v[208:211], v154 offset:55296
	ds_read_b128 v[212:215], v154 offset:56320
	global_load_lds_dwordx4 v[216:217], off
	s_add_i32 m0, s26, 0x2000
	s_add_u32 s24, s24, 0x80080
	v_lshl_add_u64 v[216:217], v[218:219], 0, s[8:9]
	s_addc_u32 s25, s25, 0
	s_add_i32 s26, s71, s33
	global_load_lds_dwordx4 v[216:217], off
	s_mov_b32 m0, s26
	s_nop 0
	global_load_lds_dwordx4 v134, s[24:25]
	s_add_i32 m0, s26, 0x2000
	s_nop 0
	global_load_lds_dwordx4 v130, s[24:25]
	v_lshl_add_u64 v[216:217], v[220:221], 0, s[8:9]
	s_mov_b32 m0, s44
	s_nop 0
	global_load_lds_dwordx4 v[216:217], off
	v_lshl_add_u64 v[216:217], v[222:223], 0, s[8:9]
	s_mov_b32 m0, s45
	s_nop 0
	global_load_lds_dwordx4 v[216:217], off
	s_waitcnt vmcnt(8)
	s_waitcnt lgkmcnt(0)
	s_barrier
	v_mfma_f32_16x16x32_bf16 v[62:65], v[146:149], v[184:187], v[62:65]
	v_mfma_f32_16x16x32_bf16 v[58:61], v[160:163], v[184:187], v[58:61]
	v_mfma_f32_16x16x32_bf16 v[54:57], v[146:149], v[192:195], v[54:57]
	v_mfma_f32_16x16x32_bf16 v[46:49], v[160:163], v[192:195], v[46:49]
	v_mfma_f32_16x16x32_bf16 v[38:41], v[146:149], v[200:203], v[38:41]
	v_mfma_f32_16x16x32_bf16 v[30:33], v[160:163], v[200:203], v[30:33]
	v_mfma_f32_16x16x32_bf16 v[22:25], v[146:149], v[208:211], v[22:25]
	v_mfma_f32_16x16x32_bf16 v[14:17], v[160:163], v[208:211], v[14:17]
	v_mfma_f32_16x16x32_bf16 v[62:65], v[156:159], v[188:191], v[62:65]
	v_mfma_f32_16x16x32_bf16 v[58:61], v[164:167], v[188:191], v[58:61]
	v_mfma_f32_16x16x32_bf16 v[54:57], v[156:159], v[196:199], v[54:57]
	v_mfma_f32_16x16x32_bf16 v[46:49], v[164:167], v[196:199], v[46:49]
	v_mfma_f32_16x16x32_bf16 v[38:41], v[156:159], v[204:207], v[38:41]
	v_mfma_f32_16x16x32_bf16 v[30:33], v[164:167], v[204:207], v[30:33]
	v_mfma_f32_16x16x32_bf16 v[22:25], v[156:159], v[212:215], v[22:25]
	v_mfma_f32_16x16x32_bf16 v[14:17], v[164:167], v[212:215], v[14:17]
	v_mfma_f32_16x16x32_bf16 v[50:53], v[168:171], v[184:187], v[50:53]
	v_mfma_f32_16x16x32_bf16 v[42:45], v[176:179], v[184:187], v[42:45]
	v_mfma_f32_16x16x32_bf16 v[34:37], v[168:171], v[192:195], v[34:37]
	v_mfma_f32_16x16x32_bf16 v[26:29], v[176:179], v[192:195], v[26:29]
	v_mfma_f32_16x16x32_bf16 v[18:21], v[168:171], v[200:203], v[18:21]
	v_mfma_f32_16x16x32_bf16 v[10:13], v[176:179], v[200:203], v[10:13]
	v_mfma_f32_16x16x32_bf16 v[6:9], v[168:171], v[208:211], v[6:9]
	v_mfma_f32_16x16x32_bf16 v[2:5], v[176:179], v[208:211], v[2:5]
	v_mfma_f32_16x16x32_bf16 v[50:53], v[172:175], v[188:191], v[50:53]
	v_mfma_f32_16x16x32_bf16 v[42:45], v[180:183], v[188:191], v[42:45]
	v_mfma_f32_16x16x32_bf16 v[34:37], v[172:175], v[196:199], v[34:37]
	v_mfma_f32_16x16x32_bf16 v[26:29], v[180:183], v[196:199], v[26:29]
	v_mfma_f32_16x16x32_bf16 v[18:21], v[172:175], v[204:207], v[18:21]
	v_mfma_f32_16x16x32_bf16 v[10:13], v[180:183], v[204:207], v[10:13]
	v_mfma_f32_16x16x32_bf16 v[6:9], v[172:175], v[212:215], v[6:9]
	v_mfma_f32_16x16x32_bf16 v[2:5], v[180:183], v[212:215], v[2:5]
	s_barrier
	s_add_i32 s69, s69, 2
	s_add_u32 s22, s22, 0x100
	s_addc_u32 s23, s23, 0
	s_add_u32 s67, s67, 0x100
	s_addc_u32 s68, s68, 0
	s_cmp_gt_u32 s69, 29
	s_cbranch_scc0 .LBB0_767
	s_setprio 0
	s_and_b64 vcc, exec, s[10:11]
	s_cbranch_vccz .LBB0_770
	s_barrier

.LBB0_1042:
	s_ashr_i32 s35, s34, 31
	s_lshl_b64 s[36:37], s[34:35], 19
	s_add_u32 s36, s29, s36
	s_addc_u32 s37, s33, s37
	s_and_b64 s[38:39], s[12:13], exec
	s_cselect_b32 s1, s37, s49
	s_cselect_b32 s35, s36, s48
	s_ashr_i32 s31, s30, 31
	s_lshl_b64 s[38:39], s[30:31], 19
	s_add_u32 s38, s62, s38
	s_addc_u32 s39, s63, s39
	s_and_b64 s[40:41], s[12:13], exec
	s_cselect_b32 s31, s39, s45
	s_cselect_b32 s43, s38, s44
	s_add_u32 s40, s48, 0x40080
	s_addc_u32 s41, s49, 0
	s_add_u32 s60, s44, 0x100
	v_mov_b32_e32 v34, 0
	s_addc_u32 s61, s45, 0
	s_mov_b32 s81, -2
	v_mov_b32_e32 v35, v34
	v_mov_b32_e32 v36, v34
	v_mov_b32_e32 v37, v34
	v_mov_b32_e32 v38, v34
	v_mov_b32_e32 v39, v34
	v_mov_b32_e32 v40, v34
	v_mov_b32_e32 v41, v34
	v_mov_b32_e32 v50, v34
	v_mov_b32_e32 v51, v34
	v_mov_b32_e32 v52, v34
	v_mov_b32_e32 v53, v34
	v_mov_b32_e32 v54, v34
	v_mov_b32_e32 v55, v34
	v_mov_b32_e32 v56, v34
	v_mov_b32_e32 v57, v34
	v_mov_b32_e32 v66, v34
	v_mov_b32_e32 v67, v34
	v_mov_b32_e32 v68, v34
	v_mov_b32_e32 v69, v34
	v_mov_b32_e32 v70, v34
	v_mov_b32_e32 v71, v34
	v_mov_b32_e32 v72, v34
	v_mov_b32_e32 v73, v34
	v_mov_b32_e32 v82, v34
	v_mov_b32_e32 v83, v34
	v_mov_b32_e32 v84, v34
	v_mov_b32_e32 v85, v34
	v_mov_b32_e32 v86, v34
	v_mov_b32_e32 v87, v34
	v_mov_b32_e32 v88, v34
	v_mov_b32_e32 v89, v34
	v_mov_b32_e32 v42, v34
	v_mov_b32_e32 v43, v34
	v_mov_b32_e32 v44, v34
	v_mov_b32_e32 v45, v34
	v_mov_b32_e32 v46, v34
	v_mov_b32_e32 v47, v34
	v_mov_b32_e32 v48, v34
	v_mov_b32_e32 v49, v34
	v_mov_b32_e32 v58, v34
	v_mov_b32_e32 v59, v34
	v_mov_b32_e32 v60, v34
	v_mov_b32_e32 v61, v34
	v_mov_b32_e32 v62, v34
	v_mov_b32_e32 v63, v34
	v_mov_b32_e32 v64, v34
	v_mov_b32_e32 v65, v34
	v_mov_b32_e32 v74, v34
	v_mov_b32_e32 v75, v34
	v_mov_b32_e32 v76, v34
	v_mov_b32_e32 v77, v34
	v_mov_b32_e32 v78, v34
	v_mov_b32_e32 v79, v34
	v_mov_b32_e32 v80, v34
	v_mov_b32_e32 v81, v34
	v_mov_b32_e32 v90, v34
	v_mov_b32_e32 v91, v34
	v_mov_b32_e32 v92, v34
	v_mov_b32_e32 v93, v34
	v_mov_b32_e32 v94, v34
	v_mov_b32_e32 v95, v34
	v_mov_b32_e32 v96, v34
	v_mov_b32_e32 v97, v34
	v_mov_b32_e32 v98, v34
	v_mov_b32_e32 v99, v34
	v_mov_b32_e32 v100, v34
	v_mov_b32_e32 v101, v34
	v_mov_b32_e32 v102, v34
	v_mov_b32_e32 v103, v34
	v_mov_b32_e32 v104, v34
	v_mov_b32_e32 v105, v34
	v_mov_b32_e32 v114, v34
	v_mov_b32_e32 v115, v34
	v_mov_b32_e32 v116, v34
	v_mov_b32_e32 v117, v34
	v_mov_b32_e32 v118, v34
	v_mov_b32_e32 v119, v34
	v_mov_b32_e32 v120, v34
	v_mov_b32_e32 v121, v34
	v_mov_b32_e32 v130, v34
	v_mov_b32_e32 v131, v34
	v_mov_b32_e32 v132, v34
	v_mov_b32_e32 v133, v34
	v_mov_b32_e32 v134, v34
	v_mov_b32_e32 v135, v34
	v_mov_b32_e32 v136, v34
	v_mov_b32_e32 v137, v34
	v_mov_b32_e32 v146, v34
	v_mov_b32_e32 v147, v34
	v_mov_b32_e32 v148, v34
	v_mov_b32_e32 v149, v34
	v_mov_b32_e32 v150, v34
	v_mov_b32_e32 v151, v34
	v_mov_b32_e32 v152, v34
	v_mov_b32_e32 v153, v34
	v_mov_b32_e32 v106, v34
	v_mov_b32_e32 v107, v34
	v_mov_b32_e32 v108, v34
	v_mov_b32_e32 v109, v34
	v_mov_b32_e32 v110, v34
	v_mov_b32_e32 v111, v34
	v_mov_b32_e32 v112, v34
	v_mov_b32_e32 v113, v34
	v_mov_b32_e32 v122, v34
	v_mov_b32_e32 v123, v34
	v_mov_b32_e32 v124, v34
	v_mov_b32_e32 v125, v34
	v_mov_b32_e32 v126, v34
	v_mov_b32_e32 v127, v34
	v_mov_b32_e32 v128, v34
	v_mov_b32_e32 v129, v34
	v_mov_b32_e32 v138, v34
	v_mov_b32_e32 v139, v34
	v_mov_b32_e32 v140, v34
	v_mov_b32_e32 v141, v34
	v_mov_b32_e32 v142, v34
	v_mov_b32_e32 v143, v34
	v_mov_b32_e32 v144, v34
	v_mov_b32_e32 v145, v34
	v_mov_b32_e32 v154, v34
	v_mov_b32_e32 v155, v34
	v_mov_b32_e32 v156, v34
	v_mov_b32_e32 v157, v34
	v_mov_b32_e32 v158, v34
	v_mov_b32_e32 v159, v34
	v_mov_b32_e32 v160, v34
	v_mov_b32_e32 v161, v34
	s_mov_b64 vcc, s[26:27]
	s_cbranch_vccnz .Lsp_1043
	s_setprio 1
.Lsp_1043:
.LBB0_1043:
	ds_read_b128 v[26:29], v209
	ds_read_b128 v[30:33], v209 offset:1024
	ds_read_b128 v[18:21], v209 offset:2048
	ds_read_b128 v[22:25], v209 offset:3072
	ds_read_b128 v[10:13], v210
	ds_read_b128 v[14:17], v210 offset:1024
	ds_read_b128 v[2:5], v210 offset:2048
	ds_read_b128 v[6:9], v210 offset:3072
	s_add_u32 s44, s40, 0xfffc0080
	s_addc_u32 s45, s41, -1
	s_cmp_eq_u32 s81, 12
	s_cselect_b32 s49, s1, s45
	s_cselect_b32 s48, s35, s44
	s_cselect_b32 s45, s31, s61
	s_cselect_b32 s44, s43, s60
	s_add_i32 m0, s65, 0xc000
	ds_read_b128 v[182:185], v211
	ds_read_b128 v[186:189], v211 offset:1024
	ds_read_b128 v[190:193], v211 offset:2048
	ds_read_b128 v[194:197], v211 offset:3072
	ds_read_b128 v[218:221], v211 offset:4096
	ds_read_b128 v[222:225], v211 offset:5120
	ds_read_b128 v[226:229], v211 offset:6144
	ds_read_b128 v[230:233], v211 offset:7168
	global_load_lds_dwordx4 v174, s[40:41]
	s_add_i32 m0, s65, 0xe000
	s_nop 0
	global_load_lds_dwordx4 v176, s[40:41]
	s_waitcnt vmcnt(8)
	s_waitcnt lgkmcnt(0)
	s_barrier
	v_mfma_scale_f32_16x16x128_f8f6f4 v[158:161], v[26:33], v[182:189], v[158:161], v212, v213 op_sel_hi:[0,0,0]
	v_mfma_scale_f32_16x16x128_f8f6f4 v[154:157], v[18:25], v[182:189], v[154:157], v212, v213 op_sel_hi:[0,0,0]
	v_mfma_scale_f32_16x16x128_f8f6f4 v[142:145], v[26:33], v[190:197], v[142:145], v212, v213 op_sel_hi:[0,0,0]
	v_mfma_scale_f32_16x16x128_f8f6f4 v[138:141], v[18:25], v[190:197], v[138:141], v212, v213 op_sel_hi:[0,0,0]
	v_mfma_scale_f32_16x16x128_f8f6f4 v[126:129], v[26:33], v[218:225], v[126:129], v212, v213 op_sel_hi:[0,0,0]
	v_mfma_scale_f32_16x16x128_f8f6f4 v[122:125], v[18:25], v[218:225], v[122:125], v212, v213 op_sel_hi:[0,0,0]
	v_mfma_scale_f32_16x16x128_f8f6f4 v[110:113], v[26:33], v[226:233], v[110:113], v212, v213 op_sel_hi:[0,0,0]
	v_mfma_scale_f32_16x16x128_f8f6f4 v[106:109], v[18:25], v[226:233], v[106:109], v212, v213 op_sel_hi:[0,0,0]
	v_mfma_scale_f32_16x16x128_f8f6f4 v[150:153], v[10:17], v[182:189], v[150:153], v212, v213 op_sel_hi:[0,0,0]
	v_mfma_scale_f32_16x16x128_f8f6f4 v[146:149], v[2:9], v[182:189], v[146:149], v212, v213 op_sel_hi:[0,0,0]
	v_mfma_scale_f32_16x16x128_f8f6f4 v[134:137], v[10:17], v[190:197], v[134:137], v212, v213 op_sel_hi:[0,0,0]
	v_mfma_scale_f32_16x16x128_f8f6f4 v[130:133], v[2:9], v[190:197], v[130:133], v212, v213 op_sel_hi:[0,0,0]
	v_mfma_scale_f32_16x16x128_f8f6f4 v[118:121], v[10:17], v[218:225], v[118:121], v212, v213 op_sel_hi:[0,0,0]
	v_mfma_scale_f32_16x16x128_f8f6f4 v[114:117], v[2:9], v[218:225], v[114:117], v212, v213 op_sel_hi:[0,0,0]
	v_mfma_scale_f32_16x16x128_f8f6f4 v[102:105], v[10:17], v[226:233], v[102:105], v212, v213 op_sel_hi:[0,0,0]
	v_mfma_scale_f32_16x16x128_f8f6f4 v[98:101], v[2:9], v[226:233], v[98:101], v212, v213 op_sel_hi:[0,0,0]
	s_barrier
	s_add_i32 s82, s77, s64
	v_lshl_add_u64 v[182:183], s[44:45], 0, v[164:165]
	s_mov_b32 m0, s82
	ds_read_b128 v[190:193], v211 offset:16384
	ds_read_b128 v[194:197], v211 offset:17408
	ds_read_b128 v[218:221], v211 offset:18432
	ds_read_b128 v[222:225], v211 offset:19456
	ds_read_b128 v[226:229], v211 offset:20480
	ds_read_b128 v[230:233], v211 offset:21504
	ds_read_b128 v[234:237], v211 offset:22528
	ds_read_b128 v[238:241], v211 offset:23552
	global_load_lds_dwordx4 v164, s[44:45]
	s_add_i32 m0, s82, 0x2000
	s_add_u32 s82, s44, 0x40000
	v_lshl_add_u64 v[184:185], s[44:45], 0, v[168:169]
	s_addc_u32 s83, s45, 0
	s_add_i32 s84, s78, s64
	global_load_lds_dwordx4 v168, s[44:45]
	s_mov_b32 m0, s84
	v_lshl_add_u64 v[188:189], s[48:49], 0, v[166:167]
	global_load_lds_dwordx4 v164, s[82:83]
	s_add_i32 m0, s84, 0x2000
	s_nop 0
	global_load_lds_dwordx4 v168, s[82:83]
	v_lshl_add_u64 v[186:187], s[48:49], 0, v[162:163]
	s_mov_b32 m0, s65
	s_nop 0
	global_load_lds_dwordx4 v162, s[48:49]
	s_mov_b32 m0, s66
	s_nop 0
	global_load_lds_dwordx4 v166, s[48:49]
	s_waitcnt vmcnt(8)
	s_waitcnt lgkmcnt(0)
	s_barrier
	v_mfma_scale_f32_16x16x128_f8f6f4 v[94:97], v[26:33], v[190:197], v[94:97], v212, v213 op_sel_hi:[0,0,0]
	v_mfma_scale_f32_16x16x128_f8f6f4 v[90:93], v[18:25], v[190:197], v[90:93], v212, v213 op_sel_hi:[0,0,0]
	v_mfma_scale_f32_16x16x128_f8f6f4 v[78:81], v[26:33], v[218:225], v[78:81], v212, v213 op_sel_hi:[0,0,0]
	v_mfma_scale_f32_16x16x128_f8f6f4 v[74:77], v[18:25], v[218:225], v[74:77], v212, v213 op_sel_hi:[0,0,0]
	v_mfma_scale_f32_16x16x128_f8f6f4 v[62:65], v[26:33], v[226:233], v[62:65], v212, v213 op_sel_hi:[0,0,0]
	v_mfma_scale_f32_16x16x128_f8f6f4 v[58:61], v[18:25], v[226:233], v[58:61], v212, v213 op_sel_hi:[0,0,0]
	v_mfma_scale_f32_16x16x128_f8f6f4 v[46:49], v[26:33], v[234:241], v[46:49], v212, v213 op_sel_hi:[0,0,0]
	v_mfma_scale_f32_16x16x128_f8f6f4 v[42:45], v[18:25], v[234:241], v[42:45], v212, v213 op_sel_hi:[0,0,0]
	v_mfma_scale_f32_16x16x128_f8f6f4 v[86:89], v[10:17], v[190:197], v[86:89], v212, v213 op_sel_hi:[0,0,0]
	v_mfma_scale_f32_16x16x128_f8f6f4 v[82:85], v[2:9], v[190:197], v[82:85], v212, v213 op_sel_hi:[0,0,0]
	v_mfma_scale_f32_16x16x128_f8f6f4 v[70:73], v[10:17], v[218:225], v[70:73], v212, v213 op_sel_hi:[0,0,0]
	v_mfma_scale_f32_16x16x128_f8f6f4 v[66:69], v[2:9], v[218:225], v[66:69], v212, v213 op_sel_hi:[0,0,0]
	v_mfma_scale_f32_16x16x128_f8f6f4 v[54:57], v[10:17], v[226:233], v[54:57], v212, v213 op_sel_hi:[0,0,0]
	v_mfma_scale_f32_16x16x128_f8f6f4 v[50:53], v[2:9], v[226:233], v[50:53], v212, v213 op_sel_hi:[0,0,0]
	v_mfma_scale_f32_16x16x128_f8f6f4 v[38:41], v[10:17], v[234:241], v[38:41], v212, v213 op_sel_hi:[0,0,0]
	v_mfma_scale_f32_16x16x128_f8f6f4 v[34:37], v[2:9], v[234:241], v[34:37], v212, v213 op_sel_hi:[0,0,0]
	s_barrier
	s_add_i32 s82, 0, 0x18000
	s_add_i32 s83, 0, 0x1c000
	v_add_u32_e32 v14, s82, v202
	v_add_u32_e32 v30, s83, v202
	ds_read_b128 v[2:5], v14
	ds_read_b128 v[6:9], v14 offset:1024
	ds_read_b128 v[10:13], v14 offset:2048
	ds_read_b128 v[14:17], v14 offset:3072
	ds_read_b128 v[18:21], v30
	ds_read_b128 v[22:25], v30 offset:1024
	ds_read_b128 v[26:29], v30 offset:2048
	ds_read_b128 v[30:33], v30 offset:3072
	s_add_u32 s48, s48, 0x40000
	s_addc_u32 s49, s49, 0
	s_mov_b32 m0, s67
	ds_read_b128 v[190:193], v211 offset:32768
	ds_read_b128 v[194:197], v211 offset:33792
	ds_read_b128 v[218:221], v211 offset:34816
	ds_read_b128 v[222:225], v211 offset:35840
	ds_read_b128 v[226:229], v211 offset:36864
	ds_read_b128 v[230:233], v211 offset:37888
	ds_read_b128 v[234:237], v211 offset:38912
	ds_read_b128 v[238:241], v211 offset:39936
	global_load_lds_dwordx4 v162, s[48:49]
	s_mov_b32 m0, s68
	s_nop 0
	global_load_lds_dwordx4 v166, s[48:49]
	s_waitcnt vmcnt(8)
	s_waitcnt lgkmcnt(0)
	s_barrier
	v_mfma_scale_f32_16x16x128_f8f6f4 v[158:161], v[2:9], v[190:197], v[158:161], v212, v213 op_sel_hi:[0,0,0]
	v_mfma_scale_f32_16x16x128_f8f6f4 v[154:157], v[10:17], v[190:197], v[154:157], v212, v213 op_sel_hi:[0,0,0]
	v_mfma_scale_f32_16x16x128_f8f6f4 v[142:145], v[2:9], v[218:225], v[142:145], v212, v213 op_sel_hi:[0,0,0]
	v_mfma_scale_f32_16x16x128_f8f6f4 v[138:141], v[10:17], v[218:225], v[138:141], v212, v213 op_sel_hi:[0,0,0]
	v_mfma_scale_f32_16x16x128_f8f6f4 v[126:129], v[2:9], v[226:233], v[126:129], v212, v213 op_sel_hi:[0,0,0]
	v_mfma_scale_f32_16x16x128_f8f6f4 v[122:125], v[10:17], v[226:233], v[122:125], v212, v213 op_sel_hi:[0,0,0]
	v_mfma_scale_f32_16x16x128_f8f6f4 v[110:113], v[2:9], v[234:241], v[110:113], v212, v213 op_sel_hi:[0,0,0]
	v_mfma_scale_f32_16x16x128_f8f6f4 v[106:109], v[10:17], v[234:241], v[106:109], v212, v213 op_sel_hi:[0,0,0]
	v_mfma_scale_f32_16x16x128_f8f6f4 v[150:153], v[18:25], v[190:197], v[150:153], v212, v213 op_sel_hi:[0,0,0]
	v_mfma_scale_f32_16x16x128_f8f6f4 v[146:149], v[26:33], v[190:197], v[146:149], v212, v213 op_sel_hi:[0,0,0]
	v_mfma_scale_f32_16x16x128_f8f6f4 v[134:137], v[18:25], v[218:225], v[134:137], v212, v213 op_sel_hi:[0,0,0]
	v_mfma_scale_f32_16x16x128_f8f6f4 v[130:133], v[26:33], v[218:225], v[130:133], v212, v213 op_sel_hi:[0,0,0]
	v_mfma_scale_f32_16x16x128_f8f6f4 v[118:121], v[18:25], v[226:233], v[118:121], v212, v213 op_sel_hi:[0,0,0]
	v_mfma_scale_f32_16x16x128_f8f6f4 v[114:117], v[26:33], v[226:233], v[114:117], v212, v213 op_sel_hi:[0,0,0]
	v_mfma_scale_f32_16x16x128_f8f6f4 v[102:105], v[18:25], v[234:241], v[102:105], v212, v213 op_sel_hi:[0,0,0]
	v_mfma_scale_f32_16x16x128_f8f6f4 v[98:101], v[26:33], v[234:241], v[98:101], v212, v213 op_sel_hi:[0,0,0]
	s_barrier
	s_add_i32 s48, s82, s64
	v_lshl_add_u64 v[182:183], v[182:183], 0, s[24:25]
	s_mov_b32 m0, s48
	ds_read_b128 v[190:193], v211 offset:49152
	ds_read_b128 v[194:197], v211 offset:50176
	ds_read_b128 v[218:221], v211 offset:51200
	ds_read_b128 v[222:225], v211 offset:52224
	ds_read_b128 v[226:229], v211 offset:53248
	ds_read_b128 v[230:233], v211 offset:54272
	ds_read_b128 v[234:237], v211 offset:55296
	ds_read_b128 v[238:241], v211 offset:56320
	global_load_lds_dwordx4 v[182:183], off
	s_add_i32 m0, s48, 0x2000
	s_add_u32 s44, s44, 0x40080
	v_lshl_add_u64 v[182:183], v[184:185], 0, s[24:25]
	s_addc_u32 s45, s45, 0
	s_add_i32 s48, s83, s64
	global_load_lds_dwordx4 v[182:183], off
	s_mov_b32 m0, s48
	s_nop 0
	global_load_lds_dwordx4 v164, s[44:45]
	s_add_i32 m0, s48, 0x2000
	s_nop 0
	global_load_lds_dwordx4 v168, s[44:45]
	v_lshl_add_u64 v[182:183], v[186:187], 0, s[24:25]
	s_mov_b32 m0, s72
	s_nop 0
	global_load_lds_dwordx4 v[182:183], off
	v_lshl_add_u64 v[182:183], v[188:189], 0, s[24:25]
	s_mov_b32 m0, s73
	s_nop 0
	global_load_lds_dwordx4 v[182:183], off
	s_waitcnt vmcnt(8)
	s_waitcnt lgkmcnt(0)
	s_barrier
	v_mfma_scale_f32_16x16x128_f8f6f4 v[94:97], v[2:9], v[190:197], v[94:97], v212, v213 op_sel_hi:[0,0,0]
	v_mfma_scale_f32_16x16x128_f8f6f4 v[90:93], v[10:17], v[190:197], v[90:93], v212, v213 op_sel_hi:[0,0,0]
	v_mfma_scale_f32_16x16x128_f8f6f4 v[78:81], v[2:9], v[218:225], v[78:81], v212, v213 op_sel_hi:[0,0,0]
	v_mfma_scale_f32_16x16x128_f8f6f4 v[74:77], v[10:17], v[218:225], v[74:77], v212, v213 op_sel_hi:[0,0,0]
	v_mfma_scale_f32_16x16x128_f8f6f4 v[62:65], v[2:9], v[226:233], v[62:65], v212, v213 op_sel_hi:[0,0,0]
	v_mfma_scale_f32_16x16x128_f8f6f4 v[58:61], v[10:17], v[226:233], v[58:61], v212, v213 op_sel_hi:[0,0,0]
	v_mfma_scale_f32_16x16x128_f8f6f4 v[46:49], v[2:9], v[234:241], v[46:49], v212, v213 op_sel_hi:[0,0,0]
	v_mfma_scale_f32_16x16x128_f8f6f4 v[42:45], v[10:17], v[234:241], v[42:45], v212, v213 op_sel_hi:[0,0,0]
	v_mfma_scale_f32_16x16x128_f8f6f4 v[86:89], v[18:25], v[190:197], v[86:89], v212, v213 op_sel_hi:[0,0,0]
	v_mfma_scale_f32_16x16x128_f8f6f4 v[82:85], v[26:33], v[190:197], v[82:85], v212, v213 op_sel_hi:[0,0,0]
	v_mfma_scale_f32_16x16x128_f8f6f4 v[70:73], v[18:25], v[218:225], v[70:73], v212, v213 op_sel_hi:[0,0,0]
	v_mfma_scale_f32_16x16x128_f8f6f4 v[66:69], v[26:33], v[218:225], v[66:69], v212, v213 op_sel_hi:[0,0,0]
	v_mfma_scale_f32_16x16x128_f8f6f4 v[54:57], v[18:25], v[226:233], v[54:57], v212, v213 op_sel_hi:[0,0,0]
	v_mfma_scale_f32_16x16x128_f8f6f4 v[50:53], v[26:33], v[226:233], v[50:53], v212, v213 op_sel_hi:[0,0,0]
	v_mfma_scale_f32_16x16x128_f8f6f4 v[38:41], v[18:25], v[234:241], v[38:41], v212, v213 op_sel_hi:[0,0,0]
	v_mfma_scale_f32_16x16x128_f8f6f4 v[34:37], v[26:33], v[234:241], v[34:37], v212, v213 op_sel_hi:[0,0,0]
	s_barrier
	s_add_i32 s81, s81, 2
	s_add_u32 s40, s40, 0x100
	s_addc_u32 s41, s41, 0
	s_add_u32 s60, s60, 0x100
	s_addc_u32 s61, s61, 0
	s_cmp_gt_u32 s81, 13
	s_cbranch_scc0 .LBB0_1043
	s_setprio 0
	s_and_b64 vcc, exec, s[26:27]
	s_cbranch_vccz .LBB0_1046
	s_barrier

.LBB0_1256:
	s_ashr_i32 s11, s10, 31
	s_lshl_b64 s[14:15], s[10:11], 19
	s_add_u32 s14, s29, s14
	s_addc_u32 s15, s30, s15
	s_and_b64 s[16:17], s[24:25], exec
	s_cselect_b32 s11, s15, s21
	s_cselect_b32 s49, s14, s20
	s_ashr_i32 s13, s12, 31
	s_lshl_b64 s[16:17], s[12:13], 19
	s_add_u32 s16, s31, s16
	s_addc_u32 s17, s33, s17
	s_and_b64 s[24:25], s[24:25], exec
	s_cselect_b32 s13, s17, s23
	s_cselect_b32 s60, s16, s22
	s_add_u32 s20, s20, 0x40080
	s_addc_u32 s21, s21, 0
	s_add_u32 s61, s22, 0x100
	v_mov_b32_e32 v30, 0
	s_addc_u32 s62, s23, 0
	s_mov_b32 s63, -2
	v_mov_b32_e32 v31, v30
	v_mov_b32_e32 v32, v30
	v_mov_b32_e32 v33, v30
	v_mov_b32_e32 v34, v30
	v_mov_b32_e32 v35, v30
	v_mov_b32_e32 v36, v30
	v_mov_b32_e32 v37, v30
	v_mov_b32_e32 v46, v30
	v_mov_b32_e32 v47, v30
	v_mov_b32_e32 v48, v30
	v_mov_b32_e32 v49, v30
	v_mov_b32_e32 v50, v30
	v_mov_b32_e32 v51, v30
	v_mov_b32_e32 v52, v30
	v_mov_b32_e32 v53, v30
	v_mov_b32_e32 v62, v30
	v_mov_b32_e32 v63, v30
	v_mov_b32_e32 v64, v30
	v_mov_b32_e32 v65, v30
	v_mov_b32_e32 v66, v30
	v_mov_b32_e32 v67, v30
	v_mov_b32_e32 v68, v30
	v_mov_b32_e32 v69, v30
	v_mov_b32_e32 v78, v30
	v_mov_b32_e32 v79, v30
	v_mov_b32_e32 v80, v30
	v_mov_b32_e32 v81, v30
	v_mov_b32_e32 v82, v30
	v_mov_b32_e32 v83, v30
	v_mov_b32_e32 v84, v30
	v_mov_b32_e32 v85, v30
	v_mov_b32_e32 v26, v30
	v_mov_b32_e32 v27, v30
	v_mov_b32_e32 v28, v30
	v_mov_b32_e32 v29, v30
	v_mov_b32_e32 v38, v30
	v_mov_b32_e32 v39, v30
	v_mov_b32_e32 v40, v30
	v_mov_b32_e32 v41, v30
	v_mov_b32_e32 v42, v30
	v_mov_b32_e32 v43, v30
	v_mov_b32_e32 v44, v30
	v_mov_b32_e32 v45, v30
	v_mov_b32_e32 v54, v30
	v_mov_b32_e32 v55, v30
	v_mov_b32_e32 v56, v30
	v_mov_b32_e32 v57, v30
	v_mov_b32_e32 v58, v30
	v_mov_b32_e32 v59, v30
	v_mov_b32_e32 v60, v30
	v_mov_b32_e32 v61, v30
	v_mov_b32_e32 v70, v30
	v_mov_b32_e32 v71, v30
	v_mov_b32_e32 v72, v30
	v_mov_b32_e32 v73, v30
	v_mov_b32_e32 v74, v30
	v_mov_b32_e32 v75, v30
	v_mov_b32_e32 v76, v30
	v_mov_b32_e32 v77, v30
	v_mov_b32_e32 v86, v30
	v_mov_b32_e32 v87, v30
	v_mov_b32_e32 v88, v30
	v_mov_b32_e32 v89, v30
	v_mov_b32_e32 v94, v30
	v_mov_b32_e32 v95, v30
	v_mov_b32_e32 v96, v30
	v_mov_b32_e32 v97, v30
	v_mov_b32_e32 v98, v30
	v_mov_b32_e32 v99, v30
	v_mov_b32_e32 v100, v30
	v_mov_b32_e32 v101, v30
	v_mov_b32_e32 v110, v30
	v_mov_b32_e32 v111, v30
	v_mov_b32_e32 v112, v30
	v_mov_b32_e32 v113, v30
	v_mov_b32_e32 v114, v30
	v_mov_b32_e32 v115, v30
	v_mov_b32_e32 v116, v30
	v_mov_b32_e32 v117, v30
	v_mov_b32_e32 v126, v30
	v_mov_b32_e32 v127, v30
	v_mov_b32_e32 v128, v30
	v_mov_b32_e32 v129, v30
	v_mov_b32_e32 v130, v30
	v_mov_b32_e32 v131, v30
	v_mov_b32_e32 v132, v30
	v_mov_b32_e32 v133, v30
	v_mov_b32_e32 v142, v30
	v_mov_b32_e32 v143, v30
	v_mov_b32_e32 v144, v30
	v_mov_b32_e32 v145, v30
	v_mov_b32_e32 v146, v30
	v_mov_b32_e32 v147, v30
	v_mov_b32_e32 v148, v30
	v_mov_b32_e32 v149, v30
	v_mov_b32_e32 v90, v30
	v_mov_b32_e32 v91, v30
	v_mov_b32_e32 v92, v30
	v_mov_b32_e32 v93, v30
	v_mov_b32_e32 v102, v30
	v_mov_b32_e32 v103, v30
	v_mov_b32_e32 v104, v30
	v_mov_b32_e32 v105, v30
	v_mov_b32_e32 v106, v30
	v_mov_b32_e32 v107, v30
	v_mov_b32_e32 v108, v30
	v_mov_b32_e32 v109, v30
	v_mov_b32_e32 v118, v30
	v_mov_b32_e32 v119, v30
	v_mov_b32_e32 v120, v30
	v_mov_b32_e32 v121, v30
	v_mov_b32_e32 v122, v30
	v_mov_b32_e32 v123, v30
	v_mov_b32_e32 v124, v30
	v_mov_b32_e32 v125, v30
	v_mov_b32_e32 v134, v30
	v_mov_b32_e32 v135, v30
	v_mov_b32_e32 v136, v30
	v_mov_b32_e32 v137, v30
	v_mov_b32_e32 v138, v30
	v_mov_b32_e32 v139, v30
	v_mov_b32_e32 v140, v30
	v_mov_b32_e32 v141, v30
	v_mov_b32_e32 v150, v30
	v_mov_b32_e32 v151, v30
	v_mov_b32_e32 v152, v30
	v_mov_b32_e32 v153, v30
	s_mov_b64 vcc, s[8:9]
	s_cbranch_vccnz .Lsp_1257
	s_setprio 1
.Lsp_1257:
.LBB0_1257:
	ds_read_b128 v[20:23], v202
	ds_read_b128 v[166:169], v202 offset:1024
	ds_read_b128 v[14:17], v202 offset:2048
	ds_read_b128 v[162:165], v202 offset:3072
	ds_read_b128 v[8:11], v203
	ds_read_b128 v[158:161], v203 offset:1024
	ds_read_b128 v[2:5], v203 offset:2048
	ds_read_b128 v[154:157], v203 offset:3072
	s_add_u32 s22, s20, 0xfffc0080
	s_addc_u32 s23, s21, -1
	s_cmp_eq_u32 s63, 12
	s_cselect_b32 s25, s11, s23
	s_cselect_b32 s24, s49, s22
	s_cselect_b32 s23, s13, s62
	s_cselect_b32 s22, s60, s61
	s_add_i32 m0, s35, 0xc000
	ds_read_b128 v[184:187], v204
	ds_read_b128 v[188:191], v204 offset:1024
	ds_read_b128 v[206:209], v204 offset:2048
	ds_read_b128 v[222:225], v204 offset:3072
	ds_read_b128 v[212:215], v204 offset:4096
	ds_read_b128 v[226:229], v204 offset:5120
	ds_read_b128 v[218:221], v204 offset:6144
	ds_read_b128 v[230:233], v204 offset:7168
	global_load_lds_dwordx4 v180, s[20:21]
	s_add_i32 m0, s35, 0xe000
	s_nop 0
	global_load_lds_dwordx4 v182, s[20:21]
	s_waitcnt vmcnt(8)
	s_waitcnt lgkmcnt(0)
	s_barrier
	v_mov_b32_e32 v24, v166
	v_mov_b32_e32 v25, v167
	s_nop 1
	v_mfma_scale_f32_16x16x128_f8f6f4 v[150:153], v[20:25], v[184:189], v[150:153], v168, v190 op_sel_hi:[0,0,0] cbsz:2 blgp:2
	v_mov_b32_e32 v18, v162
	v_mov_b32_e32 v19, v163
	s_nop 1
	v_mfma_scale_f32_16x16x128_f8f6f4 v[138:141], v[14:19], v[184:189], v[138:141], v164, v190 op_sel_hi:[0,0,0] cbsz:2 blgp:2
	v_mov_b32_e32 v210, v222
	v_mov_b32_e32 v211, v223
	s_nop 1
	v_mfma_scale_f32_16x16x128_f8f6f4 v[134:137], v[20:25], v[206:211], v[134:137], v168, v224 op_sel_hi:[0,0,0] cbsz:2 blgp:2
	v_mfma_scale_f32_16x16x128_f8f6f4 v[122:125], v[14:19], v[206:211], v[122:125], v164, v224 op_sel_hi:[0,0,0] cbsz:2 blgp:2
	v_mov_b32_e32 v216, v226
	v_mov_b32_e32 v217, v227
	s_nop 1
	v_mfma_scale_f32_16x16x128_f8f6f4 v[118:121], v[20:25], v[212:217], v[118:121], v168, v228 op_sel_hi:[0,0,0] cbsz:2 blgp:2
	v_mfma_scale_f32_16x16x128_f8f6f4 v[106:109], v[14:19], v[212:217], v[106:109], v164, v228 op_sel_hi:[0,0,0] cbsz:2 blgp:2
	v_mov_b32_e32 v222, v230
	v_mov_b32_e32 v223, v231
	s_nop 1
	v_mfma_scale_f32_16x16x128_f8f6f4 v[102:105], v[20:25], v[218:223], v[102:105], v168, v232 op_sel_hi:[0,0,0] cbsz:2 blgp:2
	v_mfma_scale_f32_16x16x128_f8f6f4 v[90:93], v[14:19], v[218:223], v[90:93], v164, v232 op_sel_hi:[0,0,0] cbsz:2 blgp:2
	v_mov_b32_e32 v12, v158
	v_mov_b32_e32 v13, v159
	s_nop 1
	v_mfma_scale_f32_16x16x128_f8f6f4 v[146:149], v[8:13], v[184:189], v[146:149], v160, v190 op_sel_hi:[0,0,0] cbsz:2 blgp:2
	v_mov_b32_e32 v6, v154
	v_mov_b32_e32 v7, v155
	s_nop 1
	v_mfma_scale_f32_16x16x128_f8f6f4 v[142:145], v[2:7], v[184:189], v[142:145], v156, v190 op_sel_hi:[0,0,0] cbsz:2 blgp:2
	v_mfma_scale_f32_16x16x128_f8f6f4 v[130:133], v[8:13], v[206:211], v[130:133], v160, v224 op_sel_hi:[0,0,0] cbsz:2 blgp:2
	v_mfma_scale_f32_16x16x128_f8f6f4 v[126:129], v[2:7], v[206:211], v[126:129], v156, v224 op_sel_hi:[0,0,0] cbsz:2 blgp:2
	v_mfma_scale_f32_16x16x128_f8f6f4 v[114:117], v[8:13], v[212:217], v[114:117], v160, v228 op_sel_hi:[0,0,0] cbsz:2 blgp:2
	v_mfma_scale_f32_16x16x128_f8f6f4 v[110:113], v[2:7], v[212:217], v[110:113], v156, v228 op_sel_hi:[0,0,0] cbsz:2 blgp:2
	v_mfma_scale_f32_16x16x128_f8f6f4 v[98:101], v[8:13], v[218:223], v[98:101], v160, v232 op_sel_hi:[0,0,0] cbsz:2 blgp:2
	v_mfma_scale_f32_16x16x128_f8f6f4 v[94:97], v[2:7], v[218:223], v[94:97], v156, v232 op_sel_hi:[0,0,0] cbsz:2 blgp:2
	s_barrier
	s_add_i32 s64, s42, s27
	v_lshl_add_u64 v[184:185], s[22:23], 0, v[172:173]
	s_mov_b32 m0, s64
	ds_read_b128 v[206:209], v204 offset:16384
	ds_read_b128 v[228:231], v204 offset:17408
	ds_read_b128 v[212:215], v204 offset:18432
	ds_read_b128 v[232:235], v204 offset:19456
	ds_read_b128 v[218:221], v204 offset:20480
	ds_read_b128 v[236:239], v204 offset:21504
	ds_read_b128 v[224:227], v204 offset:22528
	ds_read_b128 v[240:243], v204 offset:23552
	global_load_lds_dwordx4 v172, s[22:23]
	s_add_i32 m0, s64, 0x2000
	s_add_u32 s64, s22, 0x40000
	v_lshl_add_u64 v[186:187], s[22:23], 0, v[174:175]
	s_addc_u32 s65, s23, 0
	s_add_i32 s66, s43, s27
	global_load_lds_dwordx4 v174, s[22:23]
	s_mov_b32 m0, s66
	v_lshl_add_u64 v[188:189], s[24:25], 0, v[178:179]
	global_load_lds_dwordx4 v172, s[64:65]
	s_add_i32 m0, s66, 0x2000
	v_lshl_add_u64 v[190:191], s[24:25], 0, v[176:177]
	global_load_lds_dwordx4 v174, s[64:65]
	s_mov_b32 m0, s35
	s_nop 0
	global_load_lds_dwordx4 v178, s[24:25]
	s_mov_b32 m0, s36
	s_nop 0
	global_load_lds_dwordx4 v176, s[24:25]
	s_waitcnt vmcnt(8)
	s_waitcnt lgkmcnt(0)
	s_barrier
	v_mov_b32_e32 v210, v228
	v_mov_b32_e32 v211, v229
	s_nop 1
	v_mfma_scale_f32_16x16x128_f8f6f4 v[86:89], v[20:25], v[206:211], v[86:89], v168, v230 op_sel_hi:[0,0,0] cbsz:2 blgp:2
	v_mfma_scale_f32_16x16x128_f8f6f4 v[74:77], v[14:19], v[206:211], v[74:77], v164, v230 op_sel_hi:[0,0,0] cbsz:2 blgp:2
	v_mov_b32_e32 v216, v232
	v_mov_b32_e32 v217, v233
	s_nop 1
	v_mfma_scale_f32_16x16x128_f8f6f4 v[70:73], v[20:25], v[212:217], v[70:73], v168, v234 op_sel_hi:[0,0,0] cbsz:2 blgp:2
	v_mfma_scale_f32_16x16x128_f8f6f4 v[58:61], v[14:19], v[212:217], v[58:61], v164, v234 op_sel_hi:[0,0,0] cbsz:2 blgp:2
	v_mov_b32_e32 v222, v236
	v_mov_b32_e32 v223, v237
	s_nop 1
	v_mfma_scale_f32_16x16x128_f8f6f4 v[54:57], v[20:25], v[218:223], v[54:57], v168, v238 op_sel_hi:[0,0,0] cbsz:2 blgp:2
	v_mfma_scale_f32_16x16x128_f8f6f4 v[42:45], v[14:19], v[218:223], v[42:45], v164, v238 op_sel_hi:[0,0,0] cbsz:2 blgp:2
	v_mov_b32_e32 v228, v240
	v_mov_b32_e32 v229, v241
	s_nop 1
	v_mfma_scale_f32_16x16x128_f8f6f4 v[38:41], v[20:25], v[224:229], v[38:41], v168, v242 op_sel_hi:[0,0,0] cbsz:2 blgp:2
	v_mfma_scale_f32_16x16x128_f8f6f4 v[26:29], v[14:19], v[224:229], v[26:29], v164, v242 op_sel_hi:[0,0,0] cbsz:2 blgp:2
	v_mfma_scale_f32_16x16x128_f8f6f4 v[82:85], v[8:13], v[206:211], v[82:85], v160, v230 op_sel_hi:[0,0,0] cbsz:2 blgp:2
	v_mfma_scale_f32_16x16x128_f8f6f4 v[78:81], v[2:7], v[206:211], v[78:81], v156, v230 op_sel_hi:[0,0,0] cbsz:2 blgp:2
	v_mfma_scale_f32_16x16x128_f8f6f4 v[66:69], v[8:13], v[212:217], v[66:69], v160, v234 op_sel_hi:[0,0,0] cbsz:2 blgp:2
	v_mfma_scale_f32_16x16x128_f8f6f4 v[62:65], v[2:7], v[212:217], v[62:65], v156, v234 op_sel_hi:[0,0,0] cbsz:2 blgp:2
	v_mfma_scale_f32_16x16x128_f8f6f4 v[50:53], v[8:13], v[218:223], v[50:53], v160, v238 op_sel_hi:[0,0,0] cbsz:2 blgp:2
	v_mfma_scale_f32_16x16x128_f8f6f4 v[46:49], v[2:7], v[218:223], v[46:49], v156, v238 op_sel_hi:[0,0,0] cbsz:2 blgp:2
	v_mfma_scale_f32_16x16x128_f8f6f4 v[34:37], v[8:13], v[224:229], v[34:37], v160, v242 op_sel_hi:[0,0,0] cbsz:2 blgp:2
	v_mfma_scale_f32_16x16x128_f8f6f4 v[30:33], v[2:7], v[224:229], v[30:33], v156, v242 op_sel_hi:[0,0,0] cbsz:2 blgp:2
	s_barrier
	s_add_i32 s64, 0, 0x18000
	s_add_i32 s65, 0, 0x1c000
	v_add_u32_e32 v2, s64, v198
	v_add_u32_e32 v6, s65, v198
	ds_read_b128 v[20:23], v2
	ds_read_b128 v[166:169], v2 offset:1024
	ds_read_b128 v[14:17], v2 offset:2048
	ds_read_b128 v[162:165], v2 offset:3072
	ds_read_b128 v[8:11], v6
	ds_read_b128 v[154:157], v6 offset:1024
	ds_read_b128 v[2:5], v6 offset:2048
	ds_read_b128 v[158:161], v6 offset:3072
	s_add_u32 s24, s24, 0x40000
	s_addc_u32 s25, s25, 0
	s_mov_b32 m0, s37
	ds_read_b128 v[206:209], v204 offset:32768
	ds_read_b128 v[228:231], v204 offset:33792
	ds_read_b128 v[212:215], v204 offset:34816
	ds_read_b128 v[232:235], v204 offset:35840
	ds_read_b128 v[218:221], v204 offset:36864
	ds_read_b128 v[236:239], v204 offset:37888
	ds_read_b128 v[224:227], v204 offset:38912
	ds_read_b128 v[240:243], v204 offset:39936
	global_load_lds_dwordx4 v178, s[24:25]
	s_mov_b32 m0, s38
	s_nop 0
	global_load_lds_dwordx4 v176, s[24:25]
	s_waitcnt vmcnt(8)
	s_waitcnt lgkmcnt(0)
	s_barrier
	v_mov_b32_e32 v24, v166
	v_mov_b32_e32 v25, v167
	v_mov_b32_e32 v210, v228
	v_mov_b32_e32 v211, v229
	s_nop 1
	v_mfma_scale_f32_16x16x128_f8f6f4 v[150:153], v[20:25], v[206:211], v[150:153], v168, v230 op_sel_hi:[0,0,0] cbsz:2 blgp:2
	v_mov_b32_e32 v18, v162
	v_mov_b32_e32 v19, v163
	s_nop 1
	v_mfma_scale_f32_16x16x128_f8f6f4 v[138:141], v[14:19], v[206:211], v[138:141], v164, v230 op_sel_hi:[0,0,0] cbsz:2 blgp:2
	v_mov_b32_e32 v216, v232
	v_mov_b32_e32 v217, v233
	s_nop 1
	v_mfma_scale_f32_16x16x128_f8f6f4 v[134:137], v[20:25], v[212:217], v[134:137], v168, v234 op_sel_hi:[0,0,0] cbsz:2 blgp:2
	v_mfma_scale_f32_16x16x128_f8f6f4 v[122:125], v[14:19], v[212:217], v[122:125], v164, v234 op_sel_hi:[0,0,0] cbsz:2 blgp:2
	v_mov_b32_e32 v222, v236
	v_mov_b32_e32 v223, v237
	s_nop 1
	v_mfma_scale_f32_16x16x128_f8f6f4 v[118:121], v[20:25], v[218:223], v[118:121], v168, v238 op_sel_hi:[0,0,0] cbsz:2 blgp:2
	v_mfma_scale_f32_16x16x128_f8f6f4 v[106:109], v[14:19], v[218:223], v[106:109], v164, v238 op_sel_hi:[0,0,0] cbsz:2 blgp:2
	v_mov_b32_e32 v228, v240
	v_mov_b32_e32 v229, v241
	s_nop 1
	v_mfma_scale_f32_16x16x128_f8f6f4 v[102:105], v[20:25], v[224:229], v[102:105], v168, v242 op_sel_hi:[0,0,0] cbsz:2 blgp:2
	v_mfma_scale_f32_16x16x128_f8f6f4 v[90:93], v[14:19], v[224:229], v[90:93], v164, v242 op_sel_hi:[0,0,0] cbsz:2 blgp:2
	v_mov_b32_e32 v12, v154
	v_mov_b32_e32 v13, v155
	s_nop 1
	v_mfma_scale_f32_16x16x128_f8f6f4 v[146:149], v[8:13], v[206:211], v[146:149], v156, v230 op_sel_hi:[0,0,0] cbsz:2 blgp:2
	v_mov_b32_e32 v6, v158
	v_mov_b32_e32 v7, v159
	s_nop 1
	v_mfma_scale_f32_16x16x128_f8f6f4 v[142:145], v[2:7], v[206:211], v[142:145], v160, v230 op_sel_hi:[0,0,0] cbsz:2 blgp:2
	v_mfma_scale_f32_16x16x128_f8f6f4 v[130:133], v[8:13], v[212:217], v[130:133], v156, v234 op_sel_hi:[0,0,0] cbsz:2 blgp:2
	v_mfma_scale_f32_16x16x128_f8f6f4 v[126:129], v[2:7], v[212:217], v[126:129], v160, v234 op_sel_hi:[0,0,0] cbsz:2 blgp:2
	v_mfma_scale_f32_16x16x128_f8f6f4 v[114:117], v[8:13], v[218:223], v[114:117], v156, v238 op_sel_hi:[0,0,0] cbsz:2 blgp:2
	v_mfma_scale_f32_16x16x128_f8f6f4 v[110:113], v[2:7], v[218:223], v[110:113], v160, v238 op_sel_hi:[0,0,0] cbsz:2 blgp:2
	v_mfma_scale_f32_16x16x128_f8f6f4 v[98:101], v[8:13], v[224:229], v[98:101], v156, v242 op_sel_hi:[0,0,0] cbsz:2 blgp:2
	v_mfma_scale_f32_16x16x128_f8f6f4 v[94:97], v[2:7], v[224:229], v[94:97], v160, v242 op_sel_hi:[0,0,0] cbsz:2 blgp:2
	s_barrier
	s_add_i32 s24, s64, s27
	v_lshl_add_u64 v[154:155], v[184:185], 0, s[6:7]
	s_mov_b32 m0, s24
	ds_read_b128 v[206:209], v204 offset:49152
	ds_read_b128 v[228:231], v204 offset:50176
	ds_read_b128 v[212:215], v204 offset:51200
	ds_read_b128 v[232:235], v204 offset:52224
	ds_read_b128 v[218:221], v204 offset:53248
	ds_read_b128 v[236:239], v204 offset:54272
	ds_read_b128 v[224:227], v204 offset:55296
	ds_read_b128 v[240:243], v204 offset:56320
	global_load_lds_dwordx4 v[154:155], off
	s_add_i32 m0, s24, 0x2000
	s_add_u32 s22, s22, 0x40080
	v_lshl_add_u64 v[154:155], v[186:187], 0, s[6:7]
	s_addc_u32 s23, s23, 0
	s_add_i32 s24, s65, s27
	global_load_lds_dwordx4 v[154:155], off
	s_mov_b32 m0, s24
	s_nop 0
	global_load_lds_dwordx4 v172, s[22:23]
	s_add_i32 m0, s24, 0x2000
	s_nop 0
	global_load_lds_dwordx4 v174, s[22:23]
	v_lshl_add_u64 v[154:155], v[188:189], 0, s[6:7]
	s_mov_b32 m0, s39
	s_nop 0
	global_load_lds_dwordx4 v[154:155], off
	v_lshl_add_u64 v[154:155], v[190:191], 0, s[6:7]
	s_mov_b32 m0, s40
	s_nop 0
	global_load_lds_dwordx4 v[154:155], off
	s_waitcnt vmcnt(8)
	s_waitcnt lgkmcnt(0)
	s_barrier
	v_mov_b32_e32 v210, v228
	v_mov_b32_e32 v211, v229
	s_nop 1
	v_mfma_scale_f32_16x16x128_f8f6f4 v[86:89], v[20:25], v[206:211], v[86:89], v168, v230 op_sel_hi:[0,0,0] cbsz:2 blgp:2
	v_mfma_scale_f32_16x16x128_f8f6f4 v[74:77], v[14:19], v[206:211], v[74:77], v164, v230 op_sel_hi:[0,0,0] cbsz:2 blgp:2
	v_mov_b32_e32 v216, v232
	v_mov_b32_e32 v217, v233
	s_nop 1
	v_mfma_scale_f32_16x16x128_f8f6f4 v[70:73], v[20:25], v[212:217], v[70:73], v168, v234 op_sel_hi:[0,0,0] cbsz:2 blgp:2
	v_mfma_scale_f32_16x16x128_f8f6f4 v[58:61], v[14:19], v[212:217], v[58:61], v164, v234 op_sel_hi:[0,0,0] cbsz:2 blgp:2
	v_mov_b32_e32 v222, v236
	v_mov_b32_e32 v223, v237
	s_nop 1
	v_mfma_scale_f32_16x16x128_f8f6f4 v[54:57], v[20:25], v[218:223], v[54:57], v168, v238 op_sel_hi:[0,0,0] cbsz:2 blgp:2
	v_mfma_scale_f32_16x16x128_f8f6f4 v[42:45], v[14:19], v[218:223], v[42:45], v164, v238 op_sel_hi:[0,0,0] cbsz:2 blgp:2
	v_mov_b32_e32 v228, v240
	v_mov_b32_e32 v229, v241
	s_nop 1
	v_mfma_scale_f32_16x16x128_f8f6f4 v[38:41], v[20:25], v[224:229], v[38:41], v168, v242 op_sel_hi:[0,0,0] cbsz:2 blgp:2
	v_mfma_scale_f32_16x16x128_f8f6f4 v[26:29], v[14:19], v[224:229], v[26:29], v164, v242 op_sel_hi:[0,0,0] cbsz:2 blgp:2
	v_mfma_scale_f32_16x16x128_f8f6f4 v[82:85], v[8:13], v[206:211], v[82:85], v156, v230 op_sel_hi:[0,0,0] cbsz:2 blgp:2
	v_mfma_scale_f32_16x16x128_f8f6f4 v[78:81], v[2:7], v[206:211], v[78:81], v160, v230 op_sel_hi:[0,0,0] cbsz:2 blgp:2
	v_mfma_scale_f32_16x16x128_f8f6f4 v[66:69], v[8:13], v[212:217], v[66:69], v156, v234 op_sel_hi:[0,0,0] cbsz:2 blgp:2
	v_mfma_scale_f32_16x16x128_f8f6f4 v[62:65], v[2:7], v[212:217], v[62:65], v160, v234 op_sel_hi:[0,0,0] cbsz:2 blgp:2
	v_mfma_scale_f32_16x16x128_f8f6f4 v[50:53], v[8:13], v[218:223], v[50:53], v156, v238 op_sel_hi:[0,0,0] cbsz:2 blgp:2
	v_mfma_scale_f32_16x16x128_f8f6f4 v[46:49], v[2:7], v[218:223], v[46:49], v160, v238 op_sel_hi:[0,0,0] cbsz:2 blgp:2
	v_mfma_scale_f32_16x16x128_f8f6f4 v[34:37], v[8:13], v[224:229], v[34:37], v156, v242 op_sel_hi:[0,0,0] cbsz:2 blgp:2
	v_mfma_scale_f32_16x16x128_f8f6f4 v[30:33], v[2:7], v[224:229], v[30:33], v160, v242 op_sel_hi:[0,0,0] cbsz:2 blgp:2
	s_barrier
	s_add_i32 s63, s63, 2
	s_add_u32 s20, s20, 0x100
	s_addc_u32 s21, s21, 0
	s_add_u32 s61, s61, 0x100
	s_addc_u32 s62, s62, 0
	s_cmp_gt_u32 s63, 13
	s_cbranch_scc0 .LBB0_1257
	s_setprio 0
	s_and_b64 vcc, exec, s[8:9]
	s_cbranch_vccz .LBB0_1260
	s_barrier

.LBB0_1278:
	s_ashr_i32 s11, s10, 31
	s_lshl_b64 s[14:15], s[10:11], 19
	s_add_u32 s14, s29, s14
	s_addc_u32 s15, s30, s15
	s_and_b64 s[18:19], s[16:17], exec
	s_cselect_b32 s11, s15, s23
	s_cselect_b32 s49, s14, s22
	s_ashr_i32 s13, s12, 31
	s_lshl_b64 s[18:19], s[12:13], 19
	s_add_u32 s18, s31, s18
	s_addc_u32 s19, s33, s19
	s_and_b64 s[26:27], s[16:17], exec
	s_cselect_b32 s13, s19, s25
	s_cselect_b32 s50, s18, s24
	s_add_u32 s22, s22, 0x40080
	s_addc_u32 s23, s23, 0
	s_add_u32 s51, s24, 0x100
	v_mov_b32_e32 v30, 0
	s_addc_u32 s60, s25, 0
	s_mov_b32 s61, -2
	v_mov_b32_e32 v31, v30
	v_mov_b32_e32 v32, v30
	v_mov_b32_e32 v33, v30
	v_mov_b32_e32 v34, v30
	v_mov_b32_e32 v35, v30
	v_mov_b32_e32 v36, v30
	v_mov_b32_e32 v37, v30
	v_mov_b32_e32 v46, v30
	v_mov_b32_e32 v47, v30
	v_mov_b32_e32 v48, v30
	v_mov_b32_e32 v49, v30
	v_mov_b32_e32 v50, v30
	v_mov_b32_e32 v51, v30
	v_mov_b32_e32 v52, v30
	v_mov_b32_e32 v53, v30
	v_mov_b32_e32 v62, v30
	v_mov_b32_e32 v63, v30
	v_mov_b32_e32 v64, v30
	v_mov_b32_e32 v65, v30
	v_mov_b32_e32 v66, v30
	v_mov_b32_e32 v67, v30
	v_mov_b32_e32 v68, v30
	v_mov_b32_e32 v69, v30
	v_mov_b32_e32 v78, v30
	v_mov_b32_e32 v79, v30
	v_mov_b32_e32 v80, v30
	v_mov_b32_e32 v81, v30
	v_mov_b32_e32 v82, v30
	v_mov_b32_e32 v83, v30
	v_mov_b32_e32 v84, v30
	v_mov_b32_e32 v85, v30
	v_mov_b32_e32 v26, v30
	v_mov_b32_e32 v27, v30
	v_mov_b32_e32 v28, v30
	v_mov_b32_e32 v29, v30
	v_mov_b32_e32 v38, v30
	v_mov_b32_e32 v39, v30
	v_mov_b32_e32 v40, v30
	v_mov_b32_e32 v41, v30
	v_mov_b32_e32 v42, v30
	v_mov_b32_e32 v43, v30
	v_mov_b32_e32 v44, v30
	v_mov_b32_e32 v45, v30
	v_mov_b32_e32 v54, v30
	v_mov_b32_e32 v55, v30
	v_mov_b32_e32 v56, v30
	v_mov_b32_e32 v57, v30
	v_mov_b32_e32 v58, v30
	v_mov_b32_e32 v59, v30
	v_mov_b32_e32 v60, v30
	v_mov_b32_e32 v61, v30
	v_mov_b32_e32 v70, v30
	v_mov_b32_e32 v71, v30
	v_mov_b32_e32 v72, v30
	v_mov_b32_e32 v73, v30
	v_mov_b32_e32 v74, v30
	v_mov_b32_e32 v75, v30
	v_mov_b32_e32 v76, v30
	v_mov_b32_e32 v77, v30
	v_mov_b32_e32 v86, v30
	v_mov_b32_e32 v87, v30
	v_mov_b32_e32 v88, v30
	v_mov_b32_e32 v89, v30
	v_mov_b32_e32 v94, v30
	v_mov_b32_e32 v95, v30
	v_mov_b32_e32 v96, v30
	v_mov_b32_e32 v97, v30
	v_mov_b32_e32 v98, v30
	v_mov_b32_e32 v99, v30
	v_mov_b32_e32 v100, v30
	v_mov_b32_e32 v101, v30
	v_mov_b32_e32 v110, v30
	v_mov_b32_e32 v111, v30
	v_mov_b32_e32 v112, v30
	v_mov_b32_e32 v113, v30
	v_mov_b32_e32 v114, v30
	v_mov_b32_e32 v115, v30
	v_mov_b32_e32 v116, v30
	v_mov_b32_e32 v117, v30
	v_mov_b32_e32 v126, v30
	v_mov_b32_e32 v127, v30
	v_mov_b32_e32 v128, v30
	v_mov_b32_e32 v129, v30
	v_mov_b32_e32 v130, v30
	v_mov_b32_e32 v131, v30
	v_mov_b32_e32 v132, v30
	v_mov_b32_e32 v133, v30
	v_mov_b32_e32 v142, v30
	v_mov_b32_e32 v143, v30
	v_mov_b32_e32 v144, v30
	v_mov_b32_e32 v145, v30
	v_mov_b32_e32 v146, v30
	v_mov_b32_e32 v147, v30
	v_mov_b32_e32 v148, v30
	v_mov_b32_e32 v149, v30
	v_mov_b32_e32 v90, v30
	v_mov_b32_e32 v91, v30
	v_mov_b32_e32 v92, v30
	v_mov_b32_e32 v93, v30
	v_mov_b32_e32 v102, v30
	v_mov_b32_e32 v103, v30
	v_mov_b32_e32 v104, v30
	v_mov_b32_e32 v105, v30
	v_mov_b32_e32 v106, v30
	v_mov_b32_e32 v107, v30
	v_mov_b32_e32 v108, v30
	v_mov_b32_e32 v109, v30
	v_mov_b32_e32 v118, v30
	v_mov_b32_e32 v119, v30
	v_mov_b32_e32 v120, v30
	v_mov_b32_e32 v121, v30
	v_mov_b32_e32 v122, v30
	v_mov_b32_e32 v123, v30
	v_mov_b32_e32 v124, v30
	v_mov_b32_e32 v125, v30
	v_mov_b32_e32 v134, v30
	v_mov_b32_e32 v135, v30
	v_mov_b32_e32 v136, v30
	v_mov_b32_e32 v137, v30
	v_mov_b32_e32 v138, v30
	v_mov_b32_e32 v139, v30
	v_mov_b32_e32 v140, v30
	v_mov_b32_e32 v141, v30
	v_mov_b32_e32 v150, v30
	v_mov_b32_e32 v151, v30
	v_mov_b32_e32 v152, v30
	v_mov_b32_e32 v153, v30
	s_mov_b64 vcc, s[8:9]
	s_cbranch_vccnz .Lsp_1279
	s_setprio 1
.Lsp_1279:
.LBB0_1279:
	ds_read_b128 v[20:23], v195
	ds_read_b128 v[166:169], v195 offset:1024
	ds_read_b128 v[14:17], v195 offset:2048
	ds_read_b128 v[162:165], v195 offset:3072
	ds_read_b128 v[8:11], v196
	ds_read_b128 v[158:161], v196 offset:1024
	ds_read_b128 v[2:5], v196 offset:2048
	ds_read_b128 v[154:157], v196 offset:3072
	s_add_u32 s24, s22, 0xfffc0080
	s_addc_u32 s25, s23, -1
	s_cmp_eq_u32 s61, 12
	s_cselect_b32 s27, s11, s25
	s_cselect_b32 s26, s49, s24
	s_cselect_b32 s25, s13, s60
	s_cselect_b32 s24, s50, s51
	s_mov_b32 m0, s46
	ds_read_b128 v[184:187], v198
	ds_read_b128 v[188:191], v198 offset:1024
	ds_read_b128 v[202:205], v198 offset:2048
	ds_read_b128 v[218:221], v198 offset:3072
	ds_read_b128 v[208:211], v198 offset:4096
	ds_read_b128 v[222:225], v198 offset:5120
	ds_read_b128 v[214:217], v198 offset:6144
	ds_read_b128 v[226:229], v198 offset:7168
	global_load_lds_dwordx4 v180, s[22:23]
	s_add_i32 m0, s21, 0xe000
	s_nop 0
	global_load_lds_dwordx4 v182, s[22:23]
	s_waitcnt vmcnt(8)
	s_waitcnt lgkmcnt(0)
	s_barrier
	v_mov_b32_e32 v24, v166
	v_mov_b32_e32 v25, v167
	s_nop 1
	v_mfma_scale_f32_16x16x128_f8f6f4 v[150:153], v[20:25], v[184:189], v[150:153], v168, v190 op_sel_hi:[0,0,0] cbsz:2 blgp:2
	v_mov_b32_e32 v18, v162
	v_mov_b32_e32 v19, v163
	s_nop 1
	v_mfma_scale_f32_16x16x128_f8f6f4 v[138:141], v[14:19], v[184:189], v[138:141], v164, v190 op_sel_hi:[0,0,0] cbsz:2 blgp:2
	v_mov_b32_e32 v206, v218
	v_mov_b32_e32 v207, v219
	s_nop 1
	v_mfma_scale_f32_16x16x128_f8f6f4 v[134:137], v[20:25], v[202:207], v[134:137], v168, v220 op_sel_hi:[0,0,0] cbsz:2 blgp:2
	v_mfma_scale_f32_16x16x128_f8f6f4 v[122:125], v[14:19], v[202:207], v[122:125], v164, v220 op_sel_hi:[0,0,0] cbsz:2 blgp:2
	v_mov_b32_e32 v212, v222
	v_mov_b32_e32 v213, v223
	s_nop 1
	v_mfma_scale_f32_16x16x128_f8f6f4 v[118:121], v[20:25], v[208:213], v[118:121], v168, v224 op_sel_hi:[0,0,0] cbsz:2 blgp:2
	v_mfma_scale_f32_16x16x128_f8f6f4 v[106:109], v[14:19], v[208:213], v[106:109], v164, v224 op_sel_hi:[0,0,0] cbsz:2 blgp:2
	v_mov_b32_e32 v218, v226
	v_mov_b32_e32 v219, v227
	s_nop 1
	v_mfma_scale_f32_16x16x128_f8f6f4 v[102:105], v[20:25], v[214:219], v[102:105], v168, v228 op_sel_hi:[0,0,0] cbsz:2 blgp:2
	v_mfma_scale_f32_16x16x128_f8f6f4 v[90:93], v[14:19], v[214:219], v[90:93], v164, v228 op_sel_hi:[0,0,0] cbsz:2 blgp:2
	v_mov_b32_e32 v12, v158
	v_mov_b32_e32 v13, v159
	s_nop 1
	v_mfma_scale_f32_16x16x128_f8f6f4 v[146:149], v[8:13], v[184:189], v[146:149], v160, v190 op_sel_hi:[0,0,0] cbsz:2 blgp:2
	v_mov_b32_e32 v6, v154
	v_mov_b32_e32 v7, v155
	s_nop 1
	v_mfma_scale_f32_16x16x128_f8f6f4 v[142:145], v[2:7], v[184:189], v[142:145], v156, v190 op_sel_hi:[0,0,0] cbsz:2 blgp:2
	v_mfma_scale_f32_16x16x128_f8f6f4 v[130:133], v[8:13], v[202:207], v[130:133], v160, v220 op_sel_hi:[0,0,0] cbsz:2 blgp:2
	v_mfma_scale_f32_16x16x128_f8f6f4 v[126:129], v[2:7], v[202:207], v[126:129], v156, v220 op_sel_hi:[0,0,0] cbsz:2 blgp:2
	v_mfma_scale_f32_16x16x128_f8f6f4 v[114:117], v[8:13], v[208:213], v[114:117], v160, v224 op_sel_hi:[0,0,0] cbsz:2 blgp:2
	v_mfma_scale_f32_16x16x128_f8f6f4 v[110:113], v[2:7], v[208:213], v[110:113], v156, v224 op_sel_hi:[0,0,0] cbsz:2 blgp:2
	v_mfma_scale_f32_16x16x128_f8f6f4 v[98:101], v[8:13], v[214:219], v[98:101], v160, v228 op_sel_hi:[0,0,0] cbsz:2 blgp:2
	v_mfma_scale_f32_16x16x128_f8f6f4 v[94:97], v[2:7], v[214:219], v[94:97], v156, v228 op_sel_hi:[0,0,0] cbsz:2 blgp:2
	s_barrier
	s_add_i32 s62, s42, s35
	v_lshl_add_u64 v[184:185], s[24:25], 0, v[176:177]
	s_mov_b32 m0, s62
	ds_read_b128 v[202:205], v198 offset:16384
	ds_read_b128 v[224:227], v198 offset:17408
	ds_read_b128 v[208:211], v198 offset:18432
	ds_read_b128 v[228:231], v198 offset:19456
	ds_read_b128 v[214:217], v198 offset:20480
	ds_read_b128 v[232:235], v198 offset:21504
	ds_read_b128 v[220:223], v198 offset:22528
	ds_read_b128 v[236:239], v198 offset:23552
	global_load_lds_dwordx4 v176, s[24:25]
	s_add_i32 m0, s62, 0x2000
	s_add_u32 s62, s24, 0x40000
	v_lshl_add_u64 v[186:187], s[24:25], 0, v[172:173]
	s_addc_u32 s63, s25, 0
	s_add_i32 s64, s43, s35
	global_load_lds_dwordx4 v172, s[24:25]
	s_mov_b32 m0, s64
	v_lshl_add_u64 v[188:189], s[26:27], 0, v[178:179]
	global_load_lds_dwordx4 v176, s[62:63]
	s_add_i32 m0, s64, 0x2000
	v_lshl_add_u64 v[190:191], s[26:27], 0, v[174:175]
	global_load_lds_dwordx4 v172, s[62:63]
	s_mov_b32 m0, s21
	s_nop 0
	global_load_lds_dwordx4 v178, s[26:27]
	s_mov_b32 m0, s36
	s_nop 0
	global_load_lds_dwordx4 v174, s[26:27]
	s_waitcnt vmcnt(8)
	s_waitcnt lgkmcnt(0)
	s_barrier
	v_mov_b32_e32 v206, v224
	v_mov_b32_e32 v207, v225
	s_nop 1
	v_mfma_scale_f32_16x16x128_f8f6f4 v[86:89], v[20:25], v[202:207], v[86:89], v168, v226 op_sel_hi:[0,0,0] cbsz:2 blgp:2
	v_mfma_scale_f32_16x16x128_f8f6f4 v[74:77], v[14:19], v[202:207], v[74:77], v164, v226 op_sel_hi:[0,0,0] cbsz:2 blgp:2
	v_mov_b32_e32 v212, v228
	v_mov_b32_e32 v213, v229
	s_nop 1
	v_mfma_scale_f32_16x16x128_f8f6f4 v[70:73], v[20:25], v[208:213], v[70:73], v168, v230 op_sel_hi:[0,0,0] cbsz:2 blgp:2
	v_mfma_scale_f32_16x16x128_f8f6f4 v[58:61], v[14:19], v[208:213], v[58:61], v164, v230 op_sel_hi:[0,0,0] cbsz:2 blgp:2
	v_mov_b32_e32 v218, v232
	v_mov_b32_e32 v219, v233
	s_nop 1
	v_mfma_scale_f32_16x16x128_f8f6f4 v[54:57], v[20:25], v[214:219], v[54:57], v168, v234 op_sel_hi:[0,0,0] cbsz:2 blgp:2
	v_mfma_scale_f32_16x16x128_f8f6f4 v[42:45], v[14:19], v[214:219], v[42:45], v164, v234 op_sel_hi:[0,0,0] cbsz:2 blgp:2
	v_mov_b32_e32 v224, v236
	v_mov_b32_e32 v225, v237
	s_nop 1
	v_mfma_scale_f32_16x16x128_f8f6f4 v[38:41], v[20:25], v[220:225], v[38:41], v168, v238 op_sel_hi:[0,0,0] cbsz:2 blgp:2
	v_mfma_scale_f32_16x16x128_f8f6f4 v[26:29], v[14:19], v[220:225], v[26:29], v164, v238 op_sel_hi:[0,0,0] cbsz:2 blgp:2
	v_mfma_scale_f32_16x16x128_f8f6f4 v[82:85], v[8:13], v[202:207], v[82:85], v160, v226 op_sel_hi:[0,0,0] cbsz:2 blgp:2
	v_mfma_scale_f32_16x16x128_f8f6f4 v[78:81], v[2:7], v[202:207], v[78:81], v156, v226 op_sel_hi:[0,0,0] cbsz:2 blgp:2
	v_mfma_scale_f32_16x16x128_f8f6f4 v[66:69], v[8:13], v[208:213], v[66:69], v160, v230 op_sel_hi:[0,0,0] cbsz:2 blgp:2
	v_mfma_scale_f32_16x16x128_f8f6f4 v[62:65], v[2:7], v[208:213], v[62:65], v156, v230 op_sel_hi:[0,0,0] cbsz:2 blgp:2
	v_mfma_scale_f32_16x16x128_f8f6f4 v[50:53], v[8:13], v[214:219], v[50:53], v160, v234 op_sel_hi:[0,0,0] cbsz:2 blgp:2
	v_mfma_scale_f32_16x16x128_f8f6f4 v[46:49], v[2:7], v[214:219], v[46:49], v156, v234 op_sel_hi:[0,0,0] cbsz:2 blgp:2
	v_mfma_scale_f32_16x16x128_f8f6f4 v[34:37], v[8:13], v[220:225], v[34:37], v160, v238 op_sel_hi:[0,0,0] cbsz:2 blgp:2
	v_mfma_scale_f32_16x16x128_f8f6f4 v[30:33], v[2:7], v[220:225], v[30:33], v156, v238 op_sel_hi:[0,0,0] cbsz:2 blgp:2
	s_barrier
	s_add_i32 s62, 0, 0x18000
	s_add_i32 s63, 0, 0x1c000
	v_add_u32_e32 v2, s62, v194
	v_add_u32_e32 v6, s63, v194
	ds_read_b128 v[20:23], v2
	ds_read_b128 v[166:169], v2 offset:1024
	ds_read_b128 v[14:17], v2 offset:2048
	ds_read_b128 v[162:165], v2 offset:3072
	ds_read_b128 v[8:11], v6
	ds_read_b128 v[154:157], v6 offset:1024
	ds_read_b128 v[2:5], v6 offset:2048
	ds_read_b128 v[158:161], v6 offset:3072
	s_add_u32 s26, s26, 0x40000
	s_addc_u32 s27, s27, 0
	s_mov_b32 m0, s37
	ds_read_b128 v[202:205], v198 offset:32768
	ds_read_b128 v[224:227], v198 offset:33792
	ds_read_b128 v[208:211], v198 offset:34816
	ds_read_b128 v[228:231], v198 offset:35840
	ds_read_b128 v[214:217], v198 offset:36864
	ds_read_b128 v[232:235], v198 offset:37888
	ds_read_b128 v[220:223], v198 offset:38912
	ds_read_b128 v[236:239], v198 offset:39936
	global_load_lds_dwordx4 v178, s[26:27]
	s_mov_b32 m0, s38
	s_nop 0
	global_load_lds_dwordx4 v174, s[26:27]
	s_waitcnt vmcnt(8)
	s_waitcnt lgkmcnt(0)
	s_barrier
	v_mov_b32_e32 v24, v166
	v_mov_b32_e32 v25, v167
	v_mov_b32_e32 v206, v224
	v_mov_b32_e32 v207, v225
	s_nop 1
	v_mfma_scale_f32_16x16x128_f8f6f4 v[150:153], v[20:25], v[202:207], v[150:153], v168, v226 op_sel_hi:[0,0,0] cbsz:2 blgp:2
	v_mov_b32_e32 v18, v162
	v_mov_b32_e32 v19, v163
	s_nop 1
	v_mfma_scale_f32_16x16x128_f8f6f4 v[138:141], v[14:19], v[202:207], v[138:141], v164, v226 op_sel_hi:[0,0,0] cbsz:2 blgp:2
	v_mov_b32_e32 v212, v228
	v_mov_b32_e32 v213, v229
	s_nop 1
	v_mfma_scale_f32_16x16x128_f8f6f4 v[134:137], v[20:25], v[208:213], v[134:137], v168, v230 op_sel_hi:[0,0,0] cbsz:2 blgp:2
	v_mfma_scale_f32_16x16x128_f8f6f4 v[122:125], v[14:19], v[208:213], v[122:125], v164, v230 op_sel_hi:[0,0,0] cbsz:2 blgp:2
	v_mov_b32_e32 v218, v232
	v_mov_b32_e32 v219, v233
	s_nop 1
	v_mfma_scale_f32_16x16x128_f8f6f4 v[118:121], v[20:25], v[214:219], v[118:121], v168, v234 op_sel_hi:[0,0,0] cbsz:2 blgp:2
	v_mfma_scale_f32_16x16x128_f8f6f4 v[106:109], v[14:19], v[214:219], v[106:109], v164, v234 op_sel_hi:[0,0,0] cbsz:2 blgp:2
	v_mov_b32_e32 v224, v236
	v_mov_b32_e32 v225, v237
	s_nop 1
	v_mfma_scale_f32_16x16x128_f8f6f4 v[102:105], v[20:25], v[220:225], v[102:105], v168, v238 op_sel_hi:[0,0,0] cbsz:2 blgp:2
	v_mfma_scale_f32_16x16x128_f8f6f4 v[90:93], v[14:19], v[220:225], v[90:93], v164, v238 op_sel_hi:[0,0,0] cbsz:2 blgp:2
	v_mov_b32_e32 v12, v154
	v_mov_b32_e32 v13, v155
	s_nop 1
	v_mfma_scale_f32_16x16x128_f8f6f4 v[146:149], v[8:13], v[202:207], v[146:149], v156, v226 op_sel_hi:[0,0,0] cbsz:2 blgp:2
	v_mov_b32_e32 v6, v158
	v_mov_b32_e32 v7, v159
	s_nop 1
	v_mfma_scale_f32_16x16x128_f8f6f4 v[142:145], v[2:7], v[202:207], v[142:145], v160, v226 op_sel_hi:[0,0,0] cbsz:2 blgp:2
	v_mfma_scale_f32_16x16x128_f8f6f4 v[130:133], v[8:13], v[208:213], v[130:133], v156, v230 op_sel_hi:[0,0,0] cbsz:2 blgp:2
	v_mfma_scale_f32_16x16x128_f8f6f4 v[126:129], v[2:7], v[208:213], v[126:129], v160, v230 op_sel_hi:[0,0,0] cbsz:2 blgp:2
	v_mfma_scale_f32_16x16x128_f8f6f4 v[114:117], v[8:13], v[214:219], v[114:117], v156, v234 op_sel_hi:[0,0,0] cbsz:2 blgp:2
	v_mfma_scale_f32_16x16x128_f8f6f4 v[110:113], v[2:7], v[214:219], v[110:113], v160, v234 op_sel_hi:[0,0,0] cbsz:2 blgp:2
	v_mfma_scale_f32_16x16x128_f8f6f4 v[98:101], v[8:13], v[220:225], v[98:101], v156, v238 op_sel_hi:[0,0,0] cbsz:2 blgp:2
	v_mfma_scale_f32_16x16x128_f8f6f4 v[94:97], v[2:7], v[220:225], v[94:97], v160, v238 op_sel_hi:[0,0,0] cbsz:2 blgp:2
	s_barrier
	s_add_i32 s26, s62, s35
	v_lshl_add_u64 v[154:155], v[184:185], 0, s[6:7]
	s_mov_b32 m0, s26
	ds_read_b128 v[202:205], v198 offset:49152
	ds_read_b128 v[224:227], v198 offset:50176
	ds_read_b128 v[208:211], v198 offset:51200
	ds_read_b128 v[228:231], v198 offset:52224
	ds_read_b128 v[214:217], v198 offset:53248
	ds_read_b128 v[232:235], v198 offset:54272
	ds_read_b128 v[220:223], v198 offset:55296
	ds_read_b128 v[236:239], v198 offset:56320
	global_load_lds_dwordx4 v[154:155], off
	s_add_i32 m0, s26, 0x2000
	s_add_u32 s24, s24, 0x40080
	v_lshl_add_u64 v[154:155], v[186:187], 0, s[6:7]
	s_addc_u32 s25, s25, 0
	s_add_i32 s26, s63, s35
	global_load_lds_dwordx4 v[154:155], off
	s_mov_b32 m0, s26
	s_nop 0
	global_load_lds_dwordx4 v176, s[24:25]
	s_add_i32 m0, s26, 0x2000
	s_nop 0
	global_load_lds_dwordx4 v172, s[24:25]
	v_lshl_add_u64 v[154:155], v[188:189], 0, s[6:7]
	s_mov_b32 m0, s40
	s_nop 0
	global_load_lds_dwordx4 v[154:155], off
	v_lshl_add_u64 v[154:155], v[190:191], 0, s[6:7]
	s_mov_b32 m0, s41
	s_nop 0
	global_load_lds_dwordx4 v[154:155], off
	s_waitcnt vmcnt(8)
	s_waitcnt lgkmcnt(0)
	s_barrier
	v_mov_b32_e32 v206, v224
	v_mov_b32_e32 v207, v225
	s_nop 1
	v_mfma_scale_f32_16x16x128_f8f6f4 v[86:89], v[20:25], v[202:207], v[86:89], v168, v226 op_sel_hi:[0,0,0] cbsz:2 blgp:2
	v_mfma_scale_f32_16x16x128_f8f6f4 v[74:77], v[14:19], v[202:207], v[74:77], v164, v226 op_sel_hi:[0,0,0] cbsz:2 blgp:2
	v_mov_b32_e32 v212, v228
	v_mov_b32_e32 v213, v229
	s_nop 1
	v_mfma_scale_f32_16x16x128_f8f6f4 v[70:73], v[20:25], v[208:213], v[70:73], v168, v230 op_sel_hi:[0,0,0] cbsz:2 blgp:2
	v_mfma_scale_f32_16x16x128_f8f6f4 v[58:61], v[14:19], v[208:213], v[58:61], v164, v230 op_sel_hi:[0,0,0] cbsz:2 blgp:2
	v_mov_b32_e32 v218, v232
	v_mov_b32_e32 v219, v233
	s_nop 1
	v_mfma_scale_f32_16x16x128_f8f6f4 v[54:57], v[20:25], v[214:219], v[54:57], v168, v234 op_sel_hi:[0,0,0] cbsz:2 blgp:2
	v_mfma_scale_f32_16x16x128_f8f6f4 v[42:45], v[14:19], v[214:219], v[42:45], v164, v234 op_sel_hi:[0,0,0] cbsz:2 blgp:2
	v_mov_b32_e32 v224, v236
	v_mov_b32_e32 v225, v237
	s_nop 1
	v_mfma_scale_f32_16x16x128_f8f6f4 v[38:41], v[20:25], v[220:225], v[38:41], v168, v238 op_sel_hi:[0,0,0] cbsz:2 blgp:2
	v_mfma_scale_f32_16x16x128_f8f6f4 v[26:29], v[14:19], v[220:225], v[26:29], v164, v238 op_sel_hi:[0,0,0] cbsz:2 blgp:2
	v_mfma_scale_f32_16x16x128_f8f6f4 v[82:85], v[8:13], v[202:207], v[82:85], v156, v226 op_sel_hi:[0,0,0] cbsz:2 blgp:2
	v_mfma_scale_f32_16x16x128_f8f6f4 v[78:81], v[2:7], v[202:207], v[78:81], v160, v226 op_sel_hi:[0,0,0] cbsz:2 blgp:2
	v_mfma_scale_f32_16x16x128_f8f6f4 v[66:69], v[8:13], v[208:213], v[66:69], v156, v230 op_sel_hi:[0,0,0] cbsz:2 blgp:2
	v_mfma_scale_f32_16x16x128_f8f6f4 v[62:65], v[2:7], v[208:213], v[62:65], v160, v230 op_sel_hi:[0,0,0] cbsz:2 blgp:2
	v_mfma_scale_f32_16x16x128_f8f6f4 v[50:53], v[8:13], v[214:219], v[50:53], v156, v234 op_sel_hi:[0,0,0] cbsz:2 blgp:2
	v_mfma_scale_f32_16x16x128_f8f6f4 v[46:49], v[2:7], v[214:219], v[46:49], v160, v234 op_sel_hi:[0,0,0] cbsz:2 blgp:2
	v_mfma_scale_f32_16x16x128_f8f6f4 v[34:37], v[8:13], v[220:225], v[34:37], v156, v238 op_sel_hi:[0,0,0] cbsz:2 blgp:2
	v_mfma_scale_f32_16x16x128_f8f6f4 v[30:33], v[2:7], v[220:225], v[30:33], v160, v238 op_sel_hi:[0,0,0] cbsz:2 blgp:2
	s_barrier
	s_add_i32 s61, s61, 2
	s_add_u32 s22, s22, 0x100
	s_addc_u32 s23, s23, 0
	s_add_u32 s51, s51, 0x100
	s_addc_u32 s60, s60, 0
	s_cmp_gt_u32 s61, 13
	s_cbranch_scc0 .LBB0_1279
	s_setprio 0
	s_and_b64 vcc, exec, s[8:9]
	s_cbranch_vccz .LBB0_1282
	s_barrier

.LBB0_1390:
	s_add_u32 s24, s24, 0xe0080
	s_addc_u32 s25, s25, 0
	s_add_u32 s65, s26, 0x100
	v_mov_b32_e32 v32, 0
	s_addc_u32 s66, s27, 0
	s_mov_b32 s67, -2
	v_mov_b32_e32 v33, v32
	v_mov_b32_e32 v34, v32
	v_mov_b32_e32 v35, v32
	v_mov_b32_e32 v36, v32
	v_mov_b32_e32 v37, v32
	v_mov_b32_e32 v38, v32
	v_mov_b32_e32 v39, v32
	v_mov_b32_e32 v48, v32
	v_mov_b32_e32 v49, v32
	v_mov_b32_e32 v50, v32
	v_mov_b32_e32 v51, v32
	v_mov_b32_e32 v52, v32
	v_mov_b32_e32 v53, v32
	v_mov_b32_e32 v54, v32
	v_mov_b32_e32 v55, v32
	v_mov_b32_e32 v64, v32
	v_mov_b32_e32 v65, v32
	v_mov_b32_e32 v66, v32
	v_mov_b32_e32 v67, v32
	v_mov_b32_e32 v68, v32
	v_mov_b32_e32 v69, v32
	v_mov_b32_e32 v70, v32
	v_mov_b32_e32 v71, v32
	v_mov_b32_e32 v80, v32
	v_mov_b32_e32 v81, v32
	v_mov_b32_e32 v82, v32
	v_mov_b32_e32 v83, v32
	v_mov_b32_e32 v84, v32
	v_mov_b32_e32 v85, v32
	v_mov_b32_e32 v86, v32
	v_mov_b32_e32 v87, v32
	v_mov_b32_e32 v40, v32
	v_mov_b32_e32 v41, v32
	v_mov_b32_e32 v42, v32
	v_mov_b32_e32 v43, v32
	v_mov_b32_e32 v44, v32
	v_mov_b32_e32 v45, v32
	v_mov_b32_e32 v46, v32
	v_mov_b32_e32 v47, v32
	v_mov_b32_e32 v56, v32
	v_mov_b32_e32 v57, v32
	v_mov_b32_e32 v58, v32
	v_mov_b32_e32 v59, v32
	v_mov_b32_e32 v60, v32
	v_mov_b32_e32 v61, v32
	v_mov_b32_e32 v62, v32
	v_mov_b32_e32 v63, v32
	v_mov_b32_e32 v72, v32
	v_mov_b32_e32 v73, v32
	v_mov_b32_e32 v74, v32
	v_mov_b32_e32 v75, v32
	v_mov_b32_e32 v76, v32
	v_mov_b32_e32 v77, v32
	v_mov_b32_e32 v78, v32
	v_mov_b32_e32 v79, v32
	v_mov_b32_e32 v88, v32
	v_mov_b32_e32 v89, v32
	v_mov_b32_e32 v90, v32
	v_mov_b32_e32 v91, v32
	v_mov_b32_e32 v92, v32
	v_mov_b32_e32 v93, v32
	v_mov_b32_e32 v94, v32
	v_mov_b32_e32 v95, v32
	v_mov_b32_e32 v96, v32
	v_mov_b32_e32 v97, v32
	v_mov_b32_e32 v98, v32
	v_mov_b32_e32 v99, v32
	v_mov_b32_e32 v100, v32
	v_mov_b32_e32 v101, v32
	v_mov_b32_e32 v102, v32
	v_mov_b32_e32 v103, v32
	v_mov_b32_e32 v112, v32
	v_mov_b32_e32 v113, v32
	v_mov_b32_e32 v114, v32
	v_mov_b32_e32 v115, v32
	v_mov_b32_e32 v116, v32
	v_mov_b32_e32 v117, v32
	v_mov_b32_e32 v118, v32
	v_mov_b32_e32 v119, v32
	v_mov_b32_e32 v128, v32
	v_mov_b32_e32 v129, v32
	v_mov_b32_e32 v130, v32
	v_mov_b32_e32 v131, v32
	v_mov_b32_e32 v132, v32
	v_mov_b32_e32 v133, v32
	v_mov_b32_e32 v134, v32
	v_mov_b32_e32 v135, v32
	v_mov_b32_e32 v144, v32
	v_mov_b32_e32 v145, v32
	v_mov_b32_e32 v146, v32
	v_mov_b32_e32 v147, v32
	v_mov_b32_e32 v148, v32
	v_mov_b32_e32 v149, v32
	v_mov_b32_e32 v150, v32
	v_mov_b32_e32 v151, v32
	v_mov_b32_e32 v104, v32
	v_mov_b32_e32 v105, v32
	v_mov_b32_e32 v106, v32
	v_mov_b32_e32 v107, v32
	v_mov_b32_e32 v108, v32
	v_mov_b32_e32 v109, v32
	v_mov_b32_e32 v110, v32
	v_mov_b32_e32 v111, v32
	v_mov_b32_e32 v120, v32
	v_mov_b32_e32 v121, v32
	v_mov_b32_e32 v122, v32
	v_mov_b32_e32 v123, v32
	v_mov_b32_e32 v124, v32
	v_mov_b32_e32 v125, v32
	v_mov_b32_e32 v126, v32
	v_mov_b32_e32 v127, v32
	v_mov_b32_e32 v136, v32
	v_mov_b32_e32 v137, v32
	v_mov_b32_e32 v138, v32
	v_mov_b32_e32 v139, v32
	v_mov_b32_e32 v140, v32
	v_mov_b32_e32 v141, v32
	v_mov_b32_e32 v142, v32
	v_mov_b32_e32 v143, v32
	v_mov_b32_e32 v152, v32
	v_mov_b32_e32 v153, v32
	v_mov_b32_e32 v154, v32
	v_mov_b32_e32 v155, v32
	v_mov_b32_e32 v156, v32
	v_mov_b32_e32 v157, v32
	v_mov_b32_e32 v158, v32
	v_mov_b32_e32 v159, v32
	s_mov_b64 vcc, s[10:11]
	s_cbranch_vccnz .Lsp_1391
	s_setprio 1
.Lsp_1391:
.LBB0_1391:
	ds_read_b128 v[24:27], v186
	ds_read_b128 v[28:31], v186 offset:1024
	ds_read_b128 v[16:19], v186 offset:2048
	ds_read_b128 v[20:23], v186 offset:3072
	ds_read_b128 v[8:11], v187
	ds_read_b128 v[12:15], v187 offset:1024
	ds_read_b128 v[0:3], v187 offset:2048
	ds_read_b128 v[4:7], v187 offset:3072
	s_add_u32 s26, s24, 0xfff20080
	s_addc_u32 s27, s25, -1
	s_cmp_eq_u32 s67, 52
	s_cselect_b32 s29, s23, s27
	s_cselect_b32 s28, s22, s26
	s_cselect_b32 s27, s1, s66
	s_cselect_b32 s26, s0, s65
	s_add_i32 m0, s36, 0xc000
	ds_read_b128 v[174:177], v188
	ds_read_b128 v[178:181], v188 offset:1024
	ds_read_b128 v[192:195], v188 offset:2048
	ds_read_b128 v[196:199], v188 offset:3072
	ds_read_b128 v[202:205], v188 offset:4096
	ds_read_b128 v[206:209], v188 offset:5120
	ds_read_b128 v[210:213], v188 offset:6144
	ds_read_b128 v[214:217], v188 offset:7168
	global_load_lds_dwordx4 v170, s[24:25]
	s_add_i32 m0, s36, 0xe000
	s_nop 0
	global_load_lds_dwordx4 v172, s[24:25]
	s_waitcnt vmcnt(8)
	s_waitcnt lgkmcnt(0)
	s_barrier
	v_mfma_scale_f32_16x16x128_f8f6f4 v[156:159], v[24:31], v[174:181], v[156:159], v189, v190 op_sel_hi:[0,0,0]
	v_mfma_scale_f32_16x16x128_f8f6f4 v[152:155], v[16:23], v[174:181], v[152:155], v189, v190 op_sel_hi:[0,0,0]
	v_mfma_scale_f32_16x16x128_f8f6f4 v[140:143], v[24:31], v[192:199], v[140:143], v189, v190 op_sel_hi:[0,0,0]
	v_mfma_scale_f32_16x16x128_f8f6f4 v[136:139], v[16:23], v[192:199], v[136:139], v189, v190 op_sel_hi:[0,0,0]
	v_mfma_scale_f32_16x16x128_f8f6f4 v[124:127], v[24:31], v[202:209], v[124:127], v189, v190 op_sel_hi:[0,0,0]
	v_mfma_scale_f32_16x16x128_f8f6f4 v[120:123], v[16:23], v[202:209], v[120:123], v189, v190 op_sel_hi:[0,0,0]
	v_mfma_scale_f32_16x16x128_f8f6f4 v[108:111], v[24:31], v[210:217], v[108:111], v189, v190 op_sel_hi:[0,0,0]
	v_mfma_scale_f32_16x16x128_f8f6f4 v[104:107], v[16:23], v[210:217], v[104:107], v189, v190 op_sel_hi:[0,0,0]
	v_mfma_scale_f32_16x16x128_f8f6f4 v[148:151], v[8:15], v[174:181], v[148:151], v189, v190 op_sel_hi:[0,0,0]
	v_mfma_scale_f32_16x16x128_f8f6f4 v[144:147], v[0:7], v[174:181], v[144:147], v189, v190 op_sel_hi:[0,0,0]
	v_mfma_scale_f32_16x16x128_f8f6f4 v[132:135], v[8:15], v[192:199], v[132:135], v189, v190 op_sel_hi:[0,0,0]
	v_mfma_scale_f32_16x16x128_f8f6f4 v[128:131], v[0:7], v[192:199], v[128:131], v189, v190 op_sel_hi:[0,0,0]
	v_mfma_scale_f32_16x16x128_f8f6f4 v[116:119], v[8:15], v[202:209], v[116:119], v189, v190 op_sel_hi:[0,0,0]
	v_mfma_scale_f32_16x16x128_f8f6f4 v[112:115], v[0:7], v[202:209], v[112:115], v189, v190 op_sel_hi:[0,0,0]
	v_mfma_scale_f32_16x16x128_f8f6f4 v[100:103], v[8:15], v[210:217], v[100:103], v189, v190 op_sel_hi:[0,0,0]
	v_mfma_scale_f32_16x16x128_f8f6f4 v[96:99], v[0:7], v[210:217], v[96:99], v189, v190 op_sel_hi:[0,0,0]
	s_barrier
	s_add_i32 s68, s44, s35
	v_lshl_add_u64 v[174:175], s[26:27], 0, v[160:161]
	s_mov_b32 m0, s68
	ds_read_b128 v[192:195], v188 offset:16384
	ds_read_b128 v[196:199], v188 offset:17408
	ds_read_b128 v[202:205], v188 offset:18432
	ds_read_b128 v[206:209], v188 offset:19456
	ds_read_b128 v[210:213], v188 offset:20480
	ds_read_b128 v[214:217], v188 offset:21504
	ds_read_b128 v[218:221], v188 offset:22528
	ds_read_b128 v[222:225], v188 offset:23552
	global_load_lds_dwordx4 v160, s[26:27]
	s_add_i32 m0, s68, 0x2000
	s_add_u32 s68, s26, 0xe0000
	v_lshl_add_u64 v[176:177], s[26:27], 0, v[164:165]
	s_addc_u32 s69, s27, 0
	s_add_i32 s70, s45, s35
	global_load_lds_dwordx4 v164, s[26:27]
	s_mov_b32 m0, s70
	v_lshl_add_u64 v[180:181], s[28:29], 0, v[166:167]
	global_load_lds_dwordx4 v160, s[68:69]
	s_add_i32 m0, s70, 0x2000
	s_nop 0
	global_load_lds_dwordx4 v164, s[68:69]
	v_lshl_add_u64 v[178:179], s[28:29], 0, v[168:169]
	s_mov_b32 m0, s36
	s_nop 0
	global_load_lds_dwordx4 v168, s[28:29]
	s_mov_b32 m0, s37
	s_nop 0
	global_load_lds_dwordx4 v166, s[28:29]
	s_waitcnt vmcnt(8)
	s_waitcnt lgkmcnt(0)
	s_barrier
	v_mfma_scale_f32_16x16x128_f8f6f4 v[92:95], v[24:31], v[192:199], v[92:95], v189, v190 op_sel_hi:[0,0,0]
	v_mfma_scale_f32_16x16x128_f8f6f4 v[88:91], v[16:23], v[192:199], v[88:91], v189, v190 op_sel_hi:[0,0,0]
	v_mfma_scale_f32_16x16x128_f8f6f4 v[76:79], v[24:31], v[202:209], v[76:79], v189, v190 op_sel_hi:[0,0,0]
	v_mfma_scale_f32_16x16x128_f8f6f4 v[72:75], v[16:23], v[202:209], v[72:75], v189, v190 op_sel_hi:[0,0,0]
	v_mfma_scale_f32_16x16x128_f8f6f4 v[60:63], v[24:31], v[210:217], v[60:63], v189, v190 op_sel_hi:[0,0,0]
	v_mfma_scale_f32_16x16x128_f8f6f4 v[56:59], v[16:23], v[210:217], v[56:59], v189, v190 op_sel_hi:[0,0,0]
	v_mfma_scale_f32_16x16x128_f8f6f4 v[44:47], v[24:31], v[218:225], v[44:47], v189, v190 op_sel_hi:[0,0,0]
	v_mfma_scale_f32_16x16x128_f8f6f4 v[40:43], v[16:23], v[218:225], v[40:43], v189, v190 op_sel_hi:[0,0,0]
	v_mfma_scale_f32_16x16x128_f8f6f4 v[84:87], v[8:15], v[192:199], v[84:87], v189, v190 op_sel_hi:[0,0,0]
	v_mfma_scale_f32_16x16x128_f8f6f4 v[80:83], v[0:7], v[192:199], v[80:83], v189, v190 op_sel_hi:[0,0,0]
	v_mfma_scale_f32_16x16x128_f8f6f4 v[68:71], v[8:15], v[202:209], v[68:71], v189, v190 op_sel_hi:[0,0,0]
	v_mfma_scale_f32_16x16x128_f8f6f4 v[64:67], v[0:7], v[202:209], v[64:67], v189, v190 op_sel_hi:[0,0,0]
	v_mfma_scale_f32_16x16x128_f8f6f4 v[52:55], v[8:15], v[210:217], v[52:55], v189, v190 op_sel_hi:[0,0,0]
	v_mfma_scale_f32_16x16x128_f8f6f4 v[48:51], v[0:7], v[210:217], v[48:51], v189, v190 op_sel_hi:[0,0,0]
	v_mfma_scale_f32_16x16x128_f8f6f4 v[36:39], v[8:15], v[218:225], v[36:39], v189, v190 op_sel_hi:[0,0,0]
	v_mfma_scale_f32_16x16x128_f8f6f4 v[32:35], v[0:7], v[218:225], v[32:35], v189, v190 op_sel_hi:[0,0,0]
	s_barrier
	s_add_i32 s68, 0, 0x18000
	s_add_i32 s69, 0, 0x1c000
	v_add_u32_e32 v12, s68, v184
	v_add_u32_e32 v28, s69, v184
	ds_read_b128 v[0:3], v12
	ds_read_b128 v[4:7], v12 offset:1024
	ds_read_b128 v[8:11], v12 offset:2048
	ds_read_b128 v[12:15], v12 offset:3072
	ds_read_b128 v[16:19], v28
	ds_read_b128 v[20:23], v28 offset:1024
	ds_read_b128 v[24:27], v28 offset:2048
	ds_read_b128 v[28:31], v28 offset:3072
	s_add_u32 s28, s28, 0xe0000
	s_addc_u32 s29, s29, 0
	s_mov_b32 m0, s38
	ds_read_b128 v[192:195], v188 offset:32768
	ds_read_b128 v[196:199], v188 offset:33792
	ds_read_b128 v[202:205], v188 offset:34816
	ds_read_b128 v[206:209], v188 offset:35840
	ds_read_b128 v[210:213], v188 offset:36864
	ds_read_b128 v[214:217], v188 offset:37888
	ds_read_b128 v[218:221], v188 offset:38912
	ds_read_b128 v[222:225], v188 offset:39936
	global_load_lds_dwordx4 v168, s[28:29]
	s_mov_b32 m0, s39
	s_nop 0
	global_load_lds_dwordx4 v166, s[28:29]
	s_waitcnt vmcnt(8)
	s_waitcnt lgkmcnt(0)
	s_barrier
	v_mfma_scale_f32_16x16x128_f8f6f4 v[156:159], v[0:7], v[192:199], v[156:159], v189, v190 op_sel_hi:[0,0,0]
	v_mfma_scale_f32_16x16x128_f8f6f4 v[152:155], v[8:15], v[192:199], v[152:155], v189, v190 op_sel_hi:[0,0,0]
	v_mfma_scale_f32_16x16x128_f8f6f4 v[140:143], v[0:7], v[202:209], v[140:143], v189, v190 op_sel_hi:[0,0,0]
	v_mfma_scale_f32_16x16x128_f8f6f4 v[136:139], v[8:15], v[202:209], v[136:139], v189, v190 op_sel_hi:[0,0,0]
	v_mfma_scale_f32_16x16x128_f8f6f4 v[124:127], v[0:7], v[210:217], v[124:127], v189, v190 op_sel_hi:[0,0,0]
	v_mfma_scale_f32_16x16x128_f8f6f4 v[120:123], v[8:15], v[210:217], v[120:123], v189, v190 op_sel_hi:[0,0,0]
	v_mfma_scale_f32_16x16x128_f8f6f4 v[108:111], v[0:7], v[218:225], v[108:111], v189, v190 op_sel_hi:[0,0,0]
	v_mfma_scale_f32_16x16x128_f8f6f4 v[104:107], v[8:15], v[218:225], v[104:107], v189, v190 op_sel_hi:[0,0,0]
	v_mfma_scale_f32_16x16x128_f8f6f4 v[148:151], v[16:23], v[192:199], v[148:151], v189, v190 op_sel_hi:[0,0,0]
	v_mfma_scale_f32_16x16x128_f8f6f4 v[144:147], v[24:31], v[192:199], v[144:147], v189, v190 op_sel_hi:[0,0,0]
	v_mfma_scale_f32_16x16x128_f8f6f4 v[132:135], v[16:23], v[202:209], v[132:135], v189, v190 op_sel_hi:[0,0,0]
	v_mfma_scale_f32_16x16x128_f8f6f4 v[128:131], v[24:31], v[202:209], v[128:131], v189, v190 op_sel_hi:[0,0,0]
	v_mfma_scale_f32_16x16x128_f8f6f4 v[116:119], v[16:23], v[210:217], v[116:119], v189, v190 op_sel_hi:[0,0,0]
	v_mfma_scale_f32_16x16x128_f8f6f4 v[112:115], v[24:31], v[210:217], v[112:115], v189, v190 op_sel_hi:[0,0,0]
	v_mfma_scale_f32_16x16x128_f8f6f4 v[100:103], v[16:23], v[218:225], v[100:103], v189, v190 op_sel_hi:[0,0,0]
	v_mfma_scale_f32_16x16x128_f8f6f4 v[96:99], v[24:31], v[218:225], v[96:99], v189, v190 op_sel_hi:[0,0,0]
	s_barrier
	s_add_i32 s28, s68, s35
	v_lshl_add_u64 v[174:175], v[174:175], 0, s[8:9]
	s_mov_b32 m0, s28
	ds_read_b128 v[192:195], v188 offset:49152
	ds_read_b128 v[196:199], v188 offset:50176
	ds_read_b128 v[202:205], v188 offset:51200
	ds_read_b128 v[206:209], v188 offset:52224
	ds_read_b128 v[210:213], v188 offset:53248
	ds_read_b128 v[214:217], v188 offset:54272
	ds_read_b128 v[218:221], v188 offset:55296
	ds_read_b128 v[222:225], v188 offset:56320
	global_load_lds_dwordx4 v[174:175], off
	s_add_i32 m0, s28, 0x2000
	s_add_u32 s26, s26, 0xe0080
	v_lshl_add_u64 v[174:175], v[176:177], 0, s[8:9]
	s_addc_u32 s27, s27, 0
	s_add_i32 s28, s69, s35
	global_load_lds_dwordx4 v[174:175], off
	s_mov_b32 m0, s28
	s_nop 0
	global_load_lds_dwordx4 v160, s[26:27]
	s_add_i32 m0, s28, 0x2000
	s_nop 0
	global_load_lds_dwordx4 v164, s[26:27]
	v_lshl_add_u64 v[174:175], v[178:179], 0, s[8:9]
	s_mov_b32 m0, s41
	s_nop 0
	global_load_lds_dwordx4 v[174:175], off
	v_lshl_add_u64 v[174:175], v[180:181], 0, s[8:9]
	s_mov_b32 m0, s42
	s_nop 0
	global_load_lds_dwordx4 v[174:175], off
	s_waitcnt vmcnt(8)
	s_waitcnt lgkmcnt(0)
	s_barrier
	v_mfma_scale_f32_16x16x128_f8f6f4 v[92:95], v[0:7], v[192:199], v[92:95], v189, v190 op_sel_hi:[0,0,0]
	v_mfma_scale_f32_16x16x128_f8f6f4 v[88:91], v[8:15], v[192:199], v[88:91], v189, v190 op_sel_hi:[0,0,0]
	v_mfma_scale_f32_16x16x128_f8f6f4 v[76:79], v[0:7], v[202:209], v[76:79], v189, v190 op_sel_hi:[0,0,0]
	v_mfma_scale_f32_16x16x128_f8f6f4 v[72:75], v[8:15], v[202:209], v[72:75], v189, v190 op_sel_hi:[0,0,0]
	v_mfma_scale_f32_16x16x128_f8f6f4 v[60:63], v[0:7], v[210:217], v[60:63], v189, v190 op_sel_hi:[0,0,0]
	v_mfma_scale_f32_16x16x128_f8f6f4 v[56:59], v[8:15], v[210:217], v[56:59], v189, v190 op_sel_hi:[0,0,0]
	v_mfma_scale_f32_16x16x128_f8f6f4 v[44:47], v[0:7], v[218:225], v[44:47], v189, v190 op_sel_hi:[0,0,0]
	v_mfma_scale_f32_16x16x128_f8f6f4 v[40:43], v[8:15], v[218:225], v[40:43], v189, v190 op_sel_hi:[0,0,0]
	v_mfma_scale_f32_16x16x128_f8f6f4 v[84:87], v[16:23], v[192:199], v[84:87], v189, v190 op_sel_hi:[0,0,0]
	v_mfma_scale_f32_16x16x128_f8f6f4 v[80:83], v[24:31], v[192:199], v[80:83], v189, v190 op_sel_hi:[0,0,0]
	v_mfma_scale_f32_16x16x128_f8f6f4 v[68:71], v[16:23], v[202:209], v[68:71], v189, v190 op_sel_hi:[0,0,0]
	v_mfma_scale_f32_16x16x128_f8f6f4 v[64:67], v[24:31], v[202:209], v[64:67], v189, v190 op_sel_hi:[0,0,0]
	v_mfma_scale_f32_16x16x128_f8f6f4 v[52:55], v[16:23], v[210:217], v[52:55], v189, v190 op_sel_hi:[0,0,0]
	v_mfma_scale_f32_16x16x128_f8f6f4 v[48:51], v[24:31], v[210:217], v[48:51], v189, v190 op_sel_hi:[0,0,0]
	v_mfma_scale_f32_16x16x128_f8f6f4 v[36:39], v[16:23], v[218:225], v[36:39], v189, v190 op_sel_hi:[0,0,0]
	v_mfma_scale_f32_16x16x128_f8f6f4 v[32:35], v[24:31], v[218:225], v[32:35], v189, v190 op_sel_hi:[0,0,0]
	s_barrier
	s_add_i32 s67, s67, 2
	s_add_u32 s24, s24, 0x100
	s_addc_u32 s25, s25, 0
	s_add_u32 s65, s65, 0x100
	s_addc_u32 s66, s66, 0
	s_cmp_gt_u32 s67, 53
	s_cbranch_scc0 .LBB0_1391
	s_setprio 0
	s_and_b64 vcc, exec, s[10:11]
	s_cbranch_vccz .LBB0_1394
	s_barrier
